# static s_setprio 1 for waves 4-7 at kernel entry, all per-segment setprio flips in GEMM K-loops deleted
# baseline (speedup 1.0000x reference)
; #define LAS __attribute__((address_space(3)))
; __global__ void __launch_bounds__(NWAVES * 64, 2) fwd(P p) {
;     ...
;     const int tid = threadIdx.x, lane = tid & 63, wave = __builtin_amdgcn_readfirstlane(tid >> 6);
;     const int G = gridDim.x, bx = blockIdx.x; const int vcu = (G % 8 == 0) ? (bx % 8) * (G / 8) + bx / 8 : bx;
;     const int gw = vcu * NWAVES + wave, NGW = G * NWAVES;
;     for (int u = tid; u < (LDS_BYTES - LDSCTL_OFF) / 4; u += NWAVES * 64) ((LAS unsigned*)(lds + LDSCTL_OFF))[u] = 0u;
;     __syncthreads();
.LBB5_2:
	s_cmp_ge_u32 s16, 0x100
	s_cbranch_scc0 .Lprio_done
	s_setprio 1

; #define PG8_STAGE(bufoff, gbase, voff) do { _Pragma("unroll") for (int _i = 0; _i < 2; ++_i) { unsigned _vo = (voff)[_i]; asm volatile("" : "+v"(_vo)); \
;         __builtin_amdgcn_global_load_lds((const unsigned*)((const char*)(gbase) + _vo), (LAS unsigned*)(lds + (bufoff) + ldsw + _i * 8192), 16, 0, 0); } } while (0)
; #define PG8_STAGE_A(bufoff, gbase, h, go) do { if constexpr (Sched::GATHER) { PG8_STAGE(bufoff, gbase, go[h]); } else { PG8_STAGE(bufoff, (gbase) + (h) * hstep, voffA); } } while (0)
; #define PG8_LDA(dst, b, h) do { _Pragma("unroll") for (int m = 0; m < 4; ++m) _Pragma("unroll") for (int k = 0; k < 2; ++k) dst[m][k] = *(const LAS bf16x8*)(lds + PG8_SA(b, h) + aoff + m * 2048 + k * 1024); } while (0)
; #define PG8_LDB(dst, b, h) do { _Pragma("unroll") for (int n = 0; n < 2; ++n) _Pragma("unroll") for (int k = 0; k < 2; ++k) dst[n][k] = *(const LAS bf16x8*)(lds + PG8_SB(b, h) + boff + n * 2048 + k * 1024); } while (0)
; #define PG8_WAIT_V(n) asm volatile("s_waitcnt vmcnt(" #n ")" ::: "memory")
; #define PG8_WAIT_L(n) asm volatile("s_waitcnt lgkmcnt(" #n ")" ::: "memory")
; #define PG8_BAR __builtin_amdgcn_s_barrier()
;     ...
;         for (int t = 0; t < nt; t += 2) {
;             const bool last = (t == nt - 2);
;             if constexpr (Epi::MIDK) { if (t == nt / 2) { int fr_e = fr; asm volatile("" : "+v"(fr_e)); E.midk(acc, cur, wr, fr_e); } }
;             const char* a1 = cA + (size_t)(t + 1) * kstep;
;             const char* a2 = last ? nA : cA + (size_t)(t + 2) * kstep; const char* b2 = last ? nB : cB + (size_t)(t + 2) * kstep;
;             const char* a3 = a2 + kstep; const char* b3 = b2 + kstep;
;             PG8_LDB(B0, 0, 0); PG8_LDB(B1, 0, 1); PG8_SCHED; PG8_LDA(At, 0, 0); PG8_STAGE_A(PG8_SA(1, 1), a1, 1, gc);
;             if constexpr (Sched::GATHER) { if (last) {
; #pragma unroll
;                 for (int h = 0; h < 2; ++h)
; #pragma unroll
;                     for (int i = 0; i < 2; ++i) gc[h][i] = gn[h][i]; } }
;             PG8_WAIT_V(8); PG8_WAIT_L(0); PG8_BAR; PG8_MMA(0, 0, At, B0); PG8_MMA(0, 1, At, B1); PG8_BAR; PG8_SCHED;
;             PG8_LDA(At, 0, 1); PG8_STAGE(PG8_SB(0, 0), b2, voffB); PG8_STAGE(PG8_SB(0, 1), b2 + hstep, voffB); PG8_STAGE_A(PG8_SA(0, 0), a2, 0, gc);
;             PG8_WAIT_V(8); PG8_WAIT_L(0); PG8_BAR; PG8_MMA(1, 0, At, B0); PG8_MMA(1, 1, At, B1); PG8_BAR; PG8_SCHED;
.LBB5_802:
	ds_read_b128 v[130:133], v168
	ds_read_b128 v[134:137], v168 offset:1024
	ds_read_b128 v[142:145], v168 offset:2048
	ds_read_b128 v[146:149], v168 offset:3072
	ds_read_b128 v[150:153], v169
	ds_read_b128 v[154:157], v169 offset:1024
	ds_read_b128 v[158:161], v169 offset:2048
	ds_read_b128 v[174:177], v169 offset:3072
	s_add_u32 s4, s0, 0xfff80080
	s_addc_u32 s5, s1, -1
	s_cmp_eq_u32 s79, 28
	s_cselect_b32 s5, s41, s5
	s_cselect_b32 s4, s40, s4
	s_cselect_b32 s7, s43, s78
	s_cselect_b32 s6, s42, s77
	v_mov_b32_e32 v138, v1
	ds_read_b128 v[178:181], v170
	ds_read_b128 v[182:185], v170 offset:1024
	ds_read_b128 v[186:189], v170 offset:2048
	ds_read_b128 v[190:193], v170 offset:3072
	ds_read_b128 v[194:197], v170 offset:4096
	ds_read_b128 v[200:203], v170 offset:5120
	ds_read_b128 v[204:207], v170 offset:6144
	ds_read_b128 v[208:211], v170 offset:7168
	s_add_i32 m0, s29, 0xc000
	s_nop 0
	global_load_lds_dwordx4 v138, s[0:1]
	v_mov_b32_e32 v138, v163
	s_add_i32 m0, s29, 0xe000
	s_nop 0
	global_load_lds_dwordx4 v138, s[0:1]
	s_waitcnt vmcnt(8)
	s_waitcnt lgkmcnt(0)
	s_barrier
	s_waitcnt lgkmcnt(0)
	v_mfma_f32_16x16x32_bf16 v[126:129], v[130:133], v[178:181], v[126:129]
	v_mfma_f32_16x16x32_bf16 v[122:125], v[142:145], v[178:181], v[122:125]
	v_mfma_f32_16x16x32_bf16 v[110:113], v[130:133], v[186:189], v[110:113]
	v_mfma_f32_16x16x32_bf16 v[106:109], v[142:145], v[186:189], v[106:109]
	v_mfma_f32_16x16x32_bf16 v[94:97], v[130:133], v[194:197], v[94:97]
	v_mfma_f32_16x16x32_bf16 v[90:93], v[142:145], v[194:197], v[90:93]
	v_mfma_f32_16x16x32_bf16 v[78:81], v[130:133], v[204:207], v[78:81]
	v_mfma_f32_16x16x32_bf16 v[74:77], v[142:145], v[204:207], v[74:77]
	v_mfma_f32_16x16x32_bf16 v[126:129], v[134:137], v[182:185], v[126:129]
	v_mfma_f32_16x16x32_bf16 v[122:125], v[146:149], v[182:185], v[122:125]
	v_mfma_f32_16x16x32_bf16 v[110:113], v[134:137], v[190:193], v[110:113]
	v_mfma_f32_16x16x32_bf16 v[106:109], v[146:149], v[190:193], v[106:109]
	v_mfma_f32_16x16x32_bf16 v[94:97], v[134:137], v[200:203], v[94:97]
	v_mfma_f32_16x16x32_bf16 v[90:93], v[146:149], v[200:203], v[90:93]
	v_mfma_f32_16x16x32_bf16 v[78:81], v[134:137], v[208:211], v[78:81]
	v_mfma_f32_16x16x32_bf16 v[74:77], v[146:149], v[208:211], v[74:77]
	v_mfma_f32_16x16x32_bf16 v[118:121], v[150:153], v[178:181], v[118:121]
	v_mfma_f32_16x16x32_bf16 v[114:117], v[158:161], v[178:181], v[114:117]
	v_mfma_f32_16x16x32_bf16 v[102:105], v[150:153], v[186:189], v[102:105]
	v_mfma_f32_16x16x32_bf16 v[98:101], v[158:161], v[186:189], v[98:101]
	v_mfma_f32_16x16x32_bf16 v[86:89], v[150:153], v[194:197], v[86:89]
	v_mfma_f32_16x16x32_bf16 v[82:85], v[158:161], v[194:197], v[82:85]
	v_mfma_f32_16x16x32_bf16 v[70:73], v[150:153], v[204:207], v[70:73]
	v_mfma_f32_16x16x32_bf16 v[66:69], v[158:161], v[204:207], v[66:69]
	v_mfma_f32_16x16x32_bf16 v[118:121], v[154:157], v[182:185], v[118:121]
	v_mfma_f32_16x16x32_bf16 v[114:117], v[174:177], v[182:185], v[114:117]
	v_mfma_f32_16x16x32_bf16 v[102:105], v[154:157], v[190:193], v[102:105]
	v_mfma_f32_16x16x32_bf16 v[98:101], v[174:177], v[190:193], v[98:101]
	v_mfma_f32_16x16x32_bf16 v[86:89], v[154:157], v[200:203], v[86:89]
	v_mfma_f32_16x16x32_bf16 v[82:85], v[174:177], v[200:203], v[82:85]
	v_mfma_f32_16x16x32_bf16 v[70:73], v[154:157], v[208:211], v[70:73]
	v_mfma_f32_16x16x32_bf16 v[66:69], v[174:177], v[208:211], v[66:69]
	s_barrier
	v_mov_b32_e32 v138, v162
	s_add_i32 s80, s68, s17
	ds_read_b128 v[178:181], v170 offset:16384
	ds_read_b128 v[182:185], v170 offset:17408
	ds_read_b128 v[186:189], v170 offset:18432
	ds_read_b128 v[190:193], v170 offset:19456
	ds_read_b128 v[194:197], v170 offset:20480
	ds_read_b128 v[200:203], v170 offset:21504
	ds_read_b128 v[204:207], v170 offset:22528
	ds_read_b128 v[208:211], v170 offset:23552
	s_mov_b32 m0, s80
	s_nop 0
	global_load_lds_dwordx4 v138, s[6:7]
	v_mov_b32_e32 v138, v164
	s_add_i32 m0, s80, 0x2000
	s_add_u32 s80, s6, 0x80000
	global_load_lds_dwordx4 v138, s[6:7]
	s_addc_u32 s81, s7, 0
	v_mov_b32_e32 v138, v162
	s_add_i32 s82, s69, s17
	s_mov_b32 m0, s82
	s_nop 0
	global_load_lds_dwordx4 v138, s[80:81]
	v_mov_b32_e32 v138, v164
	s_add_i32 m0, s82, 0x2000
	s_nop 0
	global_load_lds_dwordx4 v138, s[80:81]
	v_mov_b32_e32 v138, v1
	s_mov_b32 m0, s29
	s_nop 0
	global_load_lds_dwordx4 v138, s[4:5]
	v_mov_b32_e32 v138, v163
	s_mov_b32 m0, s35
	s_nop 0
	global_load_lds_dwordx4 v138, s[4:5]
	s_waitcnt vmcnt(8)
	s_waitcnt lgkmcnt(0)
	s_barrier
	s_waitcnt lgkmcnt(0)
	v_mfma_f32_16x16x32_bf16 v[62:65], v[130:133], v[178:181], v[62:65]
	v_mfma_f32_16x16x32_bf16 v[58:61], v[142:145], v[178:181], v[58:61]
	v_mfma_f32_16x16x32_bf16 v[46:49], v[130:133], v[186:189], v[46:49]
	v_mfma_f32_16x16x32_bf16 v[42:45], v[142:145], v[186:189], v[42:45]
	v_mfma_f32_16x16x32_bf16 v[30:33], v[130:133], v[194:197], v[30:33]
	v_mfma_f32_16x16x32_bf16 v[26:29], v[142:145], v[194:197], v[26:29]
	v_mfma_f32_16x16x32_bf16 v[14:17], v[130:133], v[204:207], v[14:17]
	v_mfma_f32_16x16x32_bf16 v[10:13], v[142:145], v[204:207], v[10:13]
	v_mfma_f32_16x16x32_bf16 v[62:65], v[134:137], v[182:185], v[62:65]
	v_mfma_f32_16x16x32_bf16 v[58:61], v[146:149], v[182:185], v[58:61]
	v_mfma_f32_16x16x32_bf16 v[46:49], v[134:137], v[190:193], v[46:49]
	v_mfma_f32_16x16x32_bf16 v[42:45], v[146:149], v[190:193], v[42:45]
	v_mfma_f32_16x16x32_bf16 v[30:33], v[134:137], v[200:203], v[30:33]
	v_mfma_f32_16x16x32_bf16 v[26:29], v[146:149], v[200:203], v[26:29]
	v_mfma_f32_16x16x32_bf16 v[14:17], v[134:137], v[208:211], v[14:17]
	v_mfma_f32_16x16x32_bf16 v[10:13], v[146:149], v[208:211], v[10:13]
	v_mfma_f32_16x16x32_bf16 v[54:57], v[150:153], v[178:181], v[54:57]
	v_mfma_f32_16x16x32_bf16 v[50:53], v[158:161], v[178:181], v[50:53]
	v_mfma_f32_16x16x32_bf16 v[38:41], v[150:153], v[186:189], v[38:41]
	v_mfma_f32_16x16x32_bf16 v[34:37], v[158:161], v[186:189], v[34:37]
	v_mfma_f32_16x16x32_bf16 v[22:25], v[150:153], v[194:197], v[22:25]
	v_mfma_f32_16x16x32_bf16 v[18:21], v[158:161], v[194:197], v[18:21]
	v_mfma_f32_16x16x32_bf16 v[6:9], v[150:153], v[204:207], v[6:9]
	v_mfma_f32_16x16x32_bf16 v[2:5], v[158:161], v[204:207], v[2:5]
	v_mfma_f32_16x16x32_bf16 v[54:57], v[154:157], v[182:185], v[54:57]
	v_mfma_f32_16x16x32_bf16 v[50:53], v[174:177], v[182:185], v[50:53]
	v_mfma_f32_16x16x32_bf16 v[38:41], v[154:157], v[190:193], v[38:41]
	v_mfma_f32_16x16x32_bf16 v[34:37], v[174:177], v[190:193], v[34:37]
	v_mfma_f32_16x16x32_bf16 v[22:25], v[154:157], v[200:203], v[22:25]
	v_mfma_f32_16x16x32_bf16 v[18:21], v[174:177], v[200:203], v[18:21]
	v_mfma_f32_16x16x32_bf16 v[6:9], v[154:157], v[208:211], v[6:9]
	v_mfma_f32_16x16x32_bf16 v[2:5], v[174:177], v[208:211], v[2:5]
	s_barrier
; #define PG8_STAGE_A(bufoff, gbase, h, go) do { if constexpr (Sched::GATHER) { PG8_STAGE(bufoff, gbase, go[h]); } else { PG8_STAGE(bufoff, (gbase) + (h) * hstep, voffA); } } while (0)
; #define PG8_LDA(dst, b, h) do { _Pragma("unroll") for (int m = 0; m < 4; ++m) _Pragma("unroll") for (int k = 0; k < 2; ++k) dst[m][k] = *(const LAS bf16x8*)(lds + PG8_SA(b, h) + aoff + m * 2048 + k * 1024); } while (0)
; #define PG8_LDB(dst, b, h) do { _Pragma("unroll") for (int n = 0; n < 2; ++n) _Pragma("unroll") for (int k = 0; k < 2; ++k) dst[n][k] = *(const LAS bf16x8*)(lds + PG8_SB(b, h) + boff + n * 2048 + k * 1024); } while (0)
; #define PG8_WAIT_V(n) asm volatile("s_waitcnt vmcnt(" #n ")" ::: "memory")
; #define PG8_WAIT_L(n) asm volatile("s_waitcnt lgkmcnt(" #n ")" ::: "memory")
; #define PG8_BAR __builtin_amdgcn_s_barrier()
; #define PG8_SCHED __builtin_amdgcn_sched_barrier(0)
;     ...
;             PG8_LDB(B0, 1, 0); PG8_LDB(B1, 1, 1); PG8_SCHED; PG8_LDA(At, 1, 0); PG8_STAGE_A(PG8_SA(0, 1), a2, 1, gc);
;             PG8_WAIT_V(8); PG8_WAIT_L(0); PG8_BAR; PG8_MMA(0, 0, At, B0); PG8_MMA(0, 1, At, B1); PG8_BAR; PG8_SCHED;
	s_add_i32 s82, 0, 0x18000
	v_add_u32_e32 v138, s82, v167
	s_add_i32 s83, 0, 0x1c000
	ds_read_b128 v[130:133], v138
	ds_read_b128 v[134:137], v138 offset:1024
	ds_read_b128 v[142:145], v138 offset:2048
	ds_read_b128 v[146:149], v138 offset:3072
	v_add_u32_e32 v138, s83, v167
	ds_read_b128 v[150:153], v138
	ds_read_b128 v[154:157], v138 offset:1024
	ds_read_b128 v[158:161], v138 offset:2048
	ds_read_b128 v[174:177], v138 offset:3072
	s_add_u32 s80, s4, 0x80000
	v_mov_b32_e32 v138, v1
	s_mov_b32 m0, s37
	ds_read_b128 v[178:181], v170 offset:32768
	ds_read_b128 v[182:185], v170 offset:33792
	ds_read_b128 v[186:189], v170 offset:34816
	ds_read_b128 v[190:193], v170 offset:35840
	ds_read_b128 v[194:197], v170 offset:36864
	ds_read_b128 v[200:203], v170 offset:37888
	ds_read_b128 v[204:207], v170 offset:38912
	ds_read_b128 v[208:211], v170 offset:39936
	s_addc_u32 s81, s5, 0
	s_nop 0
	global_load_lds_dwordx4 v138, s[80:81]
	v_mov_b32_e32 v138, v163
	s_mov_b32 m0, s55
	s_nop 0
	global_load_lds_dwordx4 v138, s[80:81]
	s_waitcnt vmcnt(8)
	s_waitcnt lgkmcnt(0)
	s_barrier
	s_waitcnt lgkmcnt(0)
	v_mfma_f32_16x16x32_bf16 v[126:129], v[130:133], v[178:181], v[126:129]
	v_mfma_f32_16x16x32_bf16 v[122:125], v[142:145], v[178:181], v[122:125]
	v_mfma_f32_16x16x32_bf16 v[110:113], v[130:133], v[186:189], v[110:113]
	v_mfma_f32_16x16x32_bf16 v[106:109], v[142:145], v[186:189], v[106:109]
	v_mfma_f32_16x16x32_bf16 v[94:97], v[130:133], v[194:197], v[94:97]
	v_mfma_f32_16x16x32_bf16 v[90:93], v[142:145], v[194:197], v[90:93]
	v_mfma_f32_16x16x32_bf16 v[78:81], v[130:133], v[204:207], v[78:81]
	v_mfma_f32_16x16x32_bf16 v[74:77], v[142:145], v[204:207], v[74:77]
	v_mfma_f32_16x16x32_bf16 v[126:129], v[134:137], v[182:185], v[126:129]
	v_mfma_f32_16x16x32_bf16 v[122:125], v[146:149], v[182:185], v[122:125]
	v_mfma_f32_16x16x32_bf16 v[110:113], v[134:137], v[190:193], v[110:113]
	v_mfma_f32_16x16x32_bf16 v[106:109], v[146:149], v[190:193], v[106:109]
	v_mfma_f32_16x16x32_bf16 v[94:97], v[134:137], v[200:203], v[94:97]
	v_mfma_f32_16x16x32_bf16 v[90:93], v[146:149], v[200:203], v[90:93]
	v_mfma_f32_16x16x32_bf16 v[78:81], v[134:137], v[208:211], v[78:81]
	v_mfma_f32_16x16x32_bf16 v[74:77], v[146:149], v[208:211], v[74:77]
	v_mfma_f32_16x16x32_bf16 v[118:121], v[150:153], v[178:181], v[118:121]
	v_mfma_f32_16x16x32_bf16 v[114:117], v[158:161], v[178:181], v[114:117]
	v_mfma_f32_16x16x32_bf16 v[102:105], v[150:153], v[186:189], v[102:105]
	v_mfma_f32_16x16x32_bf16 v[98:101], v[158:161], v[186:189], v[98:101]
	v_mfma_f32_16x16x32_bf16 v[86:89], v[150:153], v[194:197], v[86:89]
	v_mfma_f32_16x16x32_bf16 v[82:85], v[158:161], v[194:197], v[82:85]
	v_mfma_f32_16x16x32_bf16 v[70:73], v[150:153], v[204:207], v[70:73]
	v_mfma_f32_16x16x32_bf16 v[66:69], v[158:161], v[204:207], v[66:69]
	v_mfma_f32_16x16x32_bf16 v[118:121], v[154:157], v[182:185], v[118:121]
	v_mfma_f32_16x16x32_bf16 v[114:117], v[174:177], v[182:185], v[114:117]
	v_mfma_f32_16x16x32_bf16 v[102:105], v[154:157], v[190:193], v[102:105]
	v_mfma_f32_16x16x32_bf16 v[98:101], v[174:177], v[190:193], v[98:101]
	v_mfma_f32_16x16x32_bf16 v[86:89], v[154:157], v[200:203], v[86:89]
	v_mfma_f32_16x16x32_bf16 v[82:85], v[174:177], v[200:203], v[82:85]
	v_mfma_f32_16x16x32_bf16 v[70:73], v[154:157], v[208:211], v[70:73]
	v_mfma_f32_16x16x32_bf16 v[66:69], v[174:177], v[208:211], v[66:69]
	s_barrier
; #define PG8_STAGE(bufoff, gbase, voff) do { _Pragma("unroll") for (int _i = 0; _i < 2; ++_i) { unsigned _vo = (voff)[_i]; asm volatile("" : "+v"(_vo)); \
;         __builtin_amdgcn_global_load_lds((const unsigned*)((const char*)(gbase) + _vo), (LAS unsigned*)(lds + (bufoff) + ldsw + _i * 8192), 16, 0, 0); } } while (0)
; #define PG8_STAGE_A(bufoff, gbase, h, go) do { if constexpr (Sched::GATHER) { PG8_STAGE(bufoff, gbase, go[h]); } else { PG8_STAGE(bufoff, (gbase) + (h) * hstep, voffA); } } while (0)
; #define PG8_LDA(dst, b, h) do { _Pragma("unroll") for (int m = 0; m < 4; ++m) _Pragma("unroll") for (int k = 0; k < 2; ++k) dst[m][k] = *(const LAS bf16x8*)(lds + PG8_SA(b, h) + aoff + m * 2048 + k * 1024); } while (0)
; #define PG8_WAIT_V(n) asm volatile("s_waitcnt vmcnt(" #n ")" ::: "memory")
; #define PG8_WAIT_L(n) asm volatile("s_waitcnt lgkmcnt(" #n ")" ::: "memory")
; #define PG8_BAR __builtin_amdgcn_s_barrier()
; #define PG8_SCHED __builtin_amdgcn_sched_barrier(0)
;     ...
;             PG8_LDA(At, 1, 1); PG8_STAGE(PG8_SB(1, 0), b3, voffB); PG8_STAGE(PG8_SB(1, 1), b3 + hstep, voffB); PG8_STAGE_A(PG8_SA(1, 0), a3, 0, gc);
;             PG8_WAIT_V(8); PG8_WAIT_L(0); PG8_BAR; PG8_MMA(1, 0, At, B0); PG8_MMA(1, 1, At, B1); PG8_BAR; PG8_SCHED;
	v_mov_b32_e32 v138, v162
	ds_read_b128 v[178:181], v170 offset:49152
	ds_read_b128 v[182:185], v170 offset:50176
	ds_read_b128 v[186:189], v170 offset:51200
	ds_read_b128 v[190:193], v170 offset:52224
	ds_read_b128 v[194:197], v170 offset:53248
	ds_read_b128 v[200:203], v170 offset:54272
	ds_read_b128 v[204:207], v170 offset:55296
	ds_read_b128 v[208:211], v170 offset:56320
	s_add_i32 s80, s82, s17
	v_lshl_add_u64 v[214:215], s[6:7], 0, v[138:139]
	v_lshl_add_u64 v[214:215], v[214:215], 0, s[12:13]
	s_mov_b32 m0, s80
	v_mov_b32_e32 v138, v164
	global_load_lds_dwordx4 v[214:215], off
	s_add_i32 m0, s80, 0x2000
	s_nop 0
	v_lshl_add_u64 v[214:215], s[6:7], 0, v[138:139]
	s_add_u32 s6, s6, 0x80080
	v_lshl_add_u64 v[214:215], v[214:215], 0, s[12:13]
	s_addc_u32 s7, s7, 0
	v_mov_b32_e32 v138, v162
	s_add_i32 s80, s83, s17
	global_load_lds_dwordx4 v[214:215], off
	s_mov_b32 m0, s80
	s_nop 0
	global_load_lds_dwordx4 v138, s[6:7]
	v_mov_b32_e32 v138, v164
	s_add_i32 m0, s80, 0x2000
	s_nop 0
	global_load_lds_dwordx4 v138, s[6:7]
	v_mov_b32_e32 v138, v1
	s_mov_b32 m0, s64
	v_lshl_add_u64 v[214:215], s[4:5], 0, v[138:139]
	v_lshl_add_u64 v[214:215], v[214:215], 0, s[12:13]
	v_mov_b32_e32 v138, v163
	global_load_lds_dwordx4 v[214:215], off
	s_mov_b32 m0, s65
	v_lshl_add_u64 v[214:215], s[4:5], 0, v[138:139]
	v_lshl_add_u64 v[214:215], v[214:215], 0, s[12:13]
	global_load_lds_dwordx4 v[214:215], off
	s_waitcnt vmcnt(8)
	s_waitcnt lgkmcnt(0)
	s_barrier
	s_waitcnt lgkmcnt(0)
	v_mfma_f32_16x16x32_bf16 v[62:65], v[130:133], v[178:181], v[62:65]
	v_mfma_f32_16x16x32_bf16 v[58:61], v[142:145], v[178:181], v[58:61]
	v_mfma_f32_16x16x32_bf16 v[46:49], v[130:133], v[186:189], v[46:49]
	v_mfma_f32_16x16x32_bf16 v[42:45], v[142:145], v[186:189], v[42:45]
	v_mfma_f32_16x16x32_bf16 v[30:33], v[130:133], v[194:197], v[30:33]
	v_mfma_f32_16x16x32_bf16 v[26:29], v[142:145], v[194:197], v[26:29]
	v_mfma_f32_16x16x32_bf16 v[14:17], v[130:133], v[204:207], v[14:17]
	v_mfma_f32_16x16x32_bf16 v[10:13], v[142:145], v[204:207], v[10:13]
	v_mfma_f32_16x16x32_bf16 v[62:65], v[134:137], v[182:185], v[62:65]
	v_mfma_f32_16x16x32_bf16 v[58:61], v[146:149], v[182:185], v[58:61]
	v_mfma_f32_16x16x32_bf16 v[46:49], v[134:137], v[190:193], v[46:49]
	v_mfma_f32_16x16x32_bf16 v[42:45], v[146:149], v[190:193], v[42:45]
	v_mfma_f32_16x16x32_bf16 v[30:33], v[134:137], v[200:203], v[30:33]
	v_mfma_f32_16x16x32_bf16 v[26:29], v[146:149], v[200:203], v[26:29]
	v_mfma_f32_16x16x32_bf16 v[14:17], v[134:137], v[208:211], v[14:17]
	v_mfma_f32_16x16x32_bf16 v[10:13], v[146:149], v[208:211], v[10:13]
	v_mfma_f32_16x16x32_bf16 v[54:57], v[150:153], v[178:181], v[54:57]
	v_mfma_f32_16x16x32_bf16 v[50:53], v[158:161], v[178:181], v[50:53]
	v_mfma_f32_16x16x32_bf16 v[38:41], v[150:153], v[186:189], v[38:41]
	v_mfma_f32_16x16x32_bf16 v[34:37], v[158:161], v[186:189], v[34:37]
	v_mfma_f32_16x16x32_bf16 v[22:25], v[150:153], v[194:197], v[22:25]
	v_mfma_f32_16x16x32_bf16 v[18:21], v[158:161], v[194:197], v[18:21]
	v_mfma_f32_16x16x32_bf16 v[6:9], v[150:153], v[204:207], v[6:9]
	v_mfma_f32_16x16x32_bf16 v[2:5], v[158:161], v[204:207], v[2:5]
	v_mfma_f32_16x16x32_bf16 v[54:57], v[154:157], v[182:185], v[54:57]
	v_mfma_f32_16x16x32_bf16 v[50:53], v[174:177], v[182:185], v[50:53]
	v_mfma_f32_16x16x32_bf16 v[38:41], v[154:157], v[190:193], v[38:41]
	v_mfma_f32_16x16x32_bf16 v[34:37], v[174:177], v[190:193], v[34:37]
	v_mfma_f32_16x16x32_bf16 v[22:25], v[154:157], v[200:203], v[22:25]
	v_mfma_f32_16x16x32_bf16 v[18:21], v[174:177], v[200:203], v[18:21]
	v_mfma_f32_16x16x32_bf16 v[6:9], v[154:157], v[208:211], v[6:9]
	v_mfma_f32_16x16x32_bf16 v[2:5], v[174:177], v[208:211], v[2:5]
	s_barrier
	s_add_i32 s79, s79, 2
	s_add_u32 s0, s0, 0x100
	s_addc_u32 s1, s1, 0
	s_add_u32 s77, s77, 0x100
	s_addc_u32 s78, s78, 0
	s_cmp_gt_u32 s79, 29
	s_cbranch_scc0 .LBB5_802
	s_and_b64 vcc, exec, s[18:19]
	s_cbranch_vccz .LBB5_805
	s_barrier

; #define PG8_STAGE(bufoff, gbase, voff) do { _Pragma("unroll") for (int _i = 0; _i < 2; ++_i) { unsigned _vo = (voff)[_i]; asm volatile("" : "+v"(_vo)); \
;         __builtin_amdgcn_global_load_lds((const unsigned*)((const char*)(gbase) + _vo), (LAS unsigned*)(lds + (bufoff) + ldsw + _i * 8192), 16, 0, 0); } } while (0)
; #define PG8_STAGE_A(bufoff, gbase, h, go) do { if constexpr (Sched::GATHER) { PG8_STAGE(bufoff, gbase, go[h]); } else { PG8_STAGE(bufoff, (gbase) + (h) * hstep, voffA); } } while (0)
; #define PG8_LDA(dst, b, h) do { _Pragma("unroll") for (int m = 0; m < 4; ++m) _Pragma("unroll") for (int k = 0; k < 2; ++k) dst[m][k] = *(const LAS bf16x8*)(lds + PG8_SA(b, h) + aoff + m * 2048 + k * 1024); } while (0)
; #define PG8_LDB(dst, b, h) do { _Pragma("unroll") for (int n = 0; n < 2; ++n) _Pragma("unroll") for (int k = 0; k < 2; ++k) dst[n][k] = *(const LAS bf16x8*)(lds + PG8_SB(b, h) + boff + n * 2048 + k * 1024); } while (0)
; #define PG8_WAIT_V(n) asm volatile("s_waitcnt vmcnt(" #n ")" ::: "memory")
; #define PG8_WAIT_L(n) asm volatile("s_waitcnt lgkmcnt(" #n ")" ::: "memory")
; #define PG8_BAR __builtin_amdgcn_s_barrier()
;     ...
;         for (int t = 0; t < nt; t += 2) {
;             const bool last = (t == nt - 2);
;             if constexpr (Epi::MIDK) { if (t == nt / 2) { int fr_e = fr; asm volatile("" : "+v"(fr_e)); E.midk(acc, cur, wr, fr_e); } }
;             const char* a1 = cA + (size_t)(t + 1) * kstep;
;             const char* a2 = last ? nA : cA + (size_t)(t + 2) * kstep; const char* b2 = last ? nB : cB + (size_t)(t + 2) * kstep;
;             const char* a3 = a2 + kstep; const char* b3 = b2 + kstep;
;             PG8_LDB(B0, 0, 0); PG8_LDB(B1, 0, 1); PG8_SCHED; PG8_LDA(At, 0, 0); PG8_STAGE_A(PG8_SA(1, 1), a1, 1, gc);
;             if constexpr (Sched::GATHER) { if (last) {
; #pragma unroll
;                 for (int h = 0; h < 2; ++h)
; #pragma unroll
;                     for (int i = 0; i < 2; ++i) gc[h][i] = gn[h][i]; } }
;             PG8_WAIT_V(8); PG8_WAIT_L(0); PG8_BAR; PG8_MMA(0, 0, At, B0); PG8_MMA(0, 1, At, B1); PG8_BAR; PG8_SCHED;
;             PG8_LDA(At, 0, 1); PG8_STAGE(PG8_SB(0, 0), b2, voffB); PG8_STAGE(PG8_SB(0, 1), b2 + hstep, voffB); PG8_STAGE_A(PG8_SA(0, 0), a2, 0, gc);
;             PG8_WAIT_V(8); PG8_WAIT_L(0); PG8_BAR; PG8_MMA(1, 0, At, B0); PG8_MMA(1, 1, At, B1); PG8_BAR; PG8_SCHED;
.LBB5_889:
	ds_read_b128 v[136:139], v131
	ds_read_b128 v[140:143], v131 offset:1024
	ds_read_b128 v[158:161], v131 offset:2048
	ds_read_b128 v[162:165], v131 offset:3072
	ds_read_b128 v[166:169], v147
	ds_read_b128 v[170:173], v147 offset:1024
	ds_read_b128 v[174:177], v147 offset:2048
	ds_read_b128 v[178:181], v147 offset:3072
	s_add_u32 s50, s42, 0xfff80080
	s_addc_u32 s51, s43, -1
	s_cmp_eq_u32 s77, 28
	s_cselect_b32 s51, s35, s51
	s_cselect_b32 s50, s34, s50
	s_cselect_b32 s55, s37, s76
	s_cselect_b32 s54, s36, s75
	v_mov_b32_e32 v132, v149
	ds_read_b128 v[182:185], v156
	ds_read_b128 v[186:189], v156 offset:1024
	ds_read_b128 v[190:193], v156 offset:2048
	ds_read_b128 v[194:197], v156 offset:3072
	ds_read_b128 v[200:203], v156 offset:4096
	ds_read_b128 v[204:207], v156 offset:5120
	ds_read_b128 v[208:211], v156 offset:6144
	ds_read_b128 v[214:217], v156 offset:7168
	s_add_i32 m0, s41, 0xc000
	s_nop 0
	global_load_lds_dwordx4 v132, s[42:43]
	v_mov_b32_e32 v132, v151
	s_add_i32 m0, s41, 0xe000
	s_nop 0
	global_load_lds_dwordx4 v132, s[42:43]
	s_waitcnt vmcnt(8)
	s_waitcnt lgkmcnt(0)
	s_barrier
	s_waitcnt lgkmcnt(0)
	v_mfma_f32_16x16x32_bf16 v[126:129], v[136:139], v[182:185], v[126:129]
	v_mfma_f32_16x16x32_bf16 v[122:125], v[158:161], v[182:185], v[122:125]
	v_mfma_f32_16x16x32_bf16 v[110:113], v[136:139], v[190:193], v[110:113]
	v_mfma_f32_16x16x32_bf16 v[106:109], v[158:161], v[190:193], v[106:109]
	v_mfma_f32_16x16x32_bf16 v[94:97], v[136:139], v[200:203], v[94:97]
	v_mfma_f32_16x16x32_bf16 v[90:93], v[158:161], v[200:203], v[90:93]
	v_mfma_f32_16x16x32_bf16 v[78:81], v[136:139], v[208:211], v[78:81]
	v_mfma_f32_16x16x32_bf16 v[74:77], v[158:161], v[208:211], v[74:77]
	v_mfma_f32_16x16x32_bf16 v[126:129], v[140:143], v[186:189], v[126:129]
	v_mfma_f32_16x16x32_bf16 v[122:125], v[162:165], v[186:189], v[122:125]
	v_mfma_f32_16x16x32_bf16 v[110:113], v[140:143], v[194:197], v[110:113]
	v_mfma_f32_16x16x32_bf16 v[106:109], v[162:165], v[194:197], v[106:109]
	v_mfma_f32_16x16x32_bf16 v[94:97], v[140:143], v[204:207], v[94:97]
	v_mfma_f32_16x16x32_bf16 v[90:93], v[162:165], v[204:207], v[90:93]
	v_mfma_f32_16x16x32_bf16 v[78:81], v[140:143], v[214:217], v[78:81]
	v_mfma_f32_16x16x32_bf16 v[74:77], v[162:165], v[214:217], v[74:77]
	v_mfma_f32_16x16x32_bf16 v[118:121], v[166:169], v[182:185], v[118:121]
	v_mfma_f32_16x16x32_bf16 v[114:117], v[174:177], v[182:185], v[114:117]
	v_mfma_f32_16x16x32_bf16 v[102:105], v[166:169], v[190:193], v[102:105]
	v_mfma_f32_16x16x32_bf16 v[98:101], v[174:177], v[190:193], v[98:101]
	v_mfma_f32_16x16x32_bf16 v[86:89], v[166:169], v[200:203], v[86:89]
	v_mfma_f32_16x16x32_bf16 v[82:85], v[174:177], v[200:203], v[82:85]
	v_mfma_f32_16x16x32_bf16 v[70:73], v[166:169], v[208:211], v[70:73]
	v_mfma_f32_16x16x32_bf16 v[66:69], v[174:177], v[208:211], v[66:69]
	v_mfma_f32_16x16x32_bf16 v[118:121], v[170:173], v[186:189], v[118:121]
	v_mfma_f32_16x16x32_bf16 v[114:117], v[178:181], v[186:189], v[114:117]
	v_mfma_f32_16x16x32_bf16 v[102:105], v[170:173], v[194:197], v[102:105]
	v_mfma_f32_16x16x32_bf16 v[98:101], v[178:181], v[194:197], v[98:101]
	v_mfma_f32_16x16x32_bf16 v[86:89], v[170:173], v[204:207], v[86:89]
	v_mfma_f32_16x16x32_bf16 v[82:85], v[178:181], v[204:207], v[82:85]
	v_mfma_f32_16x16x32_bf16 v[70:73], v[170:173], v[214:217], v[70:73]
	v_mfma_f32_16x16x32_bf16 v[66:69], v[178:181], v[214:217], v[66:69]
	s_barrier
	v_mov_b32_e32 v132, v150
	s_add_i32 s78, s68, s29
	ds_read_b128 v[182:185], v156 offset:16384
	ds_read_b128 v[186:189], v156 offset:17408
	ds_read_b128 v[190:193], v156 offset:18432
	ds_read_b128 v[194:197], v156 offset:19456
	ds_read_b128 v[200:203], v156 offset:20480
	ds_read_b128 v[204:207], v156 offset:21504
	ds_read_b128 v[208:211], v156 offset:22528
	ds_read_b128 v[214:217], v156 offset:23552
	s_mov_b32 m0, s78
	s_nop 0
	global_load_lds_dwordx4 v132, s[54:55]
	v_mov_b32_e32 v132, v152
	s_add_i32 m0, s78, 0x2000
	s_add_u32 s78, s54, 0x80000
	global_load_lds_dwordx4 v132, s[54:55]
	s_addc_u32 s79, s55, 0
	v_mov_b32_e32 v132, v150
	s_add_i32 s80, s69, s29
	s_mov_b32 m0, s80
	s_nop 0
	global_load_lds_dwordx4 v132, s[78:79]
	v_mov_b32_e32 v132, v152
	s_add_i32 m0, s80, 0x2000
	s_nop 0
	global_load_lds_dwordx4 v132, s[78:79]
	v_mov_b32_e32 v132, v149
	s_mov_b32 m0, s41
	s_nop 0
	global_load_lds_dwordx4 v132, s[50:51]
	v_mov_b32_e32 v132, v151
	s_mov_b32 m0, s60
	s_nop 0
	global_load_lds_dwordx4 v132, s[50:51]
	s_waitcnt vmcnt(8)
	s_waitcnt lgkmcnt(0)
	s_barrier
	s_waitcnt lgkmcnt(0)
	v_mfma_f32_16x16x32_bf16 v[62:65], v[136:139], v[182:185], v[62:65]
	v_mfma_f32_16x16x32_bf16 v[58:61], v[158:161], v[182:185], v[58:61]
	v_mfma_f32_16x16x32_bf16 v[46:49], v[136:139], v[190:193], v[46:49]
	v_mfma_f32_16x16x32_bf16 v[42:45], v[158:161], v[190:193], v[42:45]
	v_mfma_f32_16x16x32_bf16 v[30:33], v[136:139], v[200:203], v[30:33]
	v_mfma_f32_16x16x32_bf16 v[26:29], v[158:161], v[200:203], v[26:29]
	v_mfma_f32_16x16x32_bf16 v[14:17], v[136:139], v[208:211], v[14:17]
	v_mfma_f32_16x16x32_bf16 v[10:13], v[158:161], v[208:211], v[10:13]
	v_mfma_f32_16x16x32_bf16 v[62:65], v[140:143], v[186:189], v[62:65]
	v_mfma_f32_16x16x32_bf16 v[58:61], v[162:165], v[186:189], v[58:61]
	v_mfma_f32_16x16x32_bf16 v[46:49], v[140:143], v[194:197], v[46:49]
	v_mfma_f32_16x16x32_bf16 v[42:45], v[162:165], v[194:197], v[42:45]
	v_mfma_f32_16x16x32_bf16 v[30:33], v[140:143], v[204:207], v[30:33]
	v_mfma_f32_16x16x32_bf16 v[26:29], v[162:165], v[204:207], v[26:29]
	v_mfma_f32_16x16x32_bf16 v[14:17], v[140:143], v[214:217], v[14:17]
	v_mfma_f32_16x16x32_bf16 v[10:13], v[162:165], v[214:217], v[10:13]
	v_mfma_f32_16x16x32_bf16 v[54:57], v[166:169], v[182:185], v[54:57]
	v_mfma_f32_16x16x32_bf16 v[50:53], v[174:177], v[182:185], v[50:53]
	v_mfma_f32_16x16x32_bf16 v[38:41], v[166:169], v[190:193], v[38:41]
	v_mfma_f32_16x16x32_bf16 v[34:37], v[174:177], v[190:193], v[34:37]
	v_mfma_f32_16x16x32_bf16 v[22:25], v[166:169], v[200:203], v[22:25]
	v_mfma_f32_16x16x32_bf16 v[18:21], v[174:177], v[200:203], v[18:21]
	v_mfma_f32_16x16x32_bf16 v[6:9], v[166:169], v[208:211], v[6:9]
	v_mfma_f32_16x16x32_bf16 v[2:5], v[174:177], v[208:211], v[2:5]
	v_mfma_f32_16x16x32_bf16 v[54:57], v[170:173], v[186:189], v[54:57]
	v_mfma_f32_16x16x32_bf16 v[50:53], v[178:181], v[186:189], v[50:53]
	v_mfma_f32_16x16x32_bf16 v[38:41], v[170:173], v[194:197], v[38:41]
	v_mfma_f32_16x16x32_bf16 v[34:37], v[178:181], v[194:197], v[34:37]
	v_mfma_f32_16x16x32_bf16 v[22:25], v[170:173], v[204:207], v[22:25]
	v_mfma_f32_16x16x32_bf16 v[18:21], v[178:181], v[204:207], v[18:21]
	v_mfma_f32_16x16x32_bf16 v[6:9], v[170:173], v[214:217], v[6:9]
	v_mfma_f32_16x16x32_bf16 v[2:5], v[178:181], v[214:217], v[2:5]
	s_barrier
; #define PG8_STAGE_A(bufoff, gbase, h, go) do { if constexpr (Sched::GATHER) { PG8_STAGE(bufoff, gbase, go[h]); } else { PG8_STAGE(bufoff, (gbase) + (h) * hstep, voffA); } } while (0)
; #define PG8_LDA(dst, b, h) do { _Pragma("unroll") for (int m = 0; m < 4; ++m) _Pragma("unroll") for (int k = 0; k < 2; ++k) dst[m][k] = *(const LAS bf16x8*)(lds + PG8_SA(b, h) + aoff + m * 2048 + k * 1024); } while (0)
; #define PG8_LDB(dst, b, h) do { _Pragma("unroll") for (int n = 0; n < 2; ++n) _Pragma("unroll") for (int k = 0; k < 2; ++k) dst[n][k] = *(const LAS bf16x8*)(lds + PG8_SB(b, h) + boff + n * 2048 + k * 1024); } while (0)
; #define PG8_WAIT_V(n) asm volatile("s_waitcnt vmcnt(" #n ")" ::: "memory")
; #define PG8_WAIT_L(n) asm volatile("s_waitcnt lgkmcnt(" #n ")" ::: "memory")
; #define PG8_BAR __builtin_amdgcn_s_barrier()
; #define PG8_SCHED __builtin_amdgcn_sched_barrier(0)
;     ...
;             PG8_LDB(B0, 1, 0); PG8_LDB(B1, 1, 1); PG8_SCHED; PG8_LDA(At, 1, 0); PG8_STAGE_A(PG8_SA(0, 1), a2, 1, gc);
;             PG8_WAIT_V(8); PG8_WAIT_L(0); PG8_BAR; PG8_MMA(0, 0, At, B0); PG8_MMA(0, 1, At, B1); PG8_BAR; PG8_SCHED;
	s_add_i32 s80, 0, 0x18000
	v_add_u32_e32 v132, s80, v146
	s_add_i32 s81, 0, 0x1c000
	ds_read_b128 v[136:139], v132
	ds_read_b128 v[140:143], v132 offset:1024
	ds_read_b128 v[158:161], v132 offset:2048
	ds_read_b128 v[162:165], v132 offset:3072
	v_add_u32_e32 v132, s81, v146
	ds_read_b128 v[166:169], v132
	ds_read_b128 v[170:173], v132 offset:1024
	ds_read_b128 v[174:177], v132 offset:2048
	ds_read_b128 v[178:181], v132 offset:3072
	s_add_u32 s78, s50, 0x80000
	v_mov_b32_e32 v132, v149
	s_mov_b32 m0, s61
	ds_read_b128 v[182:185], v156 offset:32768
	ds_read_b128 v[186:189], v156 offset:33792
	ds_read_b128 v[190:193], v156 offset:34816
	ds_read_b128 v[194:197], v156 offset:35840
	ds_read_b128 v[200:203], v156 offset:36864
	ds_read_b128 v[204:207], v156 offset:37888
	ds_read_b128 v[208:211], v156 offset:38912
	ds_read_b128 v[214:217], v156 offset:39936
	s_addc_u32 s79, s51, 0
	s_nop 0
	global_load_lds_dwordx4 v132, s[78:79]
	v_mov_b32_e32 v132, v151
	s_mov_b32 m0, s62
	s_nop 0
	global_load_lds_dwordx4 v132, s[78:79]
	s_waitcnt vmcnt(8)
	s_waitcnt lgkmcnt(0)
	s_barrier
	s_waitcnt lgkmcnt(0)
	v_mfma_f32_16x16x32_bf16 v[126:129], v[136:139], v[182:185], v[126:129]
	v_mfma_f32_16x16x32_bf16 v[122:125], v[158:161], v[182:185], v[122:125]
	v_mfma_f32_16x16x32_bf16 v[110:113], v[136:139], v[190:193], v[110:113]
	v_mfma_f32_16x16x32_bf16 v[106:109], v[158:161], v[190:193], v[106:109]
	v_mfma_f32_16x16x32_bf16 v[94:97], v[136:139], v[200:203], v[94:97]
	v_mfma_f32_16x16x32_bf16 v[90:93], v[158:161], v[200:203], v[90:93]
	v_mfma_f32_16x16x32_bf16 v[78:81], v[136:139], v[208:211], v[78:81]
	v_mfma_f32_16x16x32_bf16 v[74:77], v[158:161], v[208:211], v[74:77]
	v_mfma_f32_16x16x32_bf16 v[126:129], v[140:143], v[186:189], v[126:129]
	v_mfma_f32_16x16x32_bf16 v[122:125], v[162:165], v[186:189], v[122:125]
	v_mfma_f32_16x16x32_bf16 v[110:113], v[140:143], v[194:197], v[110:113]
	v_mfma_f32_16x16x32_bf16 v[106:109], v[162:165], v[194:197], v[106:109]
	v_mfma_f32_16x16x32_bf16 v[94:97], v[140:143], v[204:207], v[94:97]
	v_mfma_f32_16x16x32_bf16 v[90:93], v[162:165], v[204:207], v[90:93]
	v_mfma_f32_16x16x32_bf16 v[78:81], v[140:143], v[214:217], v[78:81]
	v_mfma_f32_16x16x32_bf16 v[74:77], v[162:165], v[214:217], v[74:77]
	v_mfma_f32_16x16x32_bf16 v[118:121], v[166:169], v[182:185], v[118:121]
	v_mfma_f32_16x16x32_bf16 v[114:117], v[174:177], v[182:185], v[114:117]
	v_mfma_f32_16x16x32_bf16 v[102:105], v[166:169], v[190:193], v[102:105]
	v_mfma_f32_16x16x32_bf16 v[98:101], v[174:177], v[190:193], v[98:101]
	v_mfma_f32_16x16x32_bf16 v[86:89], v[166:169], v[200:203], v[86:89]
	v_mfma_f32_16x16x32_bf16 v[82:85], v[174:177], v[200:203], v[82:85]
	v_mfma_f32_16x16x32_bf16 v[70:73], v[166:169], v[208:211], v[70:73]
	v_mfma_f32_16x16x32_bf16 v[66:69], v[174:177], v[208:211], v[66:69]
	v_mfma_f32_16x16x32_bf16 v[118:121], v[170:173], v[186:189], v[118:121]
	v_mfma_f32_16x16x32_bf16 v[114:117], v[178:181], v[186:189], v[114:117]
	v_mfma_f32_16x16x32_bf16 v[102:105], v[170:173], v[194:197], v[102:105]
	v_mfma_f32_16x16x32_bf16 v[98:101], v[178:181], v[194:197], v[98:101]
	v_mfma_f32_16x16x32_bf16 v[86:89], v[170:173], v[204:207], v[86:89]
	v_mfma_f32_16x16x32_bf16 v[82:85], v[178:181], v[204:207], v[82:85]
	v_mfma_f32_16x16x32_bf16 v[70:73], v[170:173], v[214:217], v[70:73]
	v_mfma_f32_16x16x32_bf16 v[66:69], v[178:181], v[214:217], v[66:69]
	s_barrier
; #define PG8_STAGE(bufoff, gbase, voff) do { _Pragma("unroll") for (int _i = 0; _i < 2; ++_i) { unsigned _vo = (voff)[_i]; asm volatile("" : "+v"(_vo)); \
;         __builtin_amdgcn_global_load_lds((const unsigned*)((const char*)(gbase) + _vo), (LAS unsigned*)(lds + (bufoff) + ldsw + _i * 8192), 16, 0, 0); } } while (0)
; #define PG8_STAGE_A(bufoff, gbase, h, go) do { if constexpr (Sched::GATHER) { PG8_STAGE(bufoff, gbase, go[h]); } else { PG8_STAGE(bufoff, (gbase) + (h) * hstep, voffA); } } while (0)
; #define PG8_LDA(dst, b, h) do { _Pragma("unroll") for (int m = 0; m < 4; ++m) _Pragma("unroll") for (int k = 0; k < 2; ++k) dst[m][k] = *(const LAS bf16x8*)(lds + PG8_SA(b, h) + aoff + m * 2048 + k * 1024); } while (0)
; #define PG8_WAIT_V(n) asm volatile("s_waitcnt vmcnt(" #n ")" ::: "memory")
; #define PG8_WAIT_L(n) asm volatile("s_waitcnt lgkmcnt(" #n ")" ::: "memory")
; #define PG8_BAR __builtin_amdgcn_s_barrier()
; #define PG8_SCHED __builtin_amdgcn_sched_barrier(0)
;     ...
;             PG8_LDA(At, 1, 1); PG8_STAGE(PG8_SB(1, 0), b3, voffB); PG8_STAGE(PG8_SB(1, 1), b3 + hstep, voffB); PG8_STAGE_A(PG8_SA(1, 0), a3, 0, gc);
;             PG8_WAIT_V(8); PG8_WAIT_L(0); PG8_BAR; PG8_MMA(1, 0, At, B0); PG8_MMA(1, 1, At, B1); PG8_BAR; PG8_SCHED;
	v_mov_b32_e32 v132, v150
	ds_read_b128 v[182:185], v156 offset:49152
	ds_read_b128 v[186:189], v156 offset:50176
	ds_read_b128 v[190:193], v156 offset:51200
	ds_read_b128 v[194:197], v156 offset:52224
	ds_read_b128 v[200:203], v156 offset:53248
	ds_read_b128 v[204:207], v156 offset:54272
	ds_read_b128 v[208:211], v156 offset:55296
	ds_read_b128 v[214:217], v156 offset:56320
	s_add_i32 s78, s80, s29
	v_lshl_add_u64 v[218:219], s[54:55], 0, v[132:133]
	v_lshl_add_u64 v[218:219], v[218:219], 0, s[8:9]
	s_mov_b32 m0, s78
	v_mov_b32_e32 v132, v152
	global_load_lds_dwordx4 v[218:219], off
	s_add_i32 m0, s78, 0x2000
	s_nop 0
	v_lshl_add_u64 v[218:219], s[54:55], 0, v[132:133]
	s_add_u32 s54, s54, 0x80080
	v_lshl_add_u64 v[218:219], v[218:219], 0, s[8:9]
	s_addc_u32 s55, s55, 0
	v_mov_b32_e32 v132, v150
	s_add_i32 s78, s81, s29
	global_load_lds_dwordx4 v[218:219], off
	s_mov_b32 m0, s78
	s_nop 0
	global_load_lds_dwordx4 v132, s[54:55]
	v_mov_b32_e32 v132, v152
	s_add_i32 m0, s78, 0x2000
	s_nop 0
	global_load_lds_dwordx4 v132, s[54:55]
	v_mov_b32_e32 v132, v149
	s_mov_b32 m0, s65
	v_lshl_add_u64 v[218:219], s[50:51], 0, v[132:133]
	v_lshl_add_u64 v[218:219], v[218:219], 0, s[8:9]
	v_mov_b32_e32 v132, v151
	global_load_lds_dwordx4 v[218:219], off
	s_mov_b32 m0, s66
	v_lshl_add_u64 v[218:219], s[50:51], 0, v[132:133]
	v_lshl_add_u64 v[218:219], v[218:219], 0, s[8:9]
	global_load_lds_dwordx4 v[218:219], off
	s_waitcnt vmcnt(8)
	s_waitcnt lgkmcnt(0)
	s_barrier
	s_waitcnt lgkmcnt(0)
	v_mfma_f32_16x16x32_bf16 v[62:65], v[136:139], v[182:185], v[62:65]
	v_mfma_f32_16x16x32_bf16 v[58:61], v[158:161], v[182:185], v[58:61]
	v_mfma_f32_16x16x32_bf16 v[46:49], v[136:139], v[190:193], v[46:49]
	v_mfma_f32_16x16x32_bf16 v[42:45], v[158:161], v[190:193], v[42:45]
	v_mfma_f32_16x16x32_bf16 v[30:33], v[136:139], v[200:203], v[30:33]
	v_mfma_f32_16x16x32_bf16 v[26:29], v[158:161], v[200:203], v[26:29]
	v_mfma_f32_16x16x32_bf16 v[14:17], v[136:139], v[208:211], v[14:17]
	v_mfma_f32_16x16x32_bf16 v[10:13], v[158:161], v[208:211], v[10:13]
	v_mfma_f32_16x16x32_bf16 v[62:65], v[140:143], v[186:189], v[62:65]
	v_mfma_f32_16x16x32_bf16 v[58:61], v[162:165], v[186:189], v[58:61]
	v_mfma_f32_16x16x32_bf16 v[46:49], v[140:143], v[194:197], v[46:49]
	v_mfma_f32_16x16x32_bf16 v[42:45], v[162:165], v[194:197], v[42:45]
	v_mfma_f32_16x16x32_bf16 v[30:33], v[140:143], v[204:207], v[30:33]
	v_mfma_f32_16x16x32_bf16 v[26:29], v[162:165], v[204:207], v[26:29]
	v_mfma_f32_16x16x32_bf16 v[14:17], v[140:143], v[214:217], v[14:17]
	v_mfma_f32_16x16x32_bf16 v[10:13], v[162:165], v[214:217], v[10:13]
	v_mfma_f32_16x16x32_bf16 v[54:57], v[166:169], v[182:185], v[54:57]
	v_mfma_f32_16x16x32_bf16 v[50:53], v[174:177], v[182:185], v[50:53]
	v_mfma_f32_16x16x32_bf16 v[38:41], v[166:169], v[190:193], v[38:41]
	v_mfma_f32_16x16x32_bf16 v[34:37], v[174:177], v[190:193], v[34:37]
	v_mfma_f32_16x16x32_bf16 v[22:25], v[166:169], v[200:203], v[22:25]
	v_mfma_f32_16x16x32_bf16 v[18:21], v[174:177], v[200:203], v[18:21]
	v_mfma_f32_16x16x32_bf16 v[6:9], v[166:169], v[208:211], v[6:9]
	v_mfma_f32_16x16x32_bf16 v[2:5], v[174:177], v[208:211], v[2:5]
	v_mfma_f32_16x16x32_bf16 v[54:57], v[170:173], v[186:189], v[54:57]
	v_mfma_f32_16x16x32_bf16 v[50:53], v[178:181], v[186:189], v[50:53]
	v_mfma_f32_16x16x32_bf16 v[38:41], v[170:173], v[194:197], v[38:41]
	v_mfma_f32_16x16x32_bf16 v[34:37], v[178:181], v[194:197], v[34:37]
	v_mfma_f32_16x16x32_bf16 v[22:25], v[170:173], v[204:207], v[22:25]
	v_mfma_f32_16x16x32_bf16 v[18:21], v[178:181], v[204:207], v[18:21]
	v_mfma_f32_16x16x32_bf16 v[6:9], v[170:173], v[214:217], v[6:9]
	v_mfma_f32_16x16x32_bf16 v[2:5], v[178:181], v[214:217], v[2:5]
	s_barrier
	s_add_i32 s77, s77, 2
	s_add_u32 s42, s42, 0x100
	s_addc_u32 s43, s43, 0
	s_add_u32 s75, s75, 0x100
	s_addc_u32 s76, s76, 0
	s_cmp_gt_u32 s77, 29
	s_cbranch_scc0 .LBB5_889
	s_and_b64 vcc, exec, s[14:15]
	s_cbranch_vccz .LBB5_892
	s_barrier

; #define PG8_STAGE(bufoff, gbase, voff) do { _Pragma("unroll") for (int _i = 0; _i < 2; ++_i) { unsigned _vo = (voff)[_i]; asm volatile("" : "+v"(_vo)); \
;         __builtin_amdgcn_global_load_lds((const unsigned*)((const char*)(gbase) + _vo), (LAS unsigned*)(lds + (bufoff) + ldsw + _i * 8192), 16, 0, 0); } } while (0)
; #define PG8_STAGE_A(bufoff, gbase, h, go) do { if constexpr (Sched::GATHER) { PG8_STAGE(bufoff, gbase, go[h]); } else { PG8_STAGE(bufoff, (gbase) + (h) * hstep, voffA); } } while (0)
; #define PG8_LDA(dst, b, h) do { _Pragma("unroll") for (int m = 0; m < 4; ++m) _Pragma("unroll") for (int k = 0; k < 2; ++k) dst[m][k] = *(const LAS bf16x8*)(lds + PG8_SA(b, h) + aoff + m * 2048 + k * 1024); } while (0)
; #define PG8_LDB(dst, b, h) do { _Pragma("unroll") for (int n = 0; n < 2; ++n) _Pragma("unroll") for (int k = 0; k < 2; ++k) dst[n][k] = *(const LAS bf16x8*)(lds + PG8_SB(b, h) + boff + n * 2048 + k * 1024); } while (0)
; #define PG8_WAIT_V(n) asm volatile("s_waitcnt vmcnt(" #n ")" ::: "memory")
; #define PG8_WAIT_L(n) asm volatile("s_waitcnt lgkmcnt(" #n ")" ::: "memory")
; #define PG8_BAR __builtin_amdgcn_s_barrier()
;     ...
;         for (int t = 0; t < nt; t += 2) {
;             const bool last = (t == nt - 2);
;             if constexpr (Epi::MIDK) { if (t == nt / 2) { int fr_e = fr; asm volatile("" : "+v"(fr_e)); E.midk(acc, cur, wr, fr_e); } }
;             const char* a1 = cA + (size_t)(t + 1) * kstep;
;             const char* a2 = last ? nA : cA + (size_t)(t + 2) * kstep; const char* b2 = last ? nB : cB + (size_t)(t + 2) * kstep;
;             const char* a3 = a2 + kstep; const char* b3 = b2 + kstep;
;             PG8_LDB(B0, 0, 0); PG8_LDB(B1, 0, 1); PG8_SCHED; PG8_LDA(At, 0, 0); PG8_STAGE_A(PG8_SA(1, 1), a1, 1, gc);
;             if constexpr (Sched::GATHER) { if (last) {
; #pragma unroll
;                 for (int h = 0; h < 2; ++h)
; #pragma unroll
;                     for (int i = 0; i < 2; ++i) gc[h][i] = gn[h][i]; } }
;             PG8_WAIT_V(8); PG8_WAIT_L(0); PG8_BAR; PG8_MMA(0, 0, At, B0); PG8_MMA(0, 1, At, B1); PG8_BAR; PG8_SCHED;
;             PG8_LDA(At, 0, 1); PG8_STAGE(PG8_SB(0, 0), b2, voffB); PG8_STAGE(PG8_SB(0, 1), b2 + hstep, voffB); PG8_STAGE_A(PG8_SA(0, 0), a2, 0, gc);
;             PG8_WAIT_V(8); PG8_WAIT_L(0); PG8_BAR; PG8_MMA(1, 0, At, B0); PG8_MMA(1, 1, At, B1); PG8_BAR; PG8_SCHED;
.LBB5_917:
	ds_read_b128 v[130:133], v157
	ds_read_b128 v[134:137], v157 offset:1024
	ds_read_b128 v[142:145], v157 offset:2048
	ds_read_b128 v[160:163], v157 offset:3072
	ds_read_b128 v[164:167], v158
	ds_read_b128 v[168:171], v158 offset:1024
	ds_read_b128 v[172:175], v158 offset:2048
	ds_read_b128 v[176:179], v158 offset:3072
	s_add_u32 s4, s0, 0xfff80080
	s_addc_u32 s5, s1, -1
	s_cmp_eq_u32 s79, 28
	s_cselect_b32 s5, s51, s5
	s_cselect_b32 s4, s50, s4
	s_cselect_b32 s7, s61, s78
	s_cselect_b32 s6, s60, s77
	v_mov_b32_e32 v138, v149
	ds_read_b128 v[180:183], v159
	ds_read_b128 v[184:187], v159 offset:1024
	ds_read_b128 v[188:191], v159 offset:2048
	ds_read_b128 v[192:195], v159 offset:3072
	ds_read_b128 v[200:203], v159 offset:4096
	ds_read_b128 v[204:207], v159 offset:5120
	ds_read_b128 v[208:211], v159 offset:6144
	ds_read_b128 v[214:217], v159 offset:7168
	s_add_i32 m0, s39, 0xc000
	s_nop 0
	global_load_lds_dwordx4 v138, s[0:1]
	v_mov_b32_e32 v138, v151
	s_add_i32 m0, s39, 0xe000
	s_nop 0
	global_load_lds_dwordx4 v138, s[0:1]
	s_waitcnt vmcnt(8)
	s_waitcnt lgkmcnt(0)
	s_barrier
	s_waitcnt lgkmcnt(0)
	v_mfma_f32_16x16x32_bf16 v[126:129], v[130:133], v[180:183], v[126:129]
	v_mfma_f32_16x16x32_bf16 v[122:125], v[142:145], v[180:183], v[122:125]
	v_mfma_f32_16x16x32_bf16 v[118:121], v[130:133], v[188:191], v[118:121]
	v_mfma_f32_16x16x32_bf16 v[114:117], v[142:145], v[188:191], v[114:117]
	v_mfma_f32_16x16x32_bf16 v[110:113], v[130:133], v[200:203], v[110:113]
	v_mfma_f32_16x16x32_bf16 v[106:109], v[142:145], v[200:203], v[106:109]
	v_mfma_f32_16x16x32_bf16 v[102:105], v[130:133], v[208:211], v[102:105]
	v_mfma_f32_16x16x32_bf16 v[98:101], v[142:145], v[208:211], v[98:101]
	v_mfma_f32_16x16x32_bf16 v[126:129], v[134:137], v[184:187], v[126:129]
	v_mfma_f32_16x16x32_bf16 v[122:125], v[160:163], v[184:187], v[122:125]
	v_mfma_f32_16x16x32_bf16 v[118:121], v[134:137], v[192:195], v[118:121]
	v_mfma_f32_16x16x32_bf16 v[114:117], v[160:163], v[192:195], v[114:117]
	v_mfma_f32_16x16x32_bf16 v[110:113], v[134:137], v[204:207], v[110:113]
	v_mfma_f32_16x16x32_bf16 v[106:109], v[160:163], v[204:207], v[106:109]
	v_mfma_f32_16x16x32_bf16 v[102:105], v[134:137], v[214:217], v[102:105]
	v_mfma_f32_16x16x32_bf16 v[98:101], v[160:163], v[214:217], v[98:101]
	v_mfma_f32_16x16x32_bf16 v[62:65], v[164:167], v[180:183], v[62:65]
	v_mfma_f32_16x16x32_bf16 v[58:61], v[172:175], v[180:183], v[58:61]
	v_mfma_f32_16x16x32_bf16 v[54:57], v[164:167], v[188:191], v[54:57]
	v_mfma_f32_16x16x32_bf16 v[50:53], v[172:175], v[188:191], v[50:53]
	v_mfma_f32_16x16x32_bf16 v[46:49], v[164:167], v[200:203], v[46:49]
	v_mfma_f32_16x16x32_bf16 v[42:45], v[172:175], v[200:203], v[42:45]
	v_mfma_f32_16x16x32_bf16 v[38:41], v[164:167], v[208:211], v[38:41]
	v_mfma_f32_16x16x32_bf16 v[34:37], v[172:175], v[208:211], v[34:37]
	v_mfma_f32_16x16x32_bf16 v[62:65], v[168:171], v[184:187], v[62:65]
	v_mfma_f32_16x16x32_bf16 v[58:61], v[176:179], v[184:187], v[58:61]
	v_mfma_f32_16x16x32_bf16 v[54:57], v[168:171], v[192:195], v[54:57]
	v_mfma_f32_16x16x32_bf16 v[50:53], v[176:179], v[192:195], v[50:53]
	v_mfma_f32_16x16x32_bf16 v[46:49], v[168:171], v[204:207], v[46:49]
	v_mfma_f32_16x16x32_bf16 v[42:45], v[176:179], v[204:207], v[42:45]
	v_mfma_f32_16x16x32_bf16 v[38:41], v[168:171], v[214:217], v[38:41]
	v_mfma_f32_16x16x32_bf16 v[34:37], v[176:179], v[214:217], v[34:37]
	s_barrier
	v_mov_b32_e32 v138, v150
	s_add_i32 s80, s70, s37
	ds_read_b128 v[180:183], v159 offset:16384
	ds_read_b128 v[184:187], v159 offset:17408
	ds_read_b128 v[188:191], v159 offset:18432
	ds_read_b128 v[192:195], v159 offset:19456
	ds_read_b128 v[200:203], v159 offset:20480
	ds_read_b128 v[204:207], v159 offset:21504
	ds_read_b128 v[208:211], v159 offset:22528
	ds_read_b128 v[214:217], v159 offset:23552
	s_mov_b32 m0, s80
	s_nop 0
	global_load_lds_dwordx4 v138, s[6:7]
	v_mov_b32_e32 v138, v152
	s_add_i32 m0, s80, 0x2000
	s_add_u32 s80, s6, 0x80000
	global_load_lds_dwordx4 v138, s[6:7]
	s_addc_u32 s81, s7, 0
	v_mov_b32_e32 v138, v150
	s_add_i32 s82, s71, s37
	s_mov_b32 m0, s82
	s_nop 0
	global_load_lds_dwordx4 v138, s[80:81]
	v_mov_b32_e32 v138, v152
	s_add_i32 m0, s82, 0x2000
	s_nop 0
	global_load_lds_dwordx4 v138, s[80:81]
	v_mov_b32_e32 v138, v149
	s_mov_b32 m0, s39
	s_nop 0
	global_load_lds_dwordx4 v138, s[4:5]
	v_mov_b32_e32 v138, v151
	s_mov_b32 m0, s41
	s_nop 0
	global_load_lds_dwordx4 v138, s[4:5]
	s_waitcnt vmcnt(8)
	s_waitcnt lgkmcnt(0)
	s_barrier
	s_waitcnt lgkmcnt(0)
	v_mfma_f32_16x16x32_bf16 v[94:97], v[130:133], v[180:183], v[94:97]
	v_mfma_f32_16x16x32_bf16 v[90:93], v[142:145], v[180:183], v[90:93]
	v_mfma_f32_16x16x32_bf16 v[86:89], v[130:133], v[188:191], v[86:89]
	v_mfma_f32_16x16x32_bf16 v[82:85], v[142:145], v[188:191], v[82:85]
	v_mfma_f32_16x16x32_bf16 v[78:81], v[130:133], v[200:203], v[78:81]
	v_mfma_f32_16x16x32_bf16 v[74:77], v[142:145], v[200:203], v[74:77]
	v_mfma_f32_16x16x32_bf16 v[70:73], v[130:133], v[208:211], v[70:73]
	v_mfma_f32_16x16x32_bf16 v[66:69], v[142:145], v[208:211], v[66:69]
	v_mfma_f32_16x16x32_bf16 v[94:97], v[134:137], v[184:187], v[94:97]
	v_mfma_f32_16x16x32_bf16 v[90:93], v[160:163], v[184:187], v[90:93]
	v_mfma_f32_16x16x32_bf16 v[86:89], v[134:137], v[192:195], v[86:89]
	v_mfma_f32_16x16x32_bf16 v[82:85], v[160:163], v[192:195], v[82:85]
	v_mfma_f32_16x16x32_bf16 v[78:81], v[134:137], v[204:207], v[78:81]
	v_mfma_f32_16x16x32_bf16 v[74:77], v[160:163], v[204:207], v[74:77]
	v_mfma_f32_16x16x32_bf16 v[70:73], v[134:137], v[214:217], v[70:73]
	v_mfma_f32_16x16x32_bf16 v[66:69], v[160:163], v[214:217], v[66:69]
	v_mfma_f32_16x16x32_bf16 v[30:33], v[164:167], v[180:183], v[30:33]
	v_mfma_f32_16x16x32_bf16 v[26:29], v[172:175], v[180:183], v[26:29]
	v_mfma_f32_16x16x32_bf16 v[22:25], v[164:167], v[188:191], v[22:25]
	v_mfma_f32_16x16x32_bf16 v[18:21], v[172:175], v[188:191], v[18:21]
	v_mfma_f32_16x16x32_bf16 v[14:17], v[164:167], v[200:203], v[14:17]
	v_mfma_f32_16x16x32_bf16 v[10:13], v[172:175], v[200:203], v[10:13]
	v_mfma_f32_16x16x32_bf16 v[6:9], v[164:167], v[208:211], v[6:9]
	v_mfma_f32_16x16x32_bf16 v[2:5], v[172:175], v[208:211], v[2:5]
	v_mfma_f32_16x16x32_bf16 v[30:33], v[168:171], v[184:187], v[30:33]
	v_mfma_f32_16x16x32_bf16 v[26:29], v[176:179], v[184:187], v[26:29]
	v_mfma_f32_16x16x32_bf16 v[22:25], v[168:171], v[192:195], v[22:25]
	v_mfma_f32_16x16x32_bf16 v[18:21], v[176:179], v[192:195], v[18:21]
	v_mfma_f32_16x16x32_bf16 v[14:17], v[168:171], v[204:207], v[14:17]
	v_mfma_f32_16x16x32_bf16 v[10:13], v[176:179], v[204:207], v[10:13]
	v_mfma_f32_16x16x32_bf16 v[6:9], v[168:171], v[214:217], v[6:9]
	v_mfma_f32_16x16x32_bf16 v[2:5], v[176:179], v[214:217], v[2:5]
	s_barrier
; #define PG8_STAGE_A(bufoff, gbase, h, go) do { if constexpr (Sched::GATHER) { PG8_STAGE(bufoff, gbase, go[h]); } else { PG8_STAGE(bufoff, (gbase) + (h) * hstep, voffA); } } while (0)
; #define PG8_LDA(dst, b, h) do { _Pragma("unroll") for (int m = 0; m < 4; ++m) _Pragma("unroll") for (int k = 0; k < 2; ++k) dst[m][k] = *(const LAS bf16x8*)(lds + PG8_SA(b, h) + aoff + m * 2048 + k * 1024); } while (0)
; #define PG8_LDB(dst, b, h) do { _Pragma("unroll") for (int n = 0; n < 2; ++n) _Pragma("unroll") for (int k = 0; k < 2; ++k) dst[n][k] = *(const LAS bf16x8*)(lds + PG8_SB(b, h) + boff + n * 2048 + k * 1024); } while (0)
; #define PG8_WAIT_V(n) asm volatile("s_waitcnt vmcnt(" #n ")" ::: "memory")
; #define PG8_WAIT_L(n) asm volatile("s_waitcnt lgkmcnt(" #n ")" ::: "memory")
; #define PG8_BAR __builtin_amdgcn_s_barrier()
; #define PG8_SCHED __builtin_amdgcn_sched_barrier(0)
;     ...
;             PG8_LDB(B0, 1, 0); PG8_LDB(B1, 1, 1); PG8_SCHED; PG8_LDA(At, 1, 0); PG8_STAGE_A(PG8_SA(0, 1), a2, 1, gc);
;             PG8_WAIT_V(8); PG8_WAIT_L(0); PG8_BAR; PG8_MMA(0, 0, At, B0); PG8_MMA(0, 1, At, B1); PG8_BAR; PG8_SCHED;
	s_add_i32 s82, 0, 0x18000
	v_add_u32_e32 v138, s82, v156
	s_add_i32 s83, 0, 0x1c000
	ds_read_b128 v[130:133], v138
	ds_read_b128 v[134:137], v138 offset:1024
	ds_read_b128 v[142:145], v138 offset:2048
	ds_read_b128 v[160:163], v138 offset:3072
	v_add_u32_e32 v138, s83, v156
	ds_read_b128 v[164:167], v138
	ds_read_b128 v[168:171], v138 offset:1024
	ds_read_b128 v[172:175], v138 offset:2048
	ds_read_b128 v[176:179], v138 offset:3072
	s_add_u32 s80, s4, 0x80000
	v_mov_b32_e32 v138, v149
	s_mov_b32 m0, s63
	ds_read_b128 v[180:183], v159 offset:32768
	ds_read_b128 v[184:187], v159 offset:33792
	ds_read_b128 v[188:191], v159 offset:34816
	ds_read_b128 v[192:195], v159 offset:35840
	ds_read_b128 v[200:203], v159 offset:36864
	ds_read_b128 v[204:207], v159 offset:37888
	ds_read_b128 v[208:211], v159 offset:38912
	ds_read_b128 v[214:217], v159 offset:39936
	s_addc_u32 s81, s5, 0
	s_nop 0
	global_load_lds_dwordx4 v138, s[80:81]
	v_mov_b32_e32 v138, v151
	s_mov_b32 m0, s64
	s_nop 0
	global_load_lds_dwordx4 v138, s[80:81]
	s_waitcnt vmcnt(8)
	s_waitcnt lgkmcnt(0)
	s_barrier
	s_waitcnt lgkmcnt(0)
	v_mfma_f32_16x16x32_bf16 v[126:129], v[130:133], v[180:183], v[126:129]
	v_mfma_f32_16x16x32_bf16 v[122:125], v[142:145], v[180:183], v[122:125]
	v_mfma_f32_16x16x32_bf16 v[118:121], v[130:133], v[188:191], v[118:121]
	v_mfma_f32_16x16x32_bf16 v[114:117], v[142:145], v[188:191], v[114:117]
	v_mfma_f32_16x16x32_bf16 v[110:113], v[130:133], v[200:203], v[110:113]
	v_mfma_f32_16x16x32_bf16 v[106:109], v[142:145], v[200:203], v[106:109]
	v_mfma_f32_16x16x32_bf16 v[102:105], v[130:133], v[208:211], v[102:105]
	v_mfma_f32_16x16x32_bf16 v[98:101], v[142:145], v[208:211], v[98:101]
	v_mfma_f32_16x16x32_bf16 v[126:129], v[134:137], v[184:187], v[126:129]
	v_mfma_f32_16x16x32_bf16 v[122:125], v[160:163], v[184:187], v[122:125]
	v_mfma_f32_16x16x32_bf16 v[118:121], v[134:137], v[192:195], v[118:121]
	v_mfma_f32_16x16x32_bf16 v[114:117], v[160:163], v[192:195], v[114:117]
	v_mfma_f32_16x16x32_bf16 v[110:113], v[134:137], v[204:207], v[110:113]
	v_mfma_f32_16x16x32_bf16 v[106:109], v[160:163], v[204:207], v[106:109]
	v_mfma_f32_16x16x32_bf16 v[102:105], v[134:137], v[214:217], v[102:105]
	v_mfma_f32_16x16x32_bf16 v[98:101], v[160:163], v[214:217], v[98:101]
	v_mfma_f32_16x16x32_bf16 v[62:65], v[164:167], v[180:183], v[62:65]
	v_mfma_f32_16x16x32_bf16 v[58:61], v[172:175], v[180:183], v[58:61]
	v_mfma_f32_16x16x32_bf16 v[54:57], v[164:167], v[188:191], v[54:57]
	v_mfma_f32_16x16x32_bf16 v[50:53], v[172:175], v[188:191], v[50:53]
	v_mfma_f32_16x16x32_bf16 v[46:49], v[164:167], v[200:203], v[46:49]
	v_mfma_f32_16x16x32_bf16 v[42:45], v[172:175], v[200:203], v[42:45]
	v_mfma_f32_16x16x32_bf16 v[38:41], v[164:167], v[208:211], v[38:41]
	v_mfma_f32_16x16x32_bf16 v[34:37], v[172:175], v[208:211], v[34:37]
	v_mfma_f32_16x16x32_bf16 v[62:65], v[168:171], v[184:187], v[62:65]
	v_mfma_f32_16x16x32_bf16 v[58:61], v[176:179], v[184:187], v[58:61]
	v_mfma_f32_16x16x32_bf16 v[54:57], v[168:171], v[192:195], v[54:57]
	v_mfma_f32_16x16x32_bf16 v[50:53], v[176:179], v[192:195], v[50:53]
	v_mfma_f32_16x16x32_bf16 v[46:49], v[168:171], v[204:207], v[46:49]
	v_mfma_f32_16x16x32_bf16 v[42:45], v[176:179], v[204:207], v[42:45]
	v_mfma_f32_16x16x32_bf16 v[38:41], v[168:171], v[214:217], v[38:41]
	v_mfma_f32_16x16x32_bf16 v[34:37], v[176:179], v[214:217], v[34:37]
	s_barrier
; #define PG8_STAGE(bufoff, gbase, voff) do { _Pragma("unroll") for (int _i = 0; _i < 2; ++_i) { unsigned _vo = (voff)[_i]; asm volatile("" : "+v"(_vo)); \
;         __builtin_amdgcn_global_load_lds((const unsigned*)((const char*)(gbase) + _vo), (LAS unsigned*)(lds + (bufoff) + ldsw + _i * 8192), 16, 0, 0); } } while (0)
; #define PG8_STAGE_A(bufoff, gbase, h, go) do { if constexpr (Sched::GATHER) { PG8_STAGE(bufoff, gbase, go[h]); } else { PG8_STAGE(bufoff, (gbase) + (h) * hstep, voffA); } } while (0)
; #define PG8_LDA(dst, b, h) do { _Pragma("unroll") for (int m = 0; m < 4; ++m) _Pragma("unroll") for (int k = 0; k < 2; ++k) dst[m][k] = *(const LAS bf16x8*)(lds + PG8_SA(b, h) + aoff + m * 2048 + k * 1024); } while (0)
; #define PG8_WAIT_V(n) asm volatile("s_waitcnt vmcnt(" #n ")" ::: "memory")
; #define PG8_WAIT_L(n) asm volatile("s_waitcnt lgkmcnt(" #n ")" ::: "memory")
; #define PG8_BAR __builtin_amdgcn_s_barrier()
; #define PG8_SCHED __builtin_amdgcn_sched_barrier(0)
;     ...
;             PG8_LDA(At, 1, 1); PG8_STAGE(PG8_SB(1, 0), b3, voffB); PG8_STAGE(PG8_SB(1, 1), b3 + hstep, voffB); PG8_STAGE_A(PG8_SA(1, 0), a3, 0, gc);
;             PG8_WAIT_V(8); PG8_WAIT_L(0); PG8_BAR; PG8_MMA(1, 0, At, B0); PG8_MMA(1, 1, At, B1); PG8_BAR; PG8_SCHED;
	v_mov_b32_e32 v138, v150
	ds_read_b128 v[180:183], v159 offset:49152
	ds_read_b128 v[184:187], v159 offset:50176
	ds_read_b128 v[188:191], v159 offset:51200
	ds_read_b128 v[192:195], v159 offset:52224
	ds_read_b128 v[200:203], v159 offset:53248
	ds_read_b128 v[204:207], v159 offset:54272
	ds_read_b128 v[208:211], v159 offset:55296
	ds_read_b128 v[214:217], v159 offset:56320
	s_add_i32 s80, s82, s37
	v_lshl_add_u64 v[146:147], s[6:7], 0, v[138:139]
	v_lshl_add_u64 v[146:147], v[146:147], 0, s[18:19]
	s_mov_b32 m0, s80
	v_mov_b32_e32 v138, v152
	global_load_lds_dwordx4 v[146:147], off
	s_add_i32 m0, s80, 0x2000
	s_nop 0
	v_lshl_add_u64 v[146:147], s[6:7], 0, v[138:139]
	s_add_u32 s6, s6, 0x80080
	v_lshl_add_u64 v[146:147], v[146:147], 0, s[18:19]
	s_addc_u32 s7, s7, 0
	v_mov_b32_e32 v138, v150
	s_add_i32 s80, s83, s37
	global_load_lds_dwordx4 v[146:147], off
	s_mov_b32 m0, s80
	s_nop 0
	global_load_lds_dwordx4 v138, s[6:7]
	v_mov_b32_e32 v138, v152
	s_add_i32 m0, s80, 0x2000
	s_nop 0
	global_load_lds_dwordx4 v138, s[6:7]
	v_mov_b32_e32 v138, v149
	s_mov_b32 m0, s67
	v_lshl_add_u64 v[146:147], s[4:5], 0, v[138:139]
	v_lshl_add_u64 v[146:147], v[146:147], 0, s[18:19]
	v_mov_b32_e32 v138, v151
	global_load_lds_dwordx4 v[146:147], off
	s_mov_b32 m0, s68
	v_lshl_add_u64 v[146:147], s[4:5], 0, v[138:139]
	v_lshl_add_u64 v[146:147], v[146:147], 0, s[18:19]
	global_load_lds_dwordx4 v[146:147], off
	s_waitcnt vmcnt(8)
	s_waitcnt lgkmcnt(0)
	s_barrier
	s_waitcnt lgkmcnt(0)
	v_mfma_f32_16x16x32_bf16 v[94:97], v[130:133], v[180:183], v[94:97]
	v_mfma_f32_16x16x32_bf16 v[90:93], v[142:145], v[180:183], v[90:93]
	v_mfma_f32_16x16x32_bf16 v[86:89], v[130:133], v[188:191], v[86:89]
	v_mfma_f32_16x16x32_bf16 v[82:85], v[142:145], v[188:191], v[82:85]
	v_mfma_f32_16x16x32_bf16 v[78:81], v[130:133], v[200:203], v[78:81]
	v_mfma_f32_16x16x32_bf16 v[74:77], v[142:145], v[200:203], v[74:77]
	v_mfma_f32_16x16x32_bf16 v[70:73], v[130:133], v[208:211], v[70:73]
	v_mfma_f32_16x16x32_bf16 v[66:69], v[142:145], v[208:211], v[66:69]
	v_mfma_f32_16x16x32_bf16 v[94:97], v[134:137], v[184:187], v[94:97]
	v_mfma_f32_16x16x32_bf16 v[90:93], v[160:163], v[184:187], v[90:93]
	v_mfma_f32_16x16x32_bf16 v[86:89], v[134:137], v[192:195], v[86:89]
	v_mfma_f32_16x16x32_bf16 v[82:85], v[160:163], v[192:195], v[82:85]
	v_mfma_f32_16x16x32_bf16 v[78:81], v[134:137], v[204:207], v[78:81]
	v_mfma_f32_16x16x32_bf16 v[74:77], v[160:163], v[204:207], v[74:77]
	v_mfma_f32_16x16x32_bf16 v[70:73], v[134:137], v[214:217], v[70:73]
	v_mfma_f32_16x16x32_bf16 v[66:69], v[160:163], v[214:217], v[66:69]
	v_mfma_f32_16x16x32_bf16 v[30:33], v[164:167], v[180:183], v[30:33]
	v_mfma_f32_16x16x32_bf16 v[26:29], v[172:175], v[180:183], v[26:29]
	v_mfma_f32_16x16x32_bf16 v[22:25], v[164:167], v[188:191], v[22:25]
	v_mfma_f32_16x16x32_bf16 v[18:21], v[172:175], v[188:191], v[18:21]
	v_mfma_f32_16x16x32_bf16 v[14:17], v[164:167], v[200:203], v[14:17]
	v_mfma_f32_16x16x32_bf16 v[10:13], v[172:175], v[200:203], v[10:13]
	v_mfma_f32_16x16x32_bf16 v[6:9], v[164:167], v[208:211], v[6:9]
	v_mfma_f32_16x16x32_bf16 v[2:5], v[172:175], v[208:211], v[2:5]
	v_mfma_f32_16x16x32_bf16 v[30:33], v[168:171], v[184:187], v[30:33]
	v_mfma_f32_16x16x32_bf16 v[26:29], v[176:179], v[184:187], v[26:29]
	v_mfma_f32_16x16x32_bf16 v[22:25], v[168:171], v[192:195], v[22:25]
	v_mfma_f32_16x16x32_bf16 v[18:21], v[176:179], v[192:195], v[18:21]
	v_mfma_f32_16x16x32_bf16 v[14:17], v[168:171], v[204:207], v[14:17]
	v_mfma_f32_16x16x32_bf16 v[10:13], v[176:179], v[204:207], v[10:13]
	v_mfma_f32_16x16x32_bf16 v[6:9], v[168:171], v[214:217], v[6:9]
	v_mfma_f32_16x16x32_bf16 v[2:5], v[176:179], v[214:217], v[2:5]
	s_barrier
	s_add_i32 s79, s79, 2
	s_add_u32 s0, s0, 0x100
	s_addc_u32 s1, s1, 0
	s_add_u32 s77, s77, 0x100
	s_addc_u32 s78, s78, 0
	s_cmp_gt_u32 s79, 29
	s_cbranch_scc0 .LBB5_917
	s_and_b64 vcc, exec, s[34:35]
	s_cbranch_vccz .LBB5_920
	s_barrier

; #define PG8_STAGE(bufoff, gbase, voff) do { _Pragma("unroll") for (int _i = 0; _i < 2; ++_i) { unsigned _vo = (voff)[_i]; asm volatile("" : "+v"(_vo)); \
;         __builtin_amdgcn_global_load_lds((const unsigned*)((const char*)(gbase) + _vo), (LAS unsigned*)(lds + (bufoff) + ldsw + _i * 8192), 16, 0, 0); } } while (0)
; #define PG8_STAGE_A(bufoff, gbase, h, go) do { if constexpr (Sched::GATHER) { PG8_STAGE(bufoff, gbase, go[h]); } else { PG8_STAGE(bufoff, (gbase) + (h) * hstep, voffA); } } while (0)
; #define PG8_LDA(dst, b, h) do { _Pragma("unroll") for (int m = 0; m < 4; ++m) _Pragma("unroll") for (int k = 0; k < 2; ++k) dst[m][k] = *(const LAS bf16x8*)(lds + PG8_SA(b, h) + aoff + m * 2048 + k * 1024); } while (0)
; #define PG8_LDB(dst, b, h) do { _Pragma("unroll") for (int n = 0; n < 2; ++n) _Pragma("unroll") for (int k = 0; k < 2; ++k) dst[n][k] = *(const LAS bf16x8*)(lds + PG8_SB(b, h) + boff + n * 2048 + k * 1024); } while (0)
; #define PG8_WAIT_V(n) asm volatile("s_waitcnt vmcnt(" #n ")" ::: "memory")
; #define PG8_WAIT_L(n) asm volatile("s_waitcnt lgkmcnt(" #n ")" ::: "memory")
; #define PG8_BAR __builtin_amdgcn_s_barrier()
;     ...
;         for (int t = 0; t < nt; t += 2) {
;             const bool last = (t == nt - 2);
;             if constexpr (Epi::MIDK) { if (t == nt / 2) { int fr_e = fr; asm volatile("" : "+v"(fr_e)); E.midk(acc, cur, wr, fr_e); } }
;             const char* a1 = cA + (size_t)(t + 1) * kstep;
;             const char* a2 = last ? nA : cA + (size_t)(t + 2) * kstep; const char* b2 = last ? nB : cB + (size_t)(t + 2) * kstep;
;             const char* a3 = a2 + kstep; const char* b3 = b2 + kstep;
;             PG8_LDB(B0, 0, 0); PG8_LDB(B1, 0, 1); PG8_SCHED; PG8_LDA(At, 0, 0); PG8_STAGE_A(PG8_SA(1, 1), a1, 1, gc);
;             if constexpr (Sched::GATHER) { if (last) {
; #pragma unroll
;                 for (int h = 0; h < 2; ++h)
; #pragma unroll
;                     for (int i = 0; i < 2; ++i) gc[h][i] = gn[h][i]; } }
;             PG8_WAIT_V(8); PG8_WAIT_L(0); PG8_BAR; PG8_MMA(0, 0, At, B0); PG8_MMA(0, 1, At, B1); PG8_BAR; PG8_SCHED;
;             PG8_LDA(At, 0, 1); PG8_STAGE(PG8_SB(0, 0), b2, voffB); PG8_STAGE(PG8_SB(0, 1), b2 + hstep, voffB); PG8_STAGE_A(PG8_SA(0, 0), a2, 0, gc);
;             PG8_WAIT_V(8); PG8_WAIT_L(0); PG8_BAR; PG8_MMA(1, 0, At, B0); PG8_MMA(1, 1, At, B1); PG8_BAR; PG8_SCHED;
.LBB5_1164:
	v_add_u32_e32 v2, s66, v186
	ds_read_b128 v[134:137], v2
	ds_read_b128 v[138:141], v2 offset:1024
	ds_read_b128 v[142:145], v2 offset:2048
	ds_read_b128 v[146:149], v2 offset:3072
	v_add_u32_e32 v2, s67, v186
	s_add_u32 s74, s46, s48
	ds_read_b128 v[150:153], v2
	ds_read_b128 v[154:157], v2 offset:1024
	ds_read_b128 v[160:163], v2 offset:2048
	ds_read_b128 v[164:167], v2 offset:3072
	s_addc_u32 s75, s47, s49
	s_add_u32 s50, s74, 0x100
	s_addc_u32 s51, s75, 0
	s_add_u32 s52, s70, s48
	s_addc_u32 s53, s71, s49
	s_cmpk_eq_i32 s48, 0xf00
	s_cselect_b32 s51, s41, s51
	s_cselect_b32 s50, s40, s50
	s_cselect_b32 s53, s45, s53
	s_cselect_b32 s52, s44, s52
	v_mov_b32_e32 v2, v1
	ds_read_b128 v[168:171], v187
	ds_read_b128 v[172:175], v187 offset:1024
	ds_read_b128 v[176:179], v187 offset:2048
	ds_read_b128 v[190:193], v187 offset:3072
	ds_read_b128 v[194:197], v187 offset:4096
	ds_read_b128 v[200:203], v187 offset:5120
	ds_read_b128 v[204:207], v187 offset:6144
	ds_read_b128 v[208:211], v187 offset:7168
	s_add_i32 m0, s55, 0xc000
	v_lshl_add_u64 v[4:5], s[74:75], 0, v[2:3]
	v_lshl_add_u64 v[4:5], v[4:5], 0, s[34:35]
	v_mov_b32_e32 v2, v181
	global_load_lds_dwordx4 v[4:5], off
	s_add_i32 m0, s55, 0xe000
	v_lshl_add_u64 v[4:5], s[74:75], 0, v[2:3]
	v_lshl_add_u64 v[4:5], v[4:5], 0, s[34:35]
	global_load_lds_dwordx4 v[4:5], off
	s_waitcnt vmcnt(8)
	s_waitcnt lgkmcnt(0)
	s_barrier
	s_waitcnt lgkmcnt(0)
	v_mfma_f32_16x16x32_bf16 v[130:133], v[134:137], v[168:171], v[130:133]
	v_mfma_f32_16x16x32_bf16 v[126:129], v[142:145], v[168:171], v[126:129]
	v_mfma_f32_16x16x32_bf16 v[114:117], v[134:137], v[176:179], v[114:117]
	v_mfma_f32_16x16x32_bf16 v[110:113], v[142:145], v[176:179], v[110:113]
	v_mfma_f32_16x16x32_bf16 v[98:101], v[134:137], v[194:197], v[98:101]
	v_mfma_f32_16x16x32_bf16 v[94:97], v[142:145], v[194:197], v[94:97]
	v_mfma_f32_16x16x32_bf16 v[82:85], v[134:137], v[204:207], v[82:85]
	v_mfma_f32_16x16x32_bf16 v[78:81], v[142:145], v[204:207], v[78:81]
	v_mfma_f32_16x16x32_bf16 v[130:133], v[138:141], v[172:175], v[130:133]
	v_mfma_f32_16x16x32_bf16 v[126:129], v[146:149], v[172:175], v[126:129]
	v_mfma_f32_16x16x32_bf16 v[114:117], v[138:141], v[190:193], v[114:117]
	v_mfma_f32_16x16x32_bf16 v[110:113], v[146:149], v[190:193], v[110:113]
	v_mfma_f32_16x16x32_bf16 v[98:101], v[138:141], v[200:203], v[98:101]
	v_mfma_f32_16x16x32_bf16 v[94:97], v[146:149], v[200:203], v[94:97]
	v_mfma_f32_16x16x32_bf16 v[82:85], v[138:141], v[208:211], v[82:85]
	v_mfma_f32_16x16x32_bf16 v[78:81], v[146:149], v[208:211], v[78:81]
	v_mfma_f32_16x16x32_bf16 v[122:125], v[150:153], v[168:171], v[122:125]
	v_mfma_f32_16x16x32_bf16 v[118:121], v[160:163], v[168:171], v[118:121]
	v_mfma_f32_16x16x32_bf16 v[106:109], v[150:153], v[176:179], v[106:109]
	v_mfma_f32_16x16x32_bf16 v[102:105], v[160:163], v[176:179], v[102:105]
	v_mfma_f32_16x16x32_bf16 v[90:93], v[150:153], v[194:197], v[90:93]
	v_mfma_f32_16x16x32_bf16 v[86:89], v[160:163], v[194:197], v[86:89]
	v_mfma_f32_16x16x32_bf16 v[74:77], v[150:153], v[204:207], v[74:77]
	v_mfma_f32_16x16x32_bf16 v[70:73], v[160:163], v[204:207], v[70:73]
	v_mfma_f32_16x16x32_bf16 v[122:125], v[154:157], v[172:175], v[122:125]
	v_mfma_f32_16x16x32_bf16 v[118:121], v[164:167], v[172:175], v[118:121]
	v_mfma_f32_16x16x32_bf16 v[106:109], v[154:157], v[190:193], v[106:109]
	v_mfma_f32_16x16x32_bf16 v[102:105], v[164:167], v[190:193], v[102:105]
	v_mfma_f32_16x16x32_bf16 v[90:93], v[154:157], v[200:203], v[90:93]
	v_mfma_f32_16x16x32_bf16 v[86:89], v[164:167], v[200:203], v[86:89]
	v_mfma_f32_16x16x32_bf16 v[74:77], v[154:157], v[208:211], v[74:77]
	v_mfma_f32_16x16x32_bf16 v[70:73], v[164:167], v[208:211], v[70:73]
	s_barrier
	v_mov_b32_e32 v2, v180
	s_add_i32 s73, s66, s54
	ds_read_b128 v[168:171], v187 offset:16384
	ds_read_b128 v[172:175], v187 offset:17408
	ds_read_b128 v[176:179], v187 offset:18432
	ds_read_b128 v[190:193], v187 offset:19456
	ds_read_b128 v[194:197], v187 offset:20480
	ds_read_b128 v[200:203], v187 offset:21504
	ds_read_b128 v[204:207], v187 offset:22528
	ds_read_b128 v[208:211], v187 offset:23552
	s_mov_b32 m0, s73
	s_nop 0
	global_load_lds_dwordx4 v2, s[52:53]
	v_mov_b32_e32 v2, v182
	s_add_i32 m0, s73, 0x2000
	s_add_u32 s74, s52, 0x80000
	global_load_lds_dwordx4 v2, s[52:53]
	s_addc_u32 s75, s53, 0
	v_mov_b32_e32 v2, v180
	s_add_i32 s73, s67, s54
	s_mov_b32 m0, s73
	s_nop 0
	global_load_lds_dwordx4 v2, s[74:75]
	v_mov_b32_e32 v2, v182
	s_add_i32 m0, s73, 0x2000
	s_nop 0
	global_load_lds_dwordx4 v2, s[74:75]
	v_mov_b32_e32 v2, v1
	s_mov_b32 m0, s55
	s_nop 0
	global_load_lds_dwordx4 v2, s[50:51]
	v_mov_b32_e32 v2, v181
	s_mov_b32 m0, s56
	s_nop 0
	global_load_lds_dwordx4 v2, s[50:51]
	s_waitcnt vmcnt(8)
	s_waitcnt lgkmcnt(0)
	s_barrier
; #define PG8_STAGE(bufoff, gbase, voff) do { _Pragma("unroll") for (int _i = 0; _i < 2; ++_i) { unsigned _vo = (voff)[_i]; asm volatile("" : "+v"(_vo)); \
;         __builtin_amdgcn_global_load_lds((const unsigned*)((const char*)(gbase) + _vo), (LAS unsigned*)(lds + (bufoff) + ldsw + _i * 8192), 16, 0, 0); } } while (0)
; #define PG8_STAGE_A(bufoff, gbase, h, go) do { if constexpr (Sched::GATHER) { PG8_STAGE(bufoff, gbase, go[h]); } else { PG8_STAGE(bufoff, (gbase) + (h) * hstep, voffA); } } while (0)
; #define PG8_LDA(dst, b, h) do { _Pragma("unroll") for (int m = 0; m < 4; ++m) _Pragma("unroll") for (int k = 0; k < 2; ++k) dst[m][k] = *(const LAS bf16x8*)(lds + PG8_SA(b, h) + aoff + m * 2048 + k * 1024); } while (0)
; #define PG8_LDB(dst, b, h) do { _Pragma("unroll") for (int n = 0; n < 2; ++n) _Pragma("unroll") for (int k = 0; k < 2; ++k) dst[n][k] = *(const LAS bf16x8*)(lds + PG8_SB(b, h) + boff + n * 2048 + k * 1024); } while (0)
; #define PG8_WAIT_V(n) asm volatile("s_waitcnt vmcnt(" #n ")" ::: "memory")
; #define PG8_WAIT_L(n) asm volatile("s_waitcnt lgkmcnt(" #n ")" ::: "memory")
; #define PG8_BAR __builtin_amdgcn_s_barrier()
; #define PG8_SCHED __builtin_amdgcn_sched_barrier(0)
;     ...
;             PG8_WAIT_V(8); PG8_WAIT_L(0); PG8_BAR; PG8_MMA(0, 0, At, B0); PG8_MMA(0, 1, At, B1); PG8_BAR; PG8_SCHED;
;             PG8_LDA(At, 0, 1); PG8_STAGE(PG8_SB(0, 0), b2, voffB); PG8_STAGE(PG8_SB(0, 1), b2 + hstep, voffB); PG8_STAGE_A(PG8_SA(0, 0), a2, 0, gc);
;             PG8_WAIT_V(8); PG8_WAIT_L(0); PG8_BAR; PG8_MMA(1, 0, At, B0); PG8_MMA(1, 1, At, B1); PG8_BAR; PG8_SCHED;
;             PG8_LDB(B0, 1, 0); PG8_LDB(B1, 1, 1); PG8_SCHED; PG8_LDA(At, 1, 0); PG8_STAGE_A(PG8_SA(0, 1), a2, 1, gc);
;             PG8_WAIT_V(8); PG8_WAIT_L(0); PG8_BAR; PG8_MMA(0, 0, At, B0); PG8_MMA(0, 1, At, B1); PG8_BAR; PG8_SCHED;
	s_waitcnt lgkmcnt(0)
	v_mfma_f32_16x16x32_bf16 v[66:69], v[134:137], v[168:171], v[66:69]
	v_mfma_f32_16x16x32_bf16 v[62:65], v[142:145], v[168:171], v[62:65]
	v_mfma_f32_16x16x32_bf16 v[50:53], v[134:137], v[176:179], v[50:53]
	v_mfma_f32_16x16x32_bf16 v[46:49], v[142:145], v[176:179], v[46:49]
	v_mfma_f32_16x16x32_bf16 v[34:37], v[134:137], v[194:197], v[34:37]
	v_mfma_f32_16x16x32_bf16 v[30:33], v[142:145], v[194:197], v[30:33]
	v_mfma_f32_16x16x32_bf16 v[18:21], v[134:137], v[204:207], v[18:21]
	v_mfma_f32_16x16x32_bf16 v[14:17], v[142:145], v[204:207], v[14:17]
	v_mfma_f32_16x16x32_bf16 v[66:69], v[138:141], v[172:175], v[66:69]
	v_mfma_f32_16x16x32_bf16 v[62:65], v[146:149], v[172:175], v[62:65]
	v_mfma_f32_16x16x32_bf16 v[50:53], v[138:141], v[190:193], v[50:53]
	v_mfma_f32_16x16x32_bf16 v[46:49], v[146:149], v[190:193], v[46:49]
	v_mfma_f32_16x16x32_bf16 v[34:37], v[138:141], v[200:203], v[34:37]
	v_mfma_f32_16x16x32_bf16 v[30:33], v[146:149], v[200:203], v[30:33]
	v_mfma_f32_16x16x32_bf16 v[18:21], v[138:141], v[208:211], v[18:21]
	v_mfma_f32_16x16x32_bf16 v[14:17], v[146:149], v[208:211], v[14:17]
	v_mfma_f32_16x16x32_bf16 v[58:61], v[150:153], v[168:171], v[58:61]
	v_mfma_f32_16x16x32_bf16 v[54:57], v[160:163], v[168:171], v[54:57]
	v_mfma_f32_16x16x32_bf16 v[42:45], v[150:153], v[176:179], v[42:45]
	v_mfma_f32_16x16x32_bf16 v[38:41], v[160:163], v[176:179], v[38:41]
	v_mfma_f32_16x16x32_bf16 v[26:29], v[150:153], v[194:197], v[26:29]
	v_mfma_f32_16x16x32_bf16 v[22:25], v[160:163], v[194:197], v[22:25]
	v_mfma_f32_16x16x32_bf16 v[10:13], v[150:153], v[204:207], v[10:13]
	v_mfma_f32_16x16x32_bf16 v[4:7], v[160:163], v[204:207], v[6:9]
	v_mfma_f32_16x16x32_bf16 v[58:61], v[154:157], v[172:175], v[58:61]
	v_mfma_f32_16x16x32_bf16 v[54:57], v[164:167], v[172:175], v[54:57]
	v_mfma_f32_16x16x32_bf16 v[42:45], v[154:157], v[190:193], v[42:45]
	v_mfma_f32_16x16x32_bf16 v[38:41], v[164:167], v[190:193], v[38:41]
	v_mfma_f32_16x16x32_bf16 v[26:29], v[154:157], v[200:203], v[26:29]
	v_mfma_f32_16x16x32_bf16 v[22:25], v[164:167], v[200:203], v[22:25]
	v_mfma_f32_16x16x32_bf16 v[10:13], v[154:157], v[208:211], v[10:13]
	v_mfma_f32_16x16x32_bf16 v[4:7], v[164:167], v[208:211], v[4:7]
	s_barrier
	s_add_i32 s73, 0, 0x18000
	v_add_u32_e32 v2, s73, v186
	s_add_i32 s76, 0, 0x1c000
	ds_read_b128 v[134:137], v2
	ds_read_b128 v[138:141], v2 offset:1024
	ds_read_b128 v[142:145], v2 offset:2048
	ds_read_b128 v[146:149], v2 offset:3072
	v_add_u32_e32 v2, s76, v186
	ds_read_b128 v[150:153], v2
	ds_read_b128 v[154:157], v2 offset:1024
	ds_read_b128 v[160:163], v2 offset:2048
	ds_read_b128 v[164:167], v2 offset:3072
	s_add_u32 s74, s50, 0x80000
	v_mov_b32_e32 v2, v1
	s_mov_b32 m0, s57
	ds_read_b128 v[168:171], v187 offset:32768
	ds_read_b128 v[172:175], v187 offset:33792
	ds_read_b128 v[176:179], v187 offset:34816
	ds_read_b128 v[190:193], v187 offset:35840
	ds_read_b128 v[194:197], v187 offset:36864
	ds_read_b128 v[200:203], v187 offset:37888
	ds_read_b128 v[204:207], v187 offset:38912
	ds_read_b128 v[208:211], v187 offset:39936
	s_addc_u32 s75, s51, 0
	s_nop 0
	global_load_lds_dwordx4 v2, s[74:75]
	v_mov_b32_e32 v2, v181
	s_mov_b32 m0, s58
	s_nop 0
	global_load_lds_dwordx4 v2, s[74:75]
	s_waitcnt vmcnt(8)
	s_waitcnt lgkmcnt(0)
	s_barrier
	s_waitcnt lgkmcnt(0)
	v_mfma_f32_16x16x32_bf16 v[130:133], v[134:137], v[168:171], v[130:133]
	v_mfma_f32_16x16x32_bf16 v[126:129], v[142:145], v[168:171], v[126:129]
	v_mfma_f32_16x16x32_bf16 v[114:117], v[134:137], v[176:179], v[114:117]
	v_mfma_f32_16x16x32_bf16 v[110:113], v[142:145], v[176:179], v[110:113]
	v_mfma_f32_16x16x32_bf16 v[98:101], v[134:137], v[194:197], v[98:101]
	v_mfma_f32_16x16x32_bf16 v[94:97], v[142:145], v[194:197], v[94:97]
	v_mfma_f32_16x16x32_bf16 v[82:85], v[134:137], v[204:207], v[82:85]
	v_mfma_f32_16x16x32_bf16 v[78:81], v[142:145], v[204:207], v[78:81]
	v_mfma_f32_16x16x32_bf16 v[130:133], v[138:141], v[172:175], v[130:133]
	v_mfma_f32_16x16x32_bf16 v[126:129], v[146:149], v[172:175], v[126:129]
	v_mfma_f32_16x16x32_bf16 v[114:117], v[138:141], v[190:193], v[114:117]
	v_mfma_f32_16x16x32_bf16 v[110:113], v[146:149], v[190:193], v[110:113]
	v_mfma_f32_16x16x32_bf16 v[98:101], v[138:141], v[200:203], v[98:101]
	v_mfma_f32_16x16x32_bf16 v[94:97], v[146:149], v[200:203], v[94:97]
	v_mfma_f32_16x16x32_bf16 v[82:85], v[138:141], v[208:211], v[82:85]
	v_mfma_f32_16x16x32_bf16 v[78:81], v[146:149], v[208:211], v[78:81]
	v_mfma_f32_16x16x32_bf16 v[122:125], v[150:153], v[168:171], v[122:125]
	v_mfma_f32_16x16x32_bf16 v[118:121], v[160:163], v[168:171], v[118:121]
	v_mfma_f32_16x16x32_bf16 v[106:109], v[150:153], v[176:179], v[106:109]
	v_mfma_f32_16x16x32_bf16 v[102:105], v[160:163], v[176:179], v[102:105]
	v_mfma_f32_16x16x32_bf16 v[90:93], v[150:153], v[194:197], v[90:93]
	v_mfma_f32_16x16x32_bf16 v[86:89], v[160:163], v[194:197], v[86:89]
	v_mfma_f32_16x16x32_bf16 v[74:77], v[150:153], v[204:207], v[74:77]
	v_mfma_f32_16x16x32_bf16 v[70:73], v[160:163], v[204:207], v[70:73]
	v_mfma_f32_16x16x32_bf16 v[122:125], v[154:157], v[172:175], v[122:125]
	v_mfma_f32_16x16x32_bf16 v[118:121], v[164:167], v[172:175], v[118:121]
	v_mfma_f32_16x16x32_bf16 v[106:109], v[154:157], v[190:193], v[106:109]
	v_mfma_f32_16x16x32_bf16 v[102:105], v[164:167], v[190:193], v[102:105]
	v_mfma_f32_16x16x32_bf16 v[90:93], v[154:157], v[200:203], v[90:93]
	v_mfma_f32_16x16x32_bf16 v[86:89], v[164:167], v[200:203], v[86:89]
	v_mfma_f32_16x16x32_bf16 v[74:77], v[154:157], v[208:211], v[74:77]
	v_mfma_f32_16x16x32_bf16 v[70:73], v[164:167], v[208:211], v[70:73]
	s_barrier
; #define PG8_STAGE(bufoff, gbase, voff) do { _Pragma("unroll") for (int _i = 0; _i < 2; ++_i) { unsigned _vo = (voff)[_i]; asm volatile("" : "+v"(_vo)); \
;         __builtin_amdgcn_global_load_lds((const unsigned*)((const char*)(gbase) + _vo), (LAS unsigned*)(lds + (bufoff) + ldsw + _i * 8192), 16, 0, 0); } } while (0)
; #define PG8_STAGE_A(bufoff, gbase, h, go) do { if constexpr (Sched::GATHER) { PG8_STAGE(bufoff, gbase, go[h]); } else { PG8_STAGE(bufoff, (gbase) + (h) * hstep, voffA); } } while (0)
; #define PG8_LDA(dst, b, h) do { _Pragma("unroll") for (int m = 0; m < 4; ++m) _Pragma("unroll") for (int k = 0; k < 2; ++k) dst[m][k] = *(const LAS bf16x8*)(lds + PG8_SA(b, h) + aoff + m * 2048 + k * 1024); } while (0)
; #define PG8_WAIT_V(n) asm volatile("s_waitcnt vmcnt(" #n ")" ::: "memory")
; #define PG8_WAIT_L(n) asm volatile("s_waitcnt lgkmcnt(" #n ")" ::: "memory")
; #define PG8_BAR __builtin_amdgcn_s_barrier()
; #define PG8_SCHED __builtin_amdgcn_sched_barrier(0)
;     ...
;             PG8_LDA(At, 1, 1); PG8_STAGE(PG8_SB(1, 0), b3, voffB); PG8_STAGE(PG8_SB(1, 1), b3 + hstep, voffB); PG8_STAGE_A(PG8_SA(1, 0), a3, 0, gc);
;             PG8_WAIT_V(8); PG8_WAIT_L(0); PG8_BAR; PG8_MMA(1, 0, At, B0); PG8_MMA(1, 1, At, B1); PG8_BAR; PG8_SCHED;
	v_mov_b32_e32 v2, v180
	ds_read_b128 v[168:171], v187 offset:49152
	ds_read_b128 v[172:175], v187 offset:50176
	ds_read_b128 v[176:179], v187 offset:51200
	ds_read_b128 v[190:193], v187 offset:52224
	ds_read_b128 v[194:197], v187 offset:53248
	ds_read_b128 v[200:203], v187 offset:54272
	ds_read_b128 v[204:207], v187 offset:55296
	ds_read_b128 v[208:211], v187 offset:56320
	s_add_i32 s73, s73, s54
	v_lshl_add_u64 v[8:9], s[52:53], 0, v[2:3]
	v_lshl_add_u64 v[8:9], v[8:9], 0, s[18:19]
	s_mov_b32 m0, s73
	v_mov_b32_e32 v2, v182
	global_load_lds_dwordx4 v[8:9], off
	s_add_i32 m0, s73, 0x2000
	s_nop 0
	v_lshl_add_u64 v[8:9], s[52:53], 0, v[2:3]
	s_add_u32 s52, s52, 0x80080
	v_lshl_add_u64 v[8:9], v[8:9], 0, s[18:19]
	s_addc_u32 s53, s53, 0
	v_mov_b32_e32 v2, v180
	s_add_i32 s73, s76, s54
	global_load_lds_dwordx4 v[8:9], off
	s_mov_b32 m0, s73
	s_nop 0
	global_load_lds_dwordx4 v2, s[52:53]
	v_mov_b32_e32 v2, v182
	s_add_i32 m0, s73, 0x2000
	s_nop 0
	global_load_lds_dwordx4 v2, s[52:53]
	v_mov_b32_e32 v2, v1
	s_mov_b32 m0, s62
	v_lshl_add_u64 v[8:9], s[50:51], 0, v[2:3]
	v_lshl_add_u64 v[8:9], v[8:9], 0, s[18:19]
	v_mov_b32_e32 v2, v181
	global_load_lds_dwordx4 v[8:9], off
	s_mov_b32 m0, s63
	v_lshl_add_u64 v[8:9], s[50:51], 0, v[2:3]
	v_lshl_add_u64 v[8:9], v[8:9], 0, s[18:19]
	global_load_lds_dwordx4 v[8:9], off
	s_waitcnt vmcnt(8)
	s_waitcnt lgkmcnt(0)
	s_barrier
	s_waitcnt lgkmcnt(0)
	v_mfma_f32_16x16x32_bf16 v[66:69], v[134:137], v[168:171], v[66:69]
	v_mfma_f32_16x16x32_bf16 v[62:65], v[142:145], v[168:171], v[62:65]
	v_mfma_f32_16x16x32_bf16 v[50:53], v[134:137], v[176:179], v[50:53]
	v_mfma_f32_16x16x32_bf16 v[46:49], v[142:145], v[176:179], v[46:49]
	v_mfma_f32_16x16x32_bf16 v[34:37], v[134:137], v[194:197], v[34:37]
	v_mfma_f32_16x16x32_bf16 v[30:33], v[142:145], v[194:197], v[30:33]
	v_mfma_f32_16x16x32_bf16 v[18:21], v[134:137], v[204:207], v[18:21]
	v_mfma_f32_16x16x32_bf16 v[14:17], v[142:145], v[204:207], v[14:17]
	v_mfma_f32_16x16x32_bf16 v[66:69], v[138:141], v[172:175], v[66:69]
	v_mfma_f32_16x16x32_bf16 v[62:65], v[146:149], v[172:175], v[62:65]
	v_mfma_f32_16x16x32_bf16 v[50:53], v[138:141], v[190:193], v[50:53]
	v_mfma_f32_16x16x32_bf16 v[46:49], v[146:149], v[190:193], v[46:49]
	v_mfma_f32_16x16x32_bf16 v[34:37], v[138:141], v[200:203], v[34:37]
	v_mfma_f32_16x16x32_bf16 v[30:33], v[146:149], v[200:203], v[30:33]
	v_mfma_f32_16x16x32_bf16 v[18:21], v[138:141], v[208:211], v[18:21]
	v_mfma_f32_16x16x32_bf16 v[14:17], v[146:149], v[208:211], v[14:17]
	v_mfma_f32_16x16x32_bf16 v[58:61], v[150:153], v[168:171], v[58:61]
	v_mfma_f32_16x16x32_bf16 v[54:57], v[160:163], v[168:171], v[54:57]
	v_mfma_f32_16x16x32_bf16 v[42:45], v[150:153], v[176:179], v[42:45]
	v_mfma_f32_16x16x32_bf16 v[38:41], v[160:163], v[176:179], v[38:41]
	v_mfma_f32_16x16x32_bf16 v[26:29], v[150:153], v[194:197], v[26:29]
	v_mfma_f32_16x16x32_bf16 v[22:25], v[160:163], v[194:197], v[22:25]
	v_mfma_f32_16x16x32_bf16 v[8:11], v[150:153], v[204:207], v[10:13]
	v_mfma_f32_16x16x32_bf16 v[4:7], v[160:163], v[204:207], v[4:7]
	v_mfma_f32_16x16x32_bf16 v[58:61], v[154:157], v[172:175], v[58:61]
	v_mfma_f32_16x16x32_bf16 v[54:57], v[164:167], v[172:175], v[54:57]
	v_mfma_f32_16x16x32_bf16 v[42:45], v[154:157], v[190:193], v[42:45]
	v_mfma_f32_16x16x32_bf16 v[38:41], v[164:167], v[190:193], v[38:41]
	v_mfma_f32_16x16x32_bf16 v[26:29], v[154:157], v[200:203], v[26:29]
	v_mfma_f32_16x16x32_bf16 v[22:25], v[164:167], v[200:203], v[22:25]
	v_mfma_f32_16x16x32_bf16 v[10:13], v[154:157], v[208:211], v[8:11]
	v_mfma_f32_16x16x32_bf16 v[6:9], v[164:167], v[208:211], v[4:7]
	s_barrier
	s_add_i32 s72, s72, 2
	s_add_u32 s48, s48, 0x100
	s_addc_u32 s49, s49, 0
	s_cmp_gt_u32 s72, 29
	s_cbranch_scc1 .LBB5_1167

; #define PG8_STAGE(bufoff, gbase, voff) do { _Pragma("unroll") for (int _i = 0; _i < 2; ++_i) { unsigned _vo = (voff)[_i]; asm volatile("" : "+v"(_vo)); \
;         __builtin_amdgcn_global_load_lds((const unsigned*)((const char*)(gbase) + _vo), (LAS unsigned*)(lds + (bufoff) + ldsw + _i * 8192), 16, 0, 0); } } while (0)
; #define PG8_STAGE_A(bufoff, gbase, h, go) do { if constexpr (Sched::GATHER) { PG8_STAGE(bufoff, gbase, go[h]); } else { PG8_STAGE(bufoff, (gbase) + (h) * hstep, voffA); } } while (0)
; #define PG8_LDA(dst, b, h) do { _Pragma("unroll") for (int m = 0; m < 4; ++m) _Pragma("unroll") for (int k = 0; k < 2; ++k) dst[m][k] = *(const LAS bf16x8*)(lds + PG8_SA(b, h) + aoff + m * 2048 + k * 1024); } while (0)
; #define PG8_LDB(dst, b, h) do { _Pragma("unroll") for (int n = 0; n < 2; ++n) _Pragma("unroll") for (int k = 0; k < 2; ++k) dst[n][k] = *(const LAS bf16x8*)(lds + PG8_SB(b, h) + boff + n * 2048 + k * 1024); } while (0)
; #define PG8_WAIT_V(n) asm volatile("s_waitcnt vmcnt(" #n ")" ::: "memory")
; #define PG8_WAIT_L(n) asm volatile("s_waitcnt lgkmcnt(" #n ")" ::: "memory")
; #define PG8_BAR __builtin_amdgcn_s_barrier()
;     ...
;         for (int t = 0; t < nt; t += 2) {
;             const bool last = (t == nt - 2);
;             if constexpr (Epi::MIDK) { if (t == nt / 2) { int fr_e = fr; asm volatile("" : "+v"(fr_e)); E.midk(acc, cur, wr, fr_e); } }
;             const char* a1 = cA + (size_t)(t + 1) * kstep;
;             const char* a2 = last ? nA : cA + (size_t)(t + 2) * kstep; const char* b2 = last ? nB : cB + (size_t)(t + 2) * kstep;
;             const char* a3 = a2 + kstep; const char* b3 = b2 + kstep;
;             PG8_LDB(B0, 0, 0); PG8_LDB(B1, 0, 1); PG8_SCHED; PG8_LDA(At, 0, 0); PG8_STAGE_A(PG8_SA(1, 1), a1, 1, gc);
;             if constexpr (Sched::GATHER) { if (last) {
; #pragma unroll
;                 for (int h = 0; h < 2; ++h)
; #pragma unroll
;                     for (int i = 0; i < 2; ++i) gc[h][i] = gn[h][i]; } }
;             PG8_WAIT_V(8); PG8_WAIT_L(0); PG8_BAR; PG8_MMA(0, 0, At, B0); PG8_MMA(0, 1, At, B1); PG8_BAR; PG8_SCHED;
;             PG8_LDA(At, 0, 1); PG8_STAGE(PG8_SB(0, 0), b2, voffB); PG8_STAGE(PG8_SB(0, 1), b2 + hstep, voffB); PG8_STAGE_A(PG8_SA(0, 0), a2, 0, gc);
;             PG8_WAIT_V(8); PG8_WAIT_L(0); PG8_BAR; PG8_MMA(1, 0, At, B0); PG8_MMA(1, 1, At, B1); PG8_BAR; PG8_SCHED;
.LBB5_1259:
	ds_read_b128 v[132:135], v145
	ds_read_b128 v[150:153], v145 offset:1024
	ds_read_b128 v[154:157], v145 offset:2048
	ds_read_b128 v[158:161], v145 offset:3072
	ds_read_b128 v[162:165], v146
	ds_read_b128 v[166:169], v146 offset:1024
	ds_read_b128 v[170:173], v146 offset:2048
	ds_read_b128 v[174:177], v146 offset:3072
	s_add_u32 s44, s42, 0xfff80080
	s_addc_u32 s45, s43, -1
	s_cmp_eq_u32 s65, 28
	s_cselect_b32 s45, s35, s45
	s_cselect_b32 s44, s34, s44
	s_cselect_b32 s47, s37, s64
	s_cselect_b32 s46, s36, s63
	v_mov_b32_e32 v130, v1
	ds_read_b128 v[178:181], v147
	ds_read_b128 v[182:185], v147 offset:1024
	ds_read_b128 v[186:189], v147 offset:2048
	ds_read_b128 v[190:193], v147 offset:3072
	ds_read_b128 v[194:197], v147 offset:4096
	ds_read_b128 v[200:203], v147 offset:5120
	ds_read_b128 v[204:207], v147 offset:6144
	ds_read_b128 v[208:211], v147 offset:7168
	s_add_i32 m0, s41, 0xc000
	s_nop 0
	global_load_lds_dwordx4 v130, s[42:43]
	v_mov_b32_e32 v130, v139
	s_add_i32 m0, s41, 0xe000
	s_nop 0
	global_load_lds_dwordx4 v130, s[42:43]
	s_waitcnt vmcnt(8)
	s_waitcnt lgkmcnt(0)
	s_barrier
	s_waitcnt lgkmcnt(0)
	v_mfma_f32_16x16x32_bf16 v[126:129], v[132:135], v[178:181], v[126:129]
	v_mfma_f32_16x16x32_bf16 v[122:125], v[154:157], v[178:181], v[122:125]
	v_mfma_f32_16x16x32_bf16 v[114:117], v[132:135], v[186:189], v[114:117]
	v_mfma_f32_16x16x32_bf16 v[106:109], v[154:157], v[186:189], v[106:109]
	v_mfma_f32_16x16x32_bf16 v[98:101], v[132:135], v[194:197], v[98:101]
	v_mfma_f32_16x16x32_bf16 v[90:93], v[154:157], v[194:197], v[90:93]
	v_mfma_f32_16x16x32_bf16 v[82:85], v[132:135], v[204:207], v[82:85]
	v_mfma_f32_16x16x32_bf16 v[74:77], v[154:157], v[204:207], v[74:77]
	v_mfma_f32_16x16x32_bf16 v[126:129], v[150:153], v[182:185], v[126:129]
	v_mfma_f32_16x16x32_bf16 v[122:125], v[158:161], v[182:185], v[122:125]
	v_mfma_f32_16x16x32_bf16 v[114:117], v[150:153], v[190:193], v[114:117]
	v_mfma_f32_16x16x32_bf16 v[106:109], v[158:161], v[190:193], v[106:109]
	v_mfma_f32_16x16x32_bf16 v[98:101], v[150:153], v[200:203], v[98:101]
	v_mfma_f32_16x16x32_bf16 v[90:93], v[158:161], v[200:203], v[90:93]
	v_mfma_f32_16x16x32_bf16 v[82:85], v[150:153], v[208:211], v[82:85]
	v_mfma_f32_16x16x32_bf16 v[74:77], v[158:161], v[208:211], v[74:77]
	v_mfma_f32_16x16x32_bf16 v[118:121], v[162:165], v[178:181], v[118:121]
	v_mfma_f32_16x16x32_bf16 v[110:113], v[170:173], v[178:181], v[110:113]
	v_mfma_f32_16x16x32_bf16 v[102:105], v[162:165], v[186:189], v[102:105]
	v_mfma_f32_16x16x32_bf16 v[94:97], v[170:173], v[186:189], v[94:97]
	v_mfma_f32_16x16x32_bf16 v[86:89], v[162:165], v[194:197], v[86:89]
	v_mfma_f32_16x16x32_bf16 v[78:81], v[170:173], v[194:197], v[78:81]
	v_mfma_f32_16x16x32_bf16 v[70:73], v[162:165], v[204:207], v[70:73]
	v_mfma_f32_16x16x32_bf16 v[66:69], v[170:173], v[204:207], v[66:69]
	v_mfma_f32_16x16x32_bf16 v[118:121], v[166:169], v[182:185], v[118:121]
	v_mfma_f32_16x16x32_bf16 v[110:113], v[174:177], v[182:185], v[110:113]
	v_mfma_f32_16x16x32_bf16 v[102:105], v[166:169], v[190:193], v[102:105]
	v_mfma_f32_16x16x32_bf16 v[94:97], v[174:177], v[190:193], v[94:97]
	v_mfma_f32_16x16x32_bf16 v[86:89], v[166:169], v[200:203], v[86:89]
	v_mfma_f32_16x16x32_bf16 v[78:81], v[174:177], v[200:203], v[78:81]
	v_mfma_f32_16x16x32_bf16 v[70:73], v[166:169], v[208:211], v[70:73]
	v_mfma_f32_16x16x32_bf16 v[66:69], v[174:177], v[208:211], v[66:69]
	s_barrier
	v_mov_b32_e32 v130, v138
	s_add_i32 s66, s56, s29
	ds_read_b128 v[178:181], v147 offset:16384
	ds_read_b128 v[182:185], v147 offset:17408
	ds_read_b128 v[186:189], v147 offset:18432
	ds_read_b128 v[190:193], v147 offset:19456
	ds_read_b128 v[194:197], v147 offset:20480
	ds_read_b128 v[200:203], v147 offset:21504
	ds_read_b128 v[204:207], v147 offset:22528
	ds_read_b128 v[208:211], v147 offset:23552
	s_mov_b32 m0, s66
	s_nop 0
	global_load_lds_dwordx4 v130, s[46:47]
	v_mov_b32_e32 v130, v140
	s_add_i32 m0, s66, 0x2000
	s_add_u32 s66, s46, 0x80000
	global_load_lds_dwordx4 v130, s[46:47]
	s_addc_u32 s67, s47, 0
	v_mov_b32_e32 v130, v138
	s_add_i32 s68, s57, s29
	s_mov_b32 m0, s68
	s_nop 0
	global_load_lds_dwordx4 v130, s[66:67]
	v_mov_b32_e32 v130, v140
	s_add_i32 m0, s68, 0x2000
	s_nop 0
	global_load_lds_dwordx4 v130, s[66:67]
	v_mov_b32_e32 v130, v1
	s_mov_b32 m0, s41
	s_nop 0
	global_load_lds_dwordx4 v130, s[44:45]
	v_mov_b32_e32 v130, v139
	s_mov_b32 m0, s48
	s_nop 0
	global_load_lds_dwordx4 v130, s[44:45]
	s_waitcnt vmcnt(8)
	s_waitcnt lgkmcnt(0)
	s_barrier
	s_waitcnt lgkmcnt(0)
	v_mfma_f32_16x16x32_bf16 v[62:65], v[132:135], v[178:181], v[62:65]
	v_mfma_f32_16x16x32_bf16 v[58:61], v[154:157], v[178:181], v[58:61]
	v_mfma_f32_16x16x32_bf16 v[50:53], v[132:135], v[186:189], v[50:53]
	v_mfma_f32_16x16x32_bf16 v[42:45], v[154:157], v[186:189], v[42:45]
	v_mfma_f32_16x16x32_bf16 v[34:37], v[132:135], v[194:197], v[34:37]
	v_mfma_f32_16x16x32_bf16 v[26:29], v[154:157], v[194:197], v[26:29]
	v_mfma_f32_16x16x32_bf16 v[18:21], v[132:135], v[204:207], v[18:21]
	v_mfma_f32_16x16x32_bf16 v[10:13], v[154:157], v[204:207], v[10:13]
	v_mfma_f32_16x16x32_bf16 v[62:65], v[150:153], v[182:185], v[62:65]
	v_mfma_f32_16x16x32_bf16 v[58:61], v[158:161], v[182:185], v[58:61]
	v_mfma_f32_16x16x32_bf16 v[50:53], v[150:153], v[190:193], v[50:53]
	v_mfma_f32_16x16x32_bf16 v[42:45], v[158:161], v[190:193], v[42:45]
	v_mfma_f32_16x16x32_bf16 v[34:37], v[150:153], v[200:203], v[34:37]
	v_mfma_f32_16x16x32_bf16 v[26:29], v[158:161], v[200:203], v[26:29]
	v_mfma_f32_16x16x32_bf16 v[18:21], v[150:153], v[208:211], v[18:21]
	v_mfma_f32_16x16x32_bf16 v[10:13], v[158:161], v[208:211], v[10:13]
	v_mfma_f32_16x16x32_bf16 v[54:57], v[162:165], v[178:181], v[54:57]
	v_mfma_f32_16x16x32_bf16 v[46:49], v[170:173], v[178:181], v[46:49]
	v_mfma_f32_16x16x32_bf16 v[38:41], v[162:165], v[186:189], v[38:41]
	v_mfma_f32_16x16x32_bf16 v[30:33], v[170:173], v[186:189], v[30:33]
	v_mfma_f32_16x16x32_bf16 v[22:25], v[162:165], v[194:197], v[22:25]
	v_mfma_f32_16x16x32_bf16 v[14:17], v[170:173], v[194:197], v[14:17]
	v_mfma_f32_16x16x32_bf16 v[6:9], v[162:165], v[204:207], v[6:9]
	v_mfma_f32_16x16x32_bf16 v[2:5], v[170:173], v[204:207], v[2:5]
	v_mfma_f32_16x16x32_bf16 v[54:57], v[166:169], v[182:185], v[54:57]
	v_mfma_f32_16x16x32_bf16 v[46:49], v[174:177], v[182:185], v[46:49]
	v_mfma_f32_16x16x32_bf16 v[38:41], v[166:169], v[190:193], v[38:41]
	v_mfma_f32_16x16x32_bf16 v[30:33], v[174:177], v[190:193], v[30:33]
	v_mfma_f32_16x16x32_bf16 v[22:25], v[166:169], v[200:203], v[22:25]
	v_mfma_f32_16x16x32_bf16 v[14:17], v[174:177], v[200:203], v[14:17]
	v_mfma_f32_16x16x32_bf16 v[6:9], v[166:169], v[208:211], v[6:9]
	v_mfma_f32_16x16x32_bf16 v[2:5], v[174:177], v[208:211], v[2:5]
	s_barrier
; #define PG8_STAGE_A(bufoff, gbase, h, go) do { if constexpr (Sched::GATHER) { PG8_STAGE(bufoff, gbase, go[h]); } else { PG8_STAGE(bufoff, (gbase) + (h) * hstep, voffA); } } while (0)
; #define PG8_LDA(dst, b, h) do { _Pragma("unroll") for (int m = 0; m < 4; ++m) _Pragma("unroll") for (int k = 0; k < 2; ++k) dst[m][k] = *(const LAS bf16x8*)(lds + PG8_SA(b, h) + aoff + m * 2048 + k * 1024); } while (0)
; #define PG8_LDB(dst, b, h) do { _Pragma("unroll") for (int n = 0; n < 2; ++n) _Pragma("unroll") for (int k = 0; k < 2; ++k) dst[n][k] = *(const LAS bf16x8*)(lds + PG8_SB(b, h) + boff + n * 2048 + k * 1024); } while (0)
; #define PG8_WAIT_V(n) asm volatile("s_waitcnt vmcnt(" #n ")" ::: "memory")
; #define PG8_WAIT_L(n) asm volatile("s_waitcnt lgkmcnt(" #n ")" ::: "memory")
; #define PG8_BAR __builtin_amdgcn_s_barrier()
; #define PG8_SCHED __builtin_amdgcn_sched_barrier(0)
;     ...
;             PG8_LDB(B0, 1, 0); PG8_LDB(B1, 1, 1); PG8_SCHED; PG8_LDA(At, 1, 0); PG8_STAGE_A(PG8_SA(0, 1), a2, 1, gc);
;             PG8_WAIT_V(8); PG8_WAIT_L(0); PG8_BAR; PG8_MMA(0, 0, At, B0); PG8_MMA(0, 1, At, B1); PG8_BAR; PG8_SCHED;
	s_add_i32 s68, 0, 0x18000
	v_add_u32_e32 v130, s68, v143
	s_add_i32 s69, 0, 0x1c000
	ds_read_b128 v[132:135], v130
	ds_read_b128 v[150:153], v130 offset:1024
	ds_read_b128 v[154:157], v130 offset:2048
	ds_read_b128 v[158:161], v130 offset:3072
	v_add_u32_e32 v130, s69, v143
	ds_read_b128 v[162:165], v130
	ds_read_b128 v[166:169], v130 offset:1024
	ds_read_b128 v[170:173], v130 offset:2048
	ds_read_b128 v[174:177], v130 offset:3072
	s_add_u32 s66, s44, 0x80000
	v_mov_b32_e32 v130, v1
	s_mov_b32 m0, s49
	ds_read_b128 v[178:181], v147 offset:32768
	ds_read_b128 v[182:185], v147 offset:33792
	ds_read_b128 v[186:189], v147 offset:34816
	ds_read_b128 v[190:193], v147 offset:35840
	ds_read_b128 v[194:197], v147 offset:36864
	ds_read_b128 v[200:203], v147 offset:37888
	ds_read_b128 v[204:207], v147 offset:38912
	ds_read_b128 v[208:211], v147 offset:39936
	s_addc_u32 s67, s45, 0
	s_nop 0
	global_load_lds_dwordx4 v130, s[66:67]
	v_mov_b32_e32 v130, v139
	s_mov_b32 m0, s50
	s_nop 0
	global_load_lds_dwordx4 v130, s[66:67]
	s_waitcnt vmcnt(8)
	s_waitcnt lgkmcnt(0)
	s_barrier
	s_waitcnt lgkmcnt(0)
	v_mfma_f32_16x16x32_bf16 v[126:129], v[132:135], v[178:181], v[126:129]
	v_mfma_f32_16x16x32_bf16 v[122:125], v[154:157], v[178:181], v[122:125]
	v_mfma_f32_16x16x32_bf16 v[114:117], v[132:135], v[186:189], v[114:117]
	v_mfma_f32_16x16x32_bf16 v[106:109], v[154:157], v[186:189], v[106:109]
	v_mfma_f32_16x16x32_bf16 v[98:101], v[132:135], v[194:197], v[98:101]
	v_mfma_f32_16x16x32_bf16 v[90:93], v[154:157], v[194:197], v[90:93]
	v_mfma_f32_16x16x32_bf16 v[82:85], v[132:135], v[204:207], v[82:85]
	v_mfma_f32_16x16x32_bf16 v[74:77], v[154:157], v[204:207], v[74:77]
	v_mfma_f32_16x16x32_bf16 v[126:129], v[150:153], v[182:185], v[126:129]
	v_mfma_f32_16x16x32_bf16 v[122:125], v[158:161], v[182:185], v[122:125]
	v_mfma_f32_16x16x32_bf16 v[114:117], v[150:153], v[190:193], v[114:117]
	v_mfma_f32_16x16x32_bf16 v[106:109], v[158:161], v[190:193], v[106:109]
	v_mfma_f32_16x16x32_bf16 v[98:101], v[150:153], v[200:203], v[98:101]
	v_mfma_f32_16x16x32_bf16 v[90:93], v[158:161], v[200:203], v[90:93]
	v_mfma_f32_16x16x32_bf16 v[82:85], v[150:153], v[208:211], v[82:85]
	v_mfma_f32_16x16x32_bf16 v[74:77], v[158:161], v[208:211], v[74:77]
	v_mfma_f32_16x16x32_bf16 v[118:121], v[162:165], v[178:181], v[118:121]
	v_mfma_f32_16x16x32_bf16 v[110:113], v[170:173], v[178:181], v[110:113]
	v_mfma_f32_16x16x32_bf16 v[102:105], v[162:165], v[186:189], v[102:105]
	v_mfma_f32_16x16x32_bf16 v[94:97], v[170:173], v[186:189], v[94:97]
	v_mfma_f32_16x16x32_bf16 v[86:89], v[162:165], v[194:197], v[86:89]
	v_mfma_f32_16x16x32_bf16 v[78:81], v[170:173], v[194:197], v[78:81]
	v_mfma_f32_16x16x32_bf16 v[70:73], v[162:165], v[204:207], v[70:73]
	v_mfma_f32_16x16x32_bf16 v[66:69], v[170:173], v[204:207], v[66:69]
	v_mfma_f32_16x16x32_bf16 v[118:121], v[166:169], v[182:185], v[118:121]
	v_mfma_f32_16x16x32_bf16 v[110:113], v[174:177], v[182:185], v[110:113]
	v_mfma_f32_16x16x32_bf16 v[102:105], v[166:169], v[190:193], v[102:105]
	v_mfma_f32_16x16x32_bf16 v[94:97], v[174:177], v[190:193], v[94:97]
	v_mfma_f32_16x16x32_bf16 v[86:89], v[166:169], v[200:203], v[86:89]
	v_mfma_f32_16x16x32_bf16 v[78:81], v[174:177], v[200:203], v[78:81]
	v_mfma_f32_16x16x32_bf16 v[70:73], v[166:169], v[208:211], v[70:73]
	v_mfma_f32_16x16x32_bf16 v[66:69], v[174:177], v[208:211], v[66:69]
	s_barrier
; #define PG8_STAGE(bufoff, gbase, voff) do { _Pragma("unroll") for (int _i = 0; _i < 2; ++_i) { unsigned _vo = (voff)[_i]; asm volatile("" : "+v"(_vo)); \
;         __builtin_amdgcn_global_load_lds((const unsigned*)((const char*)(gbase) + _vo), (LAS unsigned*)(lds + (bufoff) + ldsw + _i * 8192), 16, 0, 0); } } while (0)
; #define PG8_STAGE_A(bufoff, gbase, h, go) do { if constexpr (Sched::GATHER) { PG8_STAGE(bufoff, gbase, go[h]); } else { PG8_STAGE(bufoff, (gbase) + (h) * hstep, voffA); } } while (0)
; #define PG8_LDA(dst, b, h) do { _Pragma("unroll") for (int m = 0; m < 4; ++m) _Pragma("unroll") for (int k = 0; k < 2; ++k) dst[m][k] = *(const LAS bf16x8*)(lds + PG8_SA(b, h) + aoff + m * 2048 + k * 1024); } while (0)
; #define PG8_WAIT_V(n) asm volatile("s_waitcnt vmcnt(" #n ")" ::: "memory")
; #define PG8_WAIT_L(n) asm volatile("s_waitcnt lgkmcnt(" #n ")" ::: "memory")
; #define PG8_BAR __builtin_amdgcn_s_barrier()
; #define PG8_SCHED __builtin_amdgcn_sched_barrier(0)
;     ...
;             PG8_LDA(At, 1, 1); PG8_STAGE(PG8_SB(1, 0), b3, voffB); PG8_STAGE(PG8_SB(1, 1), b3 + hstep, voffB); PG8_STAGE_A(PG8_SA(1, 0), a3, 0, gc);
;             PG8_WAIT_V(8); PG8_WAIT_L(0); PG8_BAR; PG8_MMA(1, 0, At, B0); PG8_MMA(1, 1, At, B1); PG8_BAR; PG8_SCHED;
;         }
;         if (wr == 0) PG8_BAR;
	v_mov_b32_e32 v130, v138
	ds_read_b128 v[178:181], v147 offset:49152
	ds_read_b128 v[182:185], v147 offset:50176
	ds_read_b128 v[186:189], v147 offset:51200
	ds_read_b128 v[190:193], v147 offset:52224
	ds_read_b128 v[194:197], v147 offset:53248
	ds_read_b128 v[200:203], v147 offset:54272
	ds_read_b128 v[204:207], v147 offset:55296
	ds_read_b128 v[208:211], v147 offset:56320
	s_add_i32 s66, s68, s29
	v_lshl_add_u64 v[136:137], s[46:47], 0, v[130:131]
	v_lshl_add_u64 v[136:137], v[136:137], 0, s[12:13]
	s_mov_b32 m0, s66
	v_mov_b32_e32 v130, v140
	global_load_lds_dwordx4 v[136:137], off
	s_add_i32 m0, s66, 0x2000
	s_nop 0
	v_lshl_add_u64 v[136:137], s[46:47], 0, v[130:131]
	s_add_u32 s46, s46, 0x80080
	v_lshl_add_u64 v[136:137], v[136:137], 0, s[12:13]
	s_addc_u32 s47, s47, 0
	v_mov_b32_e32 v130, v138
	s_add_i32 s66, s69, s29
	global_load_lds_dwordx4 v[136:137], off
	s_mov_b32 m0, s66
	s_nop 0
	global_load_lds_dwordx4 v130, s[46:47]
	v_mov_b32_e32 v130, v140
	s_add_i32 m0, s66, 0x2000
	s_nop 0
	global_load_lds_dwordx4 v130, s[46:47]
	v_mov_b32_e32 v130, v1
	s_mov_b32 m0, s53
	v_lshl_add_u64 v[136:137], s[44:45], 0, v[130:131]
	v_lshl_add_u64 v[136:137], v[136:137], 0, s[12:13]
	v_mov_b32_e32 v130, v139
	global_load_lds_dwordx4 v[136:137], off
	s_mov_b32 m0, s54
	v_lshl_add_u64 v[136:137], s[44:45], 0, v[130:131]
	v_lshl_add_u64 v[136:137], v[136:137], 0, s[12:13]
	global_load_lds_dwordx4 v[136:137], off
	s_waitcnt vmcnt(8)
	s_waitcnt lgkmcnt(0)
	s_barrier
	s_waitcnt lgkmcnt(0)
	v_mfma_f32_16x16x32_bf16 v[62:65], v[132:135], v[178:181], v[62:65]
	v_mfma_f32_16x16x32_bf16 v[58:61], v[154:157], v[178:181], v[58:61]
	v_mfma_f32_16x16x32_bf16 v[50:53], v[132:135], v[186:189], v[50:53]
	v_mfma_f32_16x16x32_bf16 v[42:45], v[154:157], v[186:189], v[42:45]
	v_mfma_f32_16x16x32_bf16 v[34:37], v[132:135], v[194:197], v[34:37]
	v_mfma_f32_16x16x32_bf16 v[26:29], v[154:157], v[194:197], v[26:29]
	v_mfma_f32_16x16x32_bf16 v[18:21], v[132:135], v[204:207], v[18:21]
	v_mfma_f32_16x16x32_bf16 v[10:13], v[154:157], v[204:207], v[10:13]
	v_mfma_f32_16x16x32_bf16 v[62:65], v[150:153], v[182:185], v[62:65]
	v_mfma_f32_16x16x32_bf16 v[58:61], v[158:161], v[182:185], v[58:61]
	v_mfma_f32_16x16x32_bf16 v[50:53], v[150:153], v[190:193], v[50:53]
	v_mfma_f32_16x16x32_bf16 v[42:45], v[158:161], v[190:193], v[42:45]
	v_mfma_f32_16x16x32_bf16 v[34:37], v[150:153], v[200:203], v[34:37]
	v_mfma_f32_16x16x32_bf16 v[26:29], v[158:161], v[200:203], v[26:29]
	v_mfma_f32_16x16x32_bf16 v[18:21], v[150:153], v[208:211], v[18:21]
	v_mfma_f32_16x16x32_bf16 v[10:13], v[158:161], v[208:211], v[10:13]
	v_mfma_f32_16x16x32_bf16 v[54:57], v[162:165], v[178:181], v[54:57]
	v_mfma_f32_16x16x32_bf16 v[46:49], v[170:173], v[178:181], v[46:49]
	v_mfma_f32_16x16x32_bf16 v[38:41], v[162:165], v[186:189], v[38:41]
	v_mfma_f32_16x16x32_bf16 v[30:33], v[170:173], v[186:189], v[30:33]
	v_mfma_f32_16x16x32_bf16 v[22:25], v[162:165], v[194:197], v[22:25]
	v_mfma_f32_16x16x32_bf16 v[14:17], v[170:173], v[194:197], v[14:17]
	v_mfma_f32_16x16x32_bf16 v[6:9], v[162:165], v[204:207], v[6:9]
	v_mfma_f32_16x16x32_bf16 v[2:5], v[170:173], v[204:207], v[2:5]
	v_mfma_f32_16x16x32_bf16 v[54:57], v[166:169], v[182:185], v[54:57]
	v_mfma_f32_16x16x32_bf16 v[46:49], v[174:177], v[182:185], v[46:49]
	v_mfma_f32_16x16x32_bf16 v[38:41], v[166:169], v[190:193], v[38:41]
	v_mfma_f32_16x16x32_bf16 v[30:33], v[174:177], v[190:193], v[30:33]
	v_mfma_f32_16x16x32_bf16 v[22:25], v[166:169], v[200:203], v[22:25]
	v_mfma_f32_16x16x32_bf16 v[14:17], v[174:177], v[200:203], v[14:17]
	v_mfma_f32_16x16x32_bf16 v[6:9], v[166:169], v[208:211], v[6:9]
	v_mfma_f32_16x16x32_bf16 v[2:5], v[174:177], v[208:211], v[2:5]
	s_barrier
	s_add_i32 s65, s65, 2
	s_add_u32 s42, s42, 0x100
	s_addc_u32 s43, s43, 0
	s_add_u32 s63, s63, 0x100
	s_addc_u32 s64, s64, 0
	s_cmp_gt_u32 s65, 29
	s_cbranch_scc0 .LBB5_1259
	v_readlane_b32 s64, v253, 42
	v_readlane_b32 s65, v253, 43
	v_readlane_b32 s76, v253, 54
	v_readlane_b32 s77, v253, 55
	s_and_b64 vcc, exec, s[14:15]
	s_mov_b64 s[64:65], s[76:77]
	v_readlane_b32 s66, v253, 44
	v_readlane_b32 s67, v253, 45
	v_readlane_b32 s68, v253, 46
	v_readlane_b32 s69, v253, 47
	v_readlane_b32 s70, v253, 48
	v_readlane_b32 s71, v253, 49
	v_readlane_b32 s72, v253, 50
	v_readlane_b32 s73, v253, 51
	v_readlane_b32 s74, v253, 52
	v_readlane_b32 s75, v253, 53
	v_readlane_b32 s78, v253, 56
	v_readlane_b32 s79, v253, 57
	s_cbranch_vccz .LBB5_1262
	s_barrier

; #define PG8_STAGE(bufoff, gbase, voff) do { _Pragma("unroll") for (int _i = 0; _i < 2; ++_i) { unsigned _vo = (voff)[_i]; asm volatile("" : "+v"(_vo)); \
;         __builtin_amdgcn_global_load_lds((const unsigned*)((const char*)(gbase) + _vo), (LAS unsigned*)(lds + (bufoff) + ldsw + _i * 8192), 16, 0, 0); } } while (0)
; #define PG8_STAGE_A(bufoff, gbase, h, go) do { if constexpr (Sched::GATHER) { PG8_STAGE(bufoff, gbase, go[h]); } else { PG8_STAGE(bufoff, (gbase) + (h) * hstep, voffA); } } while (0)
; #define PG8_LDA(dst, b, h) do { _Pragma("unroll") for (int m = 0; m < 4; ++m) _Pragma("unroll") for (int k = 0; k < 2; ++k) dst[m][k] = *(const LAS bf16x8*)(lds + PG8_SA(b, h) + aoff + m * 2048 + k * 1024); } while (0)
; #define PG8_LDB(dst, b, h) do { _Pragma("unroll") for (int n = 0; n < 2; ++n) _Pragma("unroll") for (int k = 0; k < 2; ++k) dst[n][k] = *(const LAS bf16x8*)(lds + PG8_SB(b, h) + boff + n * 2048 + k * 1024); } while (0)
; #define PG8_WAIT_V(n) asm volatile("s_waitcnt vmcnt(" #n ")" ::: "memory")
; #define PG8_WAIT_L(n) asm volatile("s_waitcnt lgkmcnt(" #n ")" ::: "memory")
; #define PG8_BAR __builtin_amdgcn_s_barrier()
;     ...
;         for (int t = 0; t < nt; t += 2) {
;             const bool last = (t == nt - 2);
;             if constexpr (Epi::MIDK) { if (t == nt / 2) { int fr_e = fr; asm volatile("" : "+v"(fr_e)); E.midk(acc, cur, wr, fr_e); } }
;             const char* a1 = cA + (size_t)(t + 1) * kstep;
;             const char* a2 = last ? nA : cA + (size_t)(t + 2) * kstep; const char* b2 = last ? nB : cB + (size_t)(t + 2) * kstep;
;             const char* a3 = a2 + kstep; const char* b3 = b2 + kstep;
;             PG8_LDB(B0, 0, 0); PG8_LDB(B1, 0, 1); PG8_SCHED; PG8_LDA(At, 0, 0); PG8_STAGE_A(PG8_SA(1, 1), a1, 1, gc);
;             if constexpr (Sched::GATHER) { if (last) {
; #pragma unroll
;                 for (int h = 0; h < 2; ++h)
; #pragma unroll
;                     for (int i = 0; i < 2; ++i) gc[h][i] = gn[h][i]; } }
;             PG8_WAIT_V(8); PG8_WAIT_L(0); PG8_BAR; PG8_MMA(0, 0, At, B0); PG8_MMA(0, 1, At, B1); PG8_BAR; PG8_SCHED;
;             PG8_LDA(At, 0, 1); PG8_STAGE(PG8_SB(0, 0), b2, voffB); PG8_STAGE(PG8_SB(0, 1), b2 + hstep, voffB); PG8_STAGE_A(PG8_SA(0, 0), a2, 0, gc);
;             PG8_WAIT_V(8); PG8_WAIT_L(0); PG8_BAR; PG8_MMA(1, 0, At, B0); PG8_MMA(1, 1, At, B1); PG8_BAR; PG8_SCHED;
.LBB5_1405:
	ds_read_b128 v[130:133], v154
	ds_read_b128 v[134:137], v154 offset:1024
	ds_read_b128 v[140:143], v154 offset:2048
	ds_read_b128 v[144:147], v154 offset:3072
	ds_read_b128 v[158:161], v155
	ds_read_b128 v[162:165], v155 offset:1024
	ds_read_b128 v[166:169], v155 offset:2048
	ds_read_b128 v[170:173], v155 offset:3072
	s_add_u32 s44, s42, 0xfffe0080
	s_addc_u32 s45, s43, -1
	s_cmp_eq_u32 s61, 4
	s_cselect_b32 s45, s37, s45
	s_cselect_b32 s44, s36, s44
	s_cselect_b32 s47, s39, s60
	s_cselect_b32 s46, s38, s35
	v_mov_b32_e32 v138, v1
	ds_read_b128 v[174:177], v156
	ds_read_b128 v[178:181], v156 offset:1024
	ds_read_b128 v[182:185], v156 offset:2048
	ds_read_b128 v[186:189], v156 offset:3072
	ds_read_b128 v[190:193], v156 offset:4096
	ds_read_b128 v[194:197], v156 offset:5120
	ds_read_b128 v[200:203], v156 offset:6144
	ds_read_b128 v[204:207], v156 offset:7168
	s_add_i32 m0, s41, 0xc000
	s_nop 0
	global_load_lds_dwordx4 v138, s[42:43]
	v_mov_b32_e32 v138, v149
	s_add_i32 m0, s41, 0xe000
	s_nop 0
	global_load_lds_dwordx4 v138, s[42:43]
	s_waitcnt vmcnt(8)
	s_waitcnt lgkmcnt(0)
	s_barrier
	s_waitcnt lgkmcnt(0)
	v_mfma_f32_16x16x32_bf16 v[126:129], v[130:133], v[174:177], v[126:129]
	v_mfma_f32_16x16x32_bf16 v[122:125], v[140:143], v[174:177], v[122:125]
	v_mfma_f32_16x16x32_bf16 v[114:117], v[130:133], v[182:185], v[114:117]
	v_mfma_f32_16x16x32_bf16 v[106:109], v[140:143], v[182:185], v[106:109]
	v_mfma_f32_16x16x32_bf16 v[94:97], v[130:133], v[190:193], v[94:97]
	v_mfma_f32_16x16x32_bf16 v[90:93], v[140:143], v[190:193], v[90:93]
	v_mfma_f32_16x16x32_bf16 v[78:81], v[130:133], v[200:203], v[78:81]
	v_mfma_f32_16x16x32_bf16 v[74:77], v[140:143], v[200:203], v[74:77]
	v_mfma_f32_16x16x32_bf16 v[126:129], v[134:137], v[178:181], v[126:129]
	v_mfma_f32_16x16x32_bf16 v[122:125], v[144:147], v[178:181], v[122:125]
	v_mfma_f32_16x16x32_bf16 v[114:117], v[134:137], v[186:189], v[114:117]
	v_mfma_f32_16x16x32_bf16 v[106:109], v[144:147], v[186:189], v[106:109]
	v_mfma_f32_16x16x32_bf16 v[94:97], v[134:137], v[194:197], v[94:97]
	v_mfma_f32_16x16x32_bf16 v[90:93], v[144:147], v[194:197], v[90:93]
	v_mfma_f32_16x16x32_bf16 v[78:81], v[134:137], v[204:207], v[78:81]
	v_mfma_f32_16x16x32_bf16 v[74:77], v[144:147], v[204:207], v[74:77]
	v_mfma_f32_16x16x32_bf16 v[118:121], v[158:161], v[174:177], v[118:121]
	v_mfma_f32_16x16x32_bf16 v[110:113], v[166:169], v[174:177], v[110:113]
	v_mfma_f32_16x16x32_bf16 v[102:105], v[158:161], v[182:185], v[102:105]
	v_mfma_f32_16x16x32_bf16 v[98:101], v[166:169], v[182:185], v[98:101]
	v_mfma_f32_16x16x32_bf16 v[86:89], v[158:161], v[190:193], v[86:89]
	v_mfma_f32_16x16x32_bf16 v[82:85], v[166:169], v[190:193], v[82:85]
	v_mfma_f32_16x16x32_bf16 v[70:73], v[158:161], v[200:203], v[70:73]
	v_mfma_f32_16x16x32_bf16 v[66:69], v[166:169], v[200:203], v[66:69]
	v_mfma_f32_16x16x32_bf16 v[118:121], v[162:165], v[178:181], v[118:121]
	v_mfma_f32_16x16x32_bf16 v[110:113], v[170:173], v[178:181], v[110:113]
	v_mfma_f32_16x16x32_bf16 v[102:105], v[162:165], v[186:189], v[102:105]
	v_mfma_f32_16x16x32_bf16 v[98:101], v[170:173], v[186:189], v[98:101]
	v_mfma_f32_16x16x32_bf16 v[86:89], v[162:165], v[194:197], v[86:89]
	v_mfma_f32_16x16x32_bf16 v[82:85], v[170:173], v[194:197], v[82:85]
	v_mfma_f32_16x16x32_bf16 v[70:73], v[162:165], v[204:207], v[70:73]
	v_mfma_f32_16x16x32_bf16 v[66:69], v[170:173], v[204:207], v[66:69]
	s_barrier
	v_mov_b32_e32 v138, v148
	s_add_i32 s62, s56, s29
	ds_read_b128 v[174:177], v156 offset:16384
	ds_read_b128 v[178:181], v156 offset:17408
	ds_read_b128 v[182:185], v156 offset:18432
	ds_read_b128 v[186:189], v156 offset:19456
	ds_read_b128 v[190:193], v156 offset:20480
	ds_read_b128 v[194:197], v156 offset:21504
	ds_read_b128 v[200:203], v156 offset:22528
	ds_read_b128 v[204:207], v156 offset:23552
	s_mov_b32 m0, s62
	s_nop 0
	global_load_lds_dwordx4 v138, s[46:47]
	v_mov_b32_e32 v138, v150
	s_add_i32 m0, s62, 0x2000
	s_add_u32 s62, s46, 0x20000
	global_load_lds_dwordx4 v138, s[46:47]
	s_addc_u32 s63, s47, 0
	v_mov_b32_e32 v138, v148
	s_add_i32 s64, s57, s29
	s_mov_b32 m0, s64
	s_nop 0
	global_load_lds_dwordx4 v138, s[62:63]
	v_mov_b32_e32 v138, v150
	s_add_i32 m0, s64, 0x2000
	s_nop 0
	global_load_lds_dwordx4 v138, s[62:63]
	v_mov_b32_e32 v138, v1
	s_mov_b32 m0, s41
	s_nop 0
	global_load_lds_dwordx4 v138, s[44:45]
	v_mov_b32_e32 v138, v149
	s_mov_b32 m0, s48
	s_nop 0
	global_load_lds_dwordx4 v138, s[44:45]
	s_waitcnt vmcnt(8)
	s_waitcnt lgkmcnt(0)
	s_barrier
	s_waitcnt lgkmcnt(0)
	v_mfma_f32_16x16x32_bf16 v[62:65], v[130:133], v[174:177], v[62:65]
	v_mfma_f32_16x16x32_bf16 v[58:61], v[140:143], v[174:177], v[58:61]
	v_mfma_f32_16x16x32_bf16 v[46:49], v[130:133], v[182:185], v[46:49]
	v_mfma_f32_16x16x32_bf16 v[42:45], v[140:143], v[182:185], v[42:45]
	v_mfma_f32_16x16x32_bf16 v[30:33], v[130:133], v[190:193], v[30:33]
	v_mfma_f32_16x16x32_bf16 v[26:29], v[140:143], v[190:193], v[26:29]
	v_mfma_f32_16x16x32_bf16 v[14:17], v[130:133], v[200:203], v[14:17]
	v_mfma_f32_16x16x32_bf16 v[10:13], v[140:143], v[200:203], v[10:13]
	v_mfma_f32_16x16x32_bf16 v[62:65], v[134:137], v[178:181], v[62:65]
	v_mfma_f32_16x16x32_bf16 v[58:61], v[144:147], v[178:181], v[58:61]
	v_mfma_f32_16x16x32_bf16 v[46:49], v[134:137], v[186:189], v[46:49]
	v_mfma_f32_16x16x32_bf16 v[42:45], v[144:147], v[186:189], v[42:45]
	v_mfma_f32_16x16x32_bf16 v[30:33], v[134:137], v[194:197], v[30:33]
	v_mfma_f32_16x16x32_bf16 v[26:29], v[144:147], v[194:197], v[26:29]
	v_mfma_f32_16x16x32_bf16 v[14:17], v[134:137], v[204:207], v[14:17]
	v_mfma_f32_16x16x32_bf16 v[10:13], v[144:147], v[204:207], v[10:13]
	v_mfma_f32_16x16x32_bf16 v[54:57], v[158:161], v[174:177], v[54:57]
	v_mfma_f32_16x16x32_bf16 v[50:53], v[166:169], v[174:177], v[50:53]
	v_mfma_f32_16x16x32_bf16 v[38:41], v[158:161], v[182:185], v[38:41]
	v_mfma_f32_16x16x32_bf16 v[34:37], v[166:169], v[182:185], v[34:37]
	v_mfma_f32_16x16x32_bf16 v[22:25], v[158:161], v[190:193], v[22:25]
	v_mfma_f32_16x16x32_bf16 v[18:21], v[166:169], v[190:193], v[18:21]
	v_mfma_f32_16x16x32_bf16 v[6:9], v[158:161], v[200:203], v[6:9]
	v_mfma_f32_16x16x32_bf16 v[2:5], v[166:169], v[200:203], v[2:5]
	v_mfma_f32_16x16x32_bf16 v[54:57], v[162:165], v[178:181], v[54:57]
	v_mfma_f32_16x16x32_bf16 v[50:53], v[170:173], v[178:181], v[50:53]
	v_mfma_f32_16x16x32_bf16 v[38:41], v[162:165], v[186:189], v[38:41]
	v_mfma_f32_16x16x32_bf16 v[34:37], v[170:173], v[186:189], v[34:37]
	v_mfma_f32_16x16x32_bf16 v[22:25], v[162:165], v[194:197], v[22:25]
	v_mfma_f32_16x16x32_bf16 v[18:21], v[170:173], v[194:197], v[18:21]
	v_mfma_f32_16x16x32_bf16 v[6:9], v[162:165], v[204:207], v[6:9]
	v_mfma_f32_16x16x32_bf16 v[2:5], v[170:173], v[204:207], v[2:5]
	s_barrier
; #define PG8_STAGE_A(bufoff, gbase, h, go) do { if constexpr (Sched::GATHER) { PG8_STAGE(bufoff, gbase, go[h]); } else { PG8_STAGE(bufoff, (gbase) + (h) * hstep, voffA); } } while (0)
; #define PG8_LDA(dst, b, h) do { _Pragma("unroll") for (int m = 0; m < 4; ++m) _Pragma("unroll") for (int k = 0; k < 2; ++k) dst[m][k] = *(const LAS bf16x8*)(lds + PG8_SA(b, h) + aoff + m * 2048 + k * 1024); } while (0)
; #define PG8_LDB(dst, b, h) do { _Pragma("unroll") for (int n = 0; n < 2; ++n) _Pragma("unroll") for (int k = 0; k < 2; ++k) dst[n][k] = *(const LAS bf16x8*)(lds + PG8_SB(b, h) + boff + n * 2048 + k * 1024); } while (0)
; #define PG8_WAIT_V(n) asm volatile("s_waitcnt vmcnt(" #n ")" ::: "memory")
; #define PG8_WAIT_L(n) asm volatile("s_waitcnt lgkmcnt(" #n ")" ::: "memory")
; #define PG8_BAR __builtin_amdgcn_s_barrier()
; #define PG8_SCHED __builtin_amdgcn_sched_barrier(0)
;     ...
;             PG8_LDB(B0, 1, 0); PG8_LDB(B1, 1, 1); PG8_SCHED; PG8_LDA(At, 1, 0); PG8_STAGE_A(PG8_SA(0, 1), a2, 1, gc);
;             PG8_WAIT_V(8); PG8_WAIT_L(0); PG8_BAR; PG8_MMA(0, 0, At, B0); PG8_MMA(0, 1, At, B1); PG8_BAR; PG8_SCHED;
	s_add_i32 s64, 0, 0x18000
	v_add_u32_e32 v138, s64, v153
	s_add_i32 s65, 0, 0x1c000
	ds_read_b128 v[130:133], v138
	ds_read_b128 v[134:137], v138 offset:1024
	ds_read_b128 v[140:143], v138 offset:2048
	ds_read_b128 v[144:147], v138 offset:3072
	v_add_u32_e32 v138, s65, v153
	ds_read_b128 v[158:161], v138
	ds_read_b128 v[162:165], v138 offset:1024
	ds_read_b128 v[166:169], v138 offset:2048
	ds_read_b128 v[170:173], v138 offset:3072
	s_add_u32 s62, s44, 0x20000
	v_mov_b32_e32 v138, v1
	s_mov_b32 m0, s49
	ds_read_b128 v[174:177], v156 offset:32768
	ds_read_b128 v[178:181], v156 offset:33792
	ds_read_b128 v[182:185], v156 offset:34816
	ds_read_b128 v[186:189], v156 offset:35840
	ds_read_b128 v[190:193], v156 offset:36864
	ds_read_b128 v[194:197], v156 offset:37888
	ds_read_b128 v[200:203], v156 offset:38912
	ds_read_b128 v[204:207], v156 offset:39936
	s_addc_u32 s63, s45, 0
	s_nop 0
	global_load_lds_dwordx4 v138, s[62:63]
	v_mov_b32_e32 v138, v149
	s_mov_b32 m0, s50
	s_nop 0
	global_load_lds_dwordx4 v138, s[62:63]
	s_waitcnt vmcnt(8)
	s_waitcnt lgkmcnt(0)
	s_barrier
	s_waitcnt lgkmcnt(0)
	v_mfma_f32_16x16x32_bf16 v[126:129], v[130:133], v[174:177], v[126:129]
	v_mfma_f32_16x16x32_bf16 v[122:125], v[140:143], v[174:177], v[122:125]
	v_mfma_f32_16x16x32_bf16 v[114:117], v[130:133], v[182:185], v[114:117]
	v_mfma_f32_16x16x32_bf16 v[106:109], v[140:143], v[182:185], v[106:109]
	v_mfma_f32_16x16x32_bf16 v[94:97], v[130:133], v[190:193], v[94:97]
	v_mfma_f32_16x16x32_bf16 v[90:93], v[140:143], v[190:193], v[90:93]
	v_mfma_f32_16x16x32_bf16 v[78:81], v[130:133], v[200:203], v[78:81]
	v_mfma_f32_16x16x32_bf16 v[74:77], v[140:143], v[200:203], v[74:77]
	v_mfma_f32_16x16x32_bf16 v[126:129], v[134:137], v[178:181], v[126:129]
	v_mfma_f32_16x16x32_bf16 v[122:125], v[144:147], v[178:181], v[122:125]
	v_mfma_f32_16x16x32_bf16 v[114:117], v[134:137], v[186:189], v[114:117]
	v_mfma_f32_16x16x32_bf16 v[106:109], v[144:147], v[186:189], v[106:109]
	v_mfma_f32_16x16x32_bf16 v[94:97], v[134:137], v[194:197], v[94:97]
	v_mfma_f32_16x16x32_bf16 v[90:93], v[144:147], v[194:197], v[90:93]
	v_mfma_f32_16x16x32_bf16 v[78:81], v[134:137], v[204:207], v[78:81]
	v_mfma_f32_16x16x32_bf16 v[74:77], v[144:147], v[204:207], v[74:77]
	v_mfma_f32_16x16x32_bf16 v[118:121], v[158:161], v[174:177], v[118:121]
	v_mfma_f32_16x16x32_bf16 v[110:113], v[166:169], v[174:177], v[110:113]
	v_mfma_f32_16x16x32_bf16 v[102:105], v[158:161], v[182:185], v[102:105]
	v_mfma_f32_16x16x32_bf16 v[98:101], v[166:169], v[182:185], v[98:101]
	v_mfma_f32_16x16x32_bf16 v[86:89], v[158:161], v[190:193], v[86:89]
	v_mfma_f32_16x16x32_bf16 v[82:85], v[166:169], v[190:193], v[82:85]
	v_mfma_f32_16x16x32_bf16 v[70:73], v[158:161], v[200:203], v[70:73]
	v_mfma_f32_16x16x32_bf16 v[66:69], v[166:169], v[200:203], v[66:69]
	v_mfma_f32_16x16x32_bf16 v[118:121], v[162:165], v[178:181], v[118:121]
	v_mfma_f32_16x16x32_bf16 v[110:113], v[170:173], v[178:181], v[110:113]
	v_mfma_f32_16x16x32_bf16 v[102:105], v[162:165], v[186:189], v[102:105]
	v_mfma_f32_16x16x32_bf16 v[98:101], v[170:173], v[186:189], v[98:101]
	v_mfma_f32_16x16x32_bf16 v[86:89], v[162:165], v[194:197], v[86:89]
	v_mfma_f32_16x16x32_bf16 v[82:85], v[170:173], v[194:197], v[82:85]
	v_mfma_f32_16x16x32_bf16 v[70:73], v[162:165], v[204:207], v[70:73]
	v_mfma_f32_16x16x32_bf16 v[66:69], v[170:173], v[204:207], v[66:69]
	s_barrier
; #define PG8_STAGE(bufoff, gbase, voff) do { _Pragma("unroll") for (int _i = 0; _i < 2; ++_i) { unsigned _vo = (voff)[_i]; asm volatile("" : "+v"(_vo)); \
;         __builtin_amdgcn_global_load_lds((const unsigned*)((const char*)(gbase) + _vo), (LAS unsigned*)(lds + (bufoff) + ldsw + _i * 8192), 16, 0, 0); } } while (0)
; #define PG8_STAGE_A(bufoff, gbase, h, go) do { if constexpr (Sched::GATHER) { PG8_STAGE(bufoff, gbase, go[h]); } else { PG8_STAGE(bufoff, (gbase) + (h) * hstep, voffA); } } while (0)
; #define PG8_LDA(dst, b, h) do { _Pragma("unroll") for (int m = 0; m < 4; ++m) _Pragma("unroll") for (int k = 0; k < 2; ++k) dst[m][k] = *(const LAS bf16x8*)(lds + PG8_SA(b, h) + aoff + m * 2048 + k * 1024); } while (0)
; #define PG8_WAIT_V(n) asm volatile("s_waitcnt vmcnt(" #n ")" ::: "memory")
; #define PG8_WAIT_L(n) asm volatile("s_waitcnt lgkmcnt(" #n ")" ::: "memory")
; #define PG8_BAR __builtin_amdgcn_s_barrier()
; #define PG8_SCHED __builtin_amdgcn_sched_barrier(0)
;     ...
;             PG8_LDA(At, 1, 1); PG8_STAGE(PG8_SB(1, 0), b3, voffB); PG8_STAGE(PG8_SB(1, 1), b3 + hstep, voffB); PG8_STAGE_A(PG8_SA(1, 0), a3, 0, gc);
;             PG8_WAIT_V(8); PG8_WAIT_L(0); PG8_BAR; PG8_MMA(1, 0, At, B0); PG8_MMA(1, 1, At, B1); PG8_BAR; PG8_SCHED;
	v_mov_b32_e32 v138, v148
	ds_read_b128 v[174:177], v156 offset:49152
	ds_read_b128 v[178:181], v156 offset:50176
	ds_read_b128 v[182:185], v156 offset:51200
	ds_read_b128 v[186:189], v156 offset:52224
	ds_read_b128 v[190:193], v156 offset:53248
	ds_read_b128 v[194:197], v156 offset:54272
	ds_read_b128 v[200:203], v156 offset:55296
	ds_read_b128 v[204:207], v156 offset:56320
	s_add_i32 s62, s64, s29
	v_lshl_add_u64 v[208:209], s[46:47], 0, v[138:139]
	v_lshl_add_u64 v[208:209], v[208:209], 0, s[12:13]
	s_mov_b32 m0, s62
	v_mov_b32_e32 v138, v150
	global_load_lds_dwordx4 v[208:209], off
	s_add_i32 m0, s62, 0x2000
	s_nop 0
	v_lshl_add_u64 v[208:209], s[46:47], 0, v[138:139]
	s_add_u32 s46, s46, 0x20080
	v_lshl_add_u64 v[208:209], v[208:209], 0, s[12:13]
	s_addc_u32 s47, s47, 0
	v_mov_b32_e32 v138, v148
	s_add_i32 s62, s65, s29
	global_load_lds_dwordx4 v[208:209], off
	s_mov_b32 m0, s62
	s_nop 0
	global_load_lds_dwordx4 v138, s[46:47]
	v_mov_b32_e32 v138, v150
	s_add_i32 m0, s62, 0x2000
	s_nop 0
	global_load_lds_dwordx4 v138, s[46:47]
	v_mov_b32_e32 v138, v1
	s_mov_b32 m0, s54
	v_lshl_add_u64 v[208:209], s[44:45], 0, v[138:139]
	v_lshl_add_u64 v[208:209], v[208:209], 0, s[12:13]
	v_mov_b32_e32 v138, v149
	global_load_lds_dwordx4 v[208:209], off
	s_mov_b32 m0, s55
	v_lshl_add_u64 v[208:209], s[44:45], 0, v[138:139]
	v_lshl_add_u64 v[208:209], v[208:209], 0, s[12:13]
	global_load_lds_dwordx4 v[208:209], off
	s_waitcnt vmcnt(8)
	s_waitcnt lgkmcnt(0)
	s_barrier
	s_waitcnt lgkmcnt(0)
	v_mfma_f32_16x16x32_bf16 v[62:65], v[130:133], v[174:177], v[62:65]
	v_mfma_f32_16x16x32_bf16 v[58:61], v[140:143], v[174:177], v[58:61]
	v_mfma_f32_16x16x32_bf16 v[46:49], v[130:133], v[182:185], v[46:49]
	v_mfma_f32_16x16x32_bf16 v[42:45], v[140:143], v[182:185], v[42:45]
	v_mfma_f32_16x16x32_bf16 v[30:33], v[130:133], v[190:193], v[30:33]
	v_mfma_f32_16x16x32_bf16 v[26:29], v[140:143], v[190:193], v[26:29]
	v_mfma_f32_16x16x32_bf16 v[14:17], v[130:133], v[200:203], v[14:17]
	v_mfma_f32_16x16x32_bf16 v[10:13], v[140:143], v[200:203], v[10:13]
	v_mfma_f32_16x16x32_bf16 v[62:65], v[134:137], v[178:181], v[62:65]
	v_mfma_f32_16x16x32_bf16 v[58:61], v[144:147], v[178:181], v[58:61]
	v_mfma_f32_16x16x32_bf16 v[46:49], v[134:137], v[186:189], v[46:49]
	v_mfma_f32_16x16x32_bf16 v[42:45], v[144:147], v[186:189], v[42:45]
	v_mfma_f32_16x16x32_bf16 v[30:33], v[134:137], v[194:197], v[30:33]
	v_mfma_f32_16x16x32_bf16 v[26:29], v[144:147], v[194:197], v[26:29]
	v_mfma_f32_16x16x32_bf16 v[14:17], v[134:137], v[204:207], v[14:17]
	v_mfma_f32_16x16x32_bf16 v[10:13], v[144:147], v[204:207], v[10:13]
	v_mfma_f32_16x16x32_bf16 v[54:57], v[158:161], v[174:177], v[54:57]
	v_mfma_f32_16x16x32_bf16 v[50:53], v[166:169], v[174:177], v[50:53]
	v_mfma_f32_16x16x32_bf16 v[38:41], v[158:161], v[182:185], v[38:41]
	v_mfma_f32_16x16x32_bf16 v[34:37], v[166:169], v[182:185], v[34:37]
	v_mfma_f32_16x16x32_bf16 v[22:25], v[158:161], v[190:193], v[22:25]
	v_mfma_f32_16x16x32_bf16 v[18:21], v[166:169], v[190:193], v[18:21]
	v_mfma_f32_16x16x32_bf16 v[6:9], v[158:161], v[200:203], v[6:9]
	v_mfma_f32_16x16x32_bf16 v[2:5], v[166:169], v[200:203], v[2:5]
	v_mfma_f32_16x16x32_bf16 v[54:57], v[162:165], v[178:181], v[54:57]
	v_mfma_f32_16x16x32_bf16 v[50:53], v[170:173], v[178:181], v[50:53]
	v_mfma_f32_16x16x32_bf16 v[38:41], v[162:165], v[186:189], v[38:41]
	v_mfma_f32_16x16x32_bf16 v[34:37], v[170:173], v[186:189], v[34:37]
	v_mfma_f32_16x16x32_bf16 v[22:25], v[162:165], v[194:197], v[22:25]
	v_mfma_f32_16x16x32_bf16 v[18:21], v[170:173], v[194:197], v[18:21]
	v_mfma_f32_16x16x32_bf16 v[6:9], v[162:165], v[204:207], v[6:9]
	v_mfma_f32_16x16x32_bf16 v[2:5], v[170:173], v[204:207], v[2:5]
	s_barrier
	s_add_i32 s61, s61, 2
	s_add_u32 s42, s42, 0x100
	s_addc_u32 s43, s43, 0
	s_add_u32 s35, s35, 0x100
	s_addc_u32 s60, s60, 0
	s_cmp_gt_u32 s61, 5
	s_cbranch_scc0 .LBB5_1405
	s_and_b64 vcc, exec, s[14:15]
	s_cbranch_vccz .LBB5_1408
	s_barrier

; #define PG8_STAGE(bufoff, gbase, voff) do { _Pragma("unroll") for (int _i = 0; _i < 2; ++_i) { unsigned _vo = (voff)[_i]; asm volatile("" : "+v"(_vo)); \
;         __builtin_amdgcn_global_load_lds((const unsigned*)((const char*)(gbase) + _vo), (LAS unsigned*)(lds + (bufoff) + ldsw + _i * 8192), 16, 0, 0); } } while (0)
; #define PG8_STAGE_A(bufoff, gbase, h, go) do { if constexpr (Sched::GATHER) { PG8_STAGE(bufoff, gbase, go[h]); } else { PG8_STAGE(bufoff, (gbase) + (h) * hstep, voffA); } } while (0)
; #define PG8_LDA(dst, b, h) do { _Pragma("unroll") for (int m = 0; m < 4; ++m) _Pragma("unroll") for (int k = 0; k < 2; ++k) dst[m][k] = *(const LAS bf16x8*)(lds + PG8_SA(b, h) + aoff + m * 2048 + k * 1024); } while (0)
; #define PG8_LDB(dst, b, h) do { _Pragma("unroll") for (int n = 0; n < 2; ++n) _Pragma("unroll") for (int k = 0; k < 2; ++k) dst[n][k] = *(const LAS bf16x8*)(lds + PG8_SB(b, h) + boff + n * 2048 + k * 1024); } while (0)
; #define PG8_WAIT_V(n) asm volatile("s_waitcnt vmcnt(" #n ")" ::: "memory")
; #define PG8_WAIT_L(n) asm volatile("s_waitcnt lgkmcnt(" #n ")" ::: "memory")
; #define PG8_BAR __builtin_amdgcn_s_barrier()
; #define PG8_SCHED __builtin_amdgcn_sched_barrier(0)
;     ...
;             PG8_LDB(B0, 0, 0); PG8_LDB(B1, 0, 1); PG8_SCHED; PG8_LDA(At, 0, 0); PG8_STAGE_A(PG8_SA(1, 1), a1, 1, gc);
;             if constexpr (Sched::GATHER) { if (last) {
; #pragma unroll
;                 for (int h = 0; h < 2; ++h)
; #pragma unroll
;                     for (int i = 0; i < 2; ++i) gc[h][i] = gn[h][i]; } }
;             PG8_WAIT_V(8); PG8_WAIT_L(0); PG8_BAR; PG8_MMA(0, 0, At, B0); PG8_MMA(0, 1, At, B1); PG8_BAR; PG8_SCHED;
;             PG8_LDA(At, 0, 1); PG8_STAGE(PG8_SB(0, 0), b2, voffB); PG8_STAGE(PG8_SB(0, 1), b2 + hstep, voffB); PG8_STAGE_A(PG8_SA(0, 0), a2, 0, gc);
;             PG8_WAIT_V(8); PG8_WAIT_L(0); PG8_BAR; PG8_MMA(1, 0, At, B0); PG8_MMA(1, 1, At, B1); PG8_BAR; PG8_SCHED;
;             PG8_LDB(B0, 1, 0); PG8_LDB(B1, 1, 1); PG8_SCHED; PG8_LDA(At, 1, 0); PG8_STAGE_A(PG8_SA(0, 1), a2, 1, gc);
;             PG8_WAIT_V(8); PG8_WAIT_L(0); PG8_BAR; PG8_MMA(0, 0, At, B0); PG8_MMA(0, 1, At, B1); PG8_BAR; PG8_SCHED;
.LBB5_1601:
	s_waitcnt vmcnt(8)
	s_add_u32 s40, s36, 0x80
	s_waitcnt lgkmcnt(0)
	s_addc_u32 s41, s37, 0
	s_and_b64 s[38:39], s[38:39], exec
	s_cselect_b32 s39, s19, s41
	s_cselect_b32 s38, s66, s40
	s_cselect_b32 s41, s67, s70
	s_cselect_b32 s40, s68, s69
	s_barrier
	s_waitcnt lgkmcnt(0)
	v_mfma_scale_f32_16x16x128_f8f6f4 v[190:193], v[18:25], v[58:65], v[190:193], v216, v216 op_sel_hi:[0,0,0]
	v_mfma_scale_f32_16x16x128_f8f6f4 v[186:189], v[26:33], v[58:65], v[186:189], v216, v216 op_sel_hi:[0,0,0]
	v_mfma_scale_f32_16x16x128_f8f6f4 v[174:177], v[18:25], v[50:57], v[174:177], v216, v216 op_sel_hi:[0,0,0]
	v_mfma_scale_f32_16x16x128_f8f6f4 v[170:173], v[26:33], v[50:57], v[170:173], v216, v216 op_sel_hi:[0,0,0]
	v_mfma_scale_f32_16x16x128_f8f6f4 v[158:161], v[18:25], v[42:49], v[158:161], v216, v216 op_sel_hi:[0,0,0]
	v_mfma_scale_f32_16x16x128_f8f6f4 v[154:157], v[26:33], v[42:49], v[154:157], v216, v216 op_sel_hi:[0,0,0]
	v_mfma_scale_f32_16x16x128_f8f6f4 v[142:145], v[18:25], v[34:41], v[142:145], v216, v216 op_sel_hi:[0,0,0]
	v_mfma_scale_f32_16x16x128_f8f6f4 v[138:141], v[26:33], v[34:41], v[138:141], v216, v216 op_sel_hi:[0,0,0]
	v_mfma_scale_f32_16x16x128_f8f6f4 v[182:185], v[2:9], v[58:65], v[182:185], v216, v216 op_sel_hi:[0,0,0]
	v_mfma_scale_f32_16x16x128_f8f6f4 v[178:181], v[10:17], v[58:65], v[178:181], v216, v216 op_sel_hi:[0,0,0]
	v_mfma_scale_f32_16x16x128_f8f6f4 v[166:169], v[2:9], v[50:57], v[166:169], v216, v216 op_sel_hi:[0,0,0]
	v_mfma_scale_f32_16x16x128_f8f6f4 v[162:165], v[10:17], v[50:57], v[162:165], v216, v216 op_sel_hi:[0,0,0]
	v_mfma_scale_f32_16x16x128_f8f6f4 v[150:153], v[2:9], v[42:49], v[150:153], v216, v216 op_sel_hi:[0,0,0]
	v_mfma_scale_f32_16x16x128_f8f6f4 v[146:149], v[10:17], v[42:49], v[146:149], v216, v216 op_sel_hi:[0,0,0]
	v_mfma_scale_f32_16x16x128_f8f6f4 v[134:137], v[2:9], v[34:41], v[134:137], v216, v216 op_sel_hi:[0,0,0]
	v_mfma_scale_f32_16x16x128_f8f6f4 v[130:133], v[10:17], v[34:41], v[130:133], v216, v216 op_sel_hi:[0,0,0]
	s_barrier
	v_mov_b32_e32 v194, v208
	s_mov_b32 m0, s45
	ds_read_b128 v[38:41], v215 offset:16384
	ds_read_b128 v[46:49], v215 offset:18432
	ds_read_b128 v[54:57], v215 offset:20480
	ds_read_b128 v[62:65], v215 offset:22528
	v_xor_b32_e32 v215, 64, v215
	ds_read_b128 v[34:37], v215 offset:16384
	ds_read_b128 v[42:45], v215 offset:18432
	ds_read_b128 v[50:53], v215 offset:20480
	ds_read_b128 v[58:61], v215 offset:22528
	s_add_u32 s72, s40, 0x40000
	global_load_lds_dwordx4 v194, s[40:41]
	v_mov_b32_e32 v194, v209
	s_mov_b32 m0, s46
	s_addc_u32 s73, s41, 0
	global_load_lds_dwordx4 v194, s[40:41]
	v_mov_b32_e32 v194, v208
	s_mov_b32 m0, s47
	s_nop 0
	global_load_lds_dwordx4 v194, s[72:73]
	v_mov_b32_e32 v194, v209
	s_mov_b32 m0, s48
	s_nop 0
	global_load_lds_dwordx4 v194, s[72:73]
	v_mov_b32_e32 v194, v205
	s_mov_b32 m0, s44
	s_nop 0
	global_load_lds_dwordx4 v194, s[38:39]
	v_mov_b32_e32 v194, v207
	s_mov_b32 m0, s49
	s_nop 0
	global_load_lds_dwordx4 v194, s[38:39]
	s_waitcnt vmcnt(8)
	s_waitcnt lgkmcnt(0)
	s_barrier
	s_waitcnt lgkmcnt(0)
	v_mfma_scale_f32_16x16x128_f8f6f4 v[126:129], v[18:25], v[34:41], v[126:129], v216, v216 op_sel_hi:[0,0,0]
	v_mfma_scale_f32_16x16x128_f8f6f4 v[122:125], v[26:33], v[34:41], v[122:125], v216, v216 op_sel_hi:[0,0,0]
	v_mfma_scale_f32_16x16x128_f8f6f4 v[110:113], v[18:25], v[42:49], v[110:113], v216, v216 op_sel_hi:[0,0,0]
	v_mfma_scale_f32_16x16x128_f8f6f4 v[106:109], v[26:33], v[42:49], v[106:109], v216, v216 op_sel_hi:[0,0,0]
	v_mfma_scale_f32_16x16x128_f8f6f4 v[94:97], v[18:25], v[50:57], v[94:97], v216, v216 op_sel_hi:[0,0,0]
	v_mfma_scale_f32_16x16x128_f8f6f4 v[90:93], v[26:33], v[50:57], v[90:93], v216, v216 op_sel_hi:[0,0,0]
	v_mfma_scale_f32_16x16x128_f8f6f4 v[78:81], v[18:25], v[58:65], v[78:81], v216, v216 op_sel_hi:[0,0,0]
	v_mfma_scale_f32_16x16x128_f8f6f4 v[74:77], v[26:33], v[58:65], v[74:77], v216, v216 op_sel_hi:[0,0,0]
	v_mfma_scale_f32_16x16x128_f8f6f4 v[118:121], v[2:9], v[34:41], v[118:121], v216, v216 op_sel_hi:[0,0,0]
	v_mfma_scale_f32_16x16x128_f8f6f4 v[114:117], v[10:17], v[34:41], v[114:117], v216, v216 op_sel_hi:[0,0,0]
	v_mfma_scale_f32_16x16x128_f8f6f4 v[102:105], v[2:9], v[42:49], v[102:105], v216, v216 op_sel_hi:[0,0,0]
	v_mfma_scale_f32_16x16x128_f8f6f4 v[98:101], v[10:17], v[42:49], v[98:101], v216, v216 op_sel_hi:[0,0,0]
	v_mfma_scale_f32_16x16x128_f8f6f4 v[86:89], v[2:9], v[50:57], v[86:89], v216, v216 op_sel_hi:[0,0,0]
	v_mfma_scale_f32_16x16x128_f8f6f4 v[82:85], v[10:17], v[50:57], v[82:85], v216, v216 op_sel_hi:[0,0,0]
	v_mfma_scale_f32_16x16x128_f8f6f4 v[70:73], v[2:9], v[58:65], v[70:73], v216, v216 op_sel_hi:[0,0,0]
	v_mfma_scale_f32_16x16x128_f8f6f4 v[66:69], v[10:17], v[58:65], v[66:69], v216, v216 op_sel_hi:[0,0,0]
	s_barrier
	s_add_i32 s72, 0, 0x18000
	s_add_i32 s73, 0, 0x1c000
	v_add_u32_e32 v14, s72, v212
	v_add_u32_e32 v30, s73, v212
	ds_read_b128 v[2:5], v14
	ds_read_b128 v[10:13], v14 offset:2048
	v_xor_b32_e32 v14, 64, v14
	ds_read_b128 v[6:9], v14
	ds_read_b128 v[14:17], v14 offset:2048
	ds_read_b128 v[18:21], v30
	ds_read_b128 v[26:29], v30 offset:2048
	v_xor_b32_e32 v30, 64, v30
	ds_read_b128 v[22:25], v30
	ds_read_b128 v[30:33], v30 offset:2048
	v_mov_b32_e32 v194, v204
	s_mov_b32 m0, s50
	ds_read_b128 v[34:37], v215 offset:32768
	ds_read_b128 v[42:45], v215 offset:34816
	ds_read_b128 v[50:53], v215 offset:36864
	ds_read_b128 v[58:61], v215 offset:38912
	v_xor_b32_e32 v215, 64, v215
	ds_read_b128 v[38:41], v215 offset:32768
	ds_read_b128 v[46:49], v215 offset:34816
	ds_read_b128 v[54:57], v215 offset:36864
	ds_read_b128 v[62:65], v215 offset:38912
	s_nop 0
	global_load_lds_dwordx4 v194, s[38:39]
	v_mov_b32_e32 v194, v206
	s_mov_b32 m0, s51
	s_nop 0
	global_load_lds_dwordx4 v194, s[38:39]
	s_waitcnt vmcnt(8)
	s_waitcnt lgkmcnt(0)
	s_barrier
; #define PG8_STAGE(bufoff, gbase, voff) do { _Pragma("unroll") for (int _i = 0; _i < 2; ++_i) { unsigned _vo = (voff)[_i]; asm volatile("" : "+v"(_vo)); \
;         __builtin_amdgcn_global_load_lds((const unsigned*)((const char*)(gbase) + _vo), (LAS unsigned*)(lds + (bufoff) + ldsw + _i * 8192), 16, 0, 0); } } while (0)
; #define PG8_STAGE_A(bufoff, gbase, h, go) do { if constexpr (Sched::GATHER) { PG8_STAGE(bufoff, gbase, go[h]); } else { PG8_STAGE(bufoff, (gbase) + (h) * hstep, voffA); } } while (0)
; #define PG8_LDA(dst, b, h) do { _Pragma("unroll") for (int m = 0; m < 4; ++m) _Pragma("unroll") for (int k = 0; k < 2; ++k) dst[m][k] = *(const LAS bf16x8*)(lds + PG8_SA(b, h) + aoff + m * 2048 + k * 1024); } while (0)
; #define PG8_LDB(dst, b, h) do { _Pragma("unroll") for (int n = 0; n < 2; ++n) _Pragma("unroll") for (int k = 0; k < 2; ++k) dst[n][k] = *(const LAS bf16x8*)(lds + PG8_SB(b, h) + boff + n * 2048 + k * 1024); } while (0)
; #define PG8_WAIT_V(n) asm volatile("s_waitcnt vmcnt(" #n ")" ::: "memory")
; #define PG8_WAIT_L(n) asm volatile("s_waitcnt lgkmcnt(" #n ")" ::: "memory")
; #define PG8_BAR __builtin_amdgcn_s_barrier()
; #define PG8_SCHED __builtin_amdgcn_sched_barrier(0)
;     ...
;             PG8_LDB(B0, 1, 0); PG8_LDB(B1, 1, 1); PG8_SCHED; PG8_LDA(At, 1, 0); PG8_STAGE_A(PG8_SA(0, 1), a2, 1, gc);
;             PG8_WAIT_V(8); PG8_WAIT_L(0); PG8_BAR; PG8_MMA(0, 0, At, B0); PG8_MMA(0, 1, At, B1); PG8_BAR; PG8_SCHED;
;             PG8_LDA(At, 1, 1); PG8_STAGE(PG8_SB(1, 0), b3, voffB); PG8_STAGE(PG8_SB(1, 1), b3 + hstep, voffB); PG8_STAGE_A(PG8_SA(1, 0), a3, 0, gc);
;             PG8_WAIT_V(8); PG8_WAIT_L(0); PG8_BAR; PG8_MMA(1, 0, At, B0); PG8_MMA(1, 1, At, B1); PG8_BAR; PG8_SCHED;
;         }
	s_waitcnt lgkmcnt(0)
	v_mfma_scale_f32_16x16x128_f8f6f4 v[190:193], v[2:9], v[34:41], v[190:193], v216, v216 op_sel_hi:[0,0,0]
	v_mfma_scale_f32_16x16x128_f8f6f4 v[186:189], v[10:17], v[34:41], v[186:189], v216, v216 op_sel_hi:[0,0,0]
	v_mfma_scale_f32_16x16x128_f8f6f4 v[174:177], v[2:9], v[42:49], v[174:177], v216, v216 op_sel_hi:[0,0,0]
	v_mfma_scale_f32_16x16x128_f8f6f4 v[170:173], v[10:17], v[42:49], v[170:173], v216, v216 op_sel_hi:[0,0,0]
	v_mfma_scale_f32_16x16x128_f8f6f4 v[158:161], v[2:9], v[50:57], v[158:161], v216, v216 op_sel_hi:[0,0,0]
	v_mfma_scale_f32_16x16x128_f8f6f4 v[154:157], v[10:17], v[50:57], v[154:157], v216, v216 op_sel_hi:[0,0,0]
	v_mfma_scale_f32_16x16x128_f8f6f4 v[142:145], v[2:9], v[58:65], v[142:145], v216, v216 op_sel_hi:[0,0,0]
	v_mfma_scale_f32_16x16x128_f8f6f4 v[138:141], v[10:17], v[58:65], v[138:141], v216, v216 op_sel_hi:[0,0,0]
	v_mfma_scale_f32_16x16x128_f8f6f4 v[182:185], v[18:25], v[34:41], v[182:185], v216, v216 op_sel_hi:[0,0,0]
	v_mfma_scale_f32_16x16x128_f8f6f4 v[178:181], v[26:33], v[34:41], v[178:181], v216, v216 op_sel_hi:[0,0,0]
	v_mfma_scale_f32_16x16x128_f8f6f4 v[166:169], v[18:25], v[42:49], v[166:169], v216, v216 op_sel_hi:[0,0,0]
	v_mfma_scale_f32_16x16x128_f8f6f4 v[162:165], v[26:33], v[42:49], v[162:165], v216, v216 op_sel_hi:[0,0,0]
	v_mfma_scale_f32_16x16x128_f8f6f4 v[150:153], v[18:25], v[50:57], v[150:153], v216, v216 op_sel_hi:[0,0,0]
	v_mfma_scale_f32_16x16x128_f8f6f4 v[146:149], v[26:33], v[50:57], v[146:149], v216, v216 op_sel_hi:[0,0,0]
	v_mfma_scale_f32_16x16x128_f8f6f4 v[134:137], v[18:25], v[58:65], v[134:137], v216, v216 op_sel_hi:[0,0,0]
	v_mfma_scale_f32_16x16x128_f8f6f4 v[130:133], v[26:33], v[58:65], v[130:133], v216, v216 op_sel_hi:[0,0,0]
	s_barrier
	v_mov_b32_e32 v194, v208
	ds_read_b128 v[38:41], v215 offset:49152
	ds_read_b128 v[46:49], v215 offset:51200
	ds_read_b128 v[54:57], v215 offset:53248
	ds_read_b128 v[62:65], v215 offset:55296
	v_xor_b32_e32 v215, 64, v215
	ds_read_b128 v[34:37], v215 offset:49152
	ds_read_b128 v[42:45], v215 offset:51200
	ds_read_b128 v[50:53], v215 offset:53248
	ds_read_b128 v[58:61], v215 offset:55296
	s_add_i32 s72, s72, s43
	v_lshl_add_u64 v[222:223], s[40:41], 0, v[194:195]
	v_lshl_add_u64 v[222:223], v[222:223], 0, s[10:11]
	s_mov_b32 m0, s72
	v_mov_b32_e32 v194, v209
	global_load_lds_dwordx4 v[222:223], off
	s_add_i32 m0, s72, 0x2000
	s_nop 0
	v_lshl_add_u64 v[222:223], s[40:41], 0, v[194:195]
	s_add_u32 s40, s40, 0x40080
	v_lshl_add_u64 v[222:223], v[222:223], 0, s[10:11]
	s_addc_u32 s41, s41, 0
	v_mov_b32_e32 v194, v208
	s_add_i32 s72, s73, s43
	global_load_lds_dwordx4 v[222:223], off
	s_mov_b32 m0, s72
	s_nop 0
	global_load_lds_dwordx4 v194, s[40:41]
	v_mov_b32_e32 v194, v209
	s_add_i32 m0, s72, 0x2000
	s_nop 0
	global_load_lds_dwordx4 v194, s[40:41]
	v_mov_b32_e32 v194, v205
	s_mov_b32 m0, s54
	v_lshl_add_u64 v[222:223], s[38:39], 0, v[194:195]
	v_lshl_add_u64 v[222:223], v[222:223], 0, s[10:11]
	v_mov_b32_e32 v194, v207
	global_load_lds_dwordx4 v[222:223], off
	s_mov_b32 m0, s55
	v_lshl_add_u64 v[222:223], s[38:39], 0, v[194:195]
	v_lshl_add_u64 v[222:223], v[222:223], 0, s[10:11]
	global_load_lds_dwordx4 v[222:223], off
	s_waitcnt vmcnt(8)
	s_waitcnt lgkmcnt(0)
	s_barrier
	s_waitcnt lgkmcnt(0)
	v_mfma_scale_f32_16x16x128_f8f6f4 v[126:129], v[2:9], v[34:41], v[126:129], v216, v216 op_sel_hi:[0,0,0]
	v_mfma_scale_f32_16x16x128_f8f6f4 v[122:125], v[10:17], v[34:41], v[122:125], v216, v216 op_sel_hi:[0,0,0]
	v_mfma_scale_f32_16x16x128_f8f6f4 v[110:113], v[2:9], v[42:49], v[110:113], v216, v216 op_sel_hi:[0,0,0]
	v_mfma_scale_f32_16x16x128_f8f6f4 v[106:109], v[10:17], v[42:49], v[106:109], v216, v216 op_sel_hi:[0,0,0]
	v_mfma_scale_f32_16x16x128_f8f6f4 v[94:97], v[2:9], v[50:57], v[94:97], v216, v216 op_sel_hi:[0,0,0]
	v_mfma_scale_f32_16x16x128_f8f6f4 v[90:93], v[10:17], v[50:57], v[90:93], v216, v216 op_sel_hi:[0,0,0]
	v_mfma_scale_f32_16x16x128_f8f6f4 v[78:81], v[2:9], v[58:65], v[78:81], v216, v216 op_sel_hi:[0,0,0]
	v_mfma_scale_f32_16x16x128_f8f6f4 v[74:77], v[10:17], v[58:65], v[74:77], v216, v216 op_sel_hi:[0,0,0]
	v_mfma_scale_f32_16x16x128_f8f6f4 v[118:121], v[18:25], v[34:41], v[118:121], v216, v216 op_sel_hi:[0,0,0]
	v_mfma_scale_f32_16x16x128_f8f6f4 v[114:117], v[26:33], v[34:41], v[114:117], v216, v216 op_sel_hi:[0,0,0]
	v_mfma_scale_f32_16x16x128_f8f6f4 v[102:105], v[18:25], v[42:49], v[102:105], v216, v216 op_sel_hi:[0,0,0]
	v_mfma_scale_f32_16x16x128_f8f6f4 v[98:101], v[26:33], v[42:49], v[98:101], v216, v216 op_sel_hi:[0,0,0]
	v_mfma_scale_f32_16x16x128_f8f6f4 v[86:89], v[18:25], v[50:57], v[86:89], v216, v216 op_sel_hi:[0,0,0]
	v_mfma_scale_f32_16x16x128_f8f6f4 v[82:85], v[26:33], v[50:57], v[82:85], v216, v216 op_sel_hi:[0,0,0]
	v_mfma_scale_f32_16x16x128_f8f6f4 v[70:73], v[18:25], v[58:65], v[70:73], v216, v216 op_sel_hi:[0,0,0]
	v_mfma_scale_f32_16x16x128_f8f6f4 v[66:69], v[26:33], v[58:65], v[66:69], v216, v216 op_sel_hi:[0,0,0]
	s_barrier
	s_add_i32 s71, s71, 2
	s_add_u32 s36, s36, 0x100
	s_addc_u32 s37, s37, 0
	s_add_u32 s69, s69, 0x100
	s_addc_u32 s70, s70, 0
	s_cmp_gt_u32 s71, 13
	s_cbranch_scc1 .LBB5_1604

; #define PG8_STAGE(bufoff, gbase, voff) do { _Pragma("unroll") for (int _i = 0; _i < 2; ++_i) { unsigned _vo = (voff)[_i]; asm volatile("" : "+v"(_vo)); \
;         __builtin_amdgcn_global_load_lds((const unsigned*)((const char*)(gbase) + _vo), (LAS unsigned*)(lds + (bufoff) + ldsw + _i * 8192), 16, 0, 0); } } while (0)
; #define PG8_STAGE_A(bufoff, gbase, h, go) do { if constexpr (Sched::GATHER) { PG8_STAGE(bufoff, gbase, go[h]); } else { PG8_STAGE(bufoff, (gbase) + (h) * hstep, voffA); } } while (0)
; #define PG8_LDA(dst, b, h) do { _Pragma("unroll") for (int m = 0; m < 4; ++m) _Pragma("unroll") for (int k = 0; k < 2; ++k) dst[m][k] = *(const LAS bf16x8*)(lds + PG8_SA(b, h) + aoff + m * 2048 + k * 1024); } while (0)
; #define PG8_LDB(dst, b, h) do { _Pragma("unroll") for (int n = 0; n < 2; ++n) _Pragma("unroll") for (int k = 0; k < 2; ++k) dst[n][k] = *(const LAS bf16x8*)(lds + PG8_SB(b, h) + boff + n * 2048 + k * 1024); } while (0)
; #define PG8_WAIT_V(n) asm volatile("s_waitcnt vmcnt(" #n ")" ::: "memory")
; #define PG8_WAIT_L(n) asm volatile("s_waitcnt lgkmcnt(" #n ")" ::: "memory")
; #define PG8_BAR __builtin_amdgcn_s_barrier()
; #define PG8_SCHED __builtin_amdgcn_sched_barrier(0)
;     ...
;             PG8_LDB(B0, 0, 0); PG8_LDB(B1, 0, 1); PG8_SCHED; PG8_LDA(At, 0, 0); PG8_STAGE_A(PG8_SA(1, 1), a1, 1, gc);
;             if constexpr (Sched::GATHER) { if (last) {
; #pragma unroll
;                 for (int h = 0; h < 2; ++h)
; #pragma unroll
;                     for (int i = 0; i < 2; ++i) gc[h][i] = gn[h][i]; } }
;             PG8_WAIT_V(8); PG8_WAIT_L(0); PG8_BAR; PG8_MMA(0, 0, At, B0); PG8_MMA(0, 1, At, B1); PG8_BAR; PG8_SCHED;
;             PG8_LDA(At, 0, 1); PG8_STAGE(PG8_SB(0, 0), b2, voffB); PG8_STAGE(PG8_SB(0, 1), b2 + hstep, voffB); PG8_STAGE_A(PG8_SA(0, 0), a2, 0, gc);
;             PG8_WAIT_V(8); PG8_WAIT_L(0); PG8_BAR; PG8_MMA(1, 0, At, B0); PG8_MMA(1, 1, At, B1); PG8_BAR; PG8_SCHED;
.LBB5_1678:
	ds_read_b128 v[130:133], v146
	ds_read_b128 v[152:155], v146 offset:2048
	v_xor_b32_e32 v146, 64, v146
	ds_read_b128 v[134:137], v146
	ds_read_b128 v[156:159], v146 offset:2048
	v_xor_b32_e32 v146, 64, v146
	ds_read_b128 v[160:163], v147
	ds_read_b128 v[168:171], v147 offset:2048
	v_xor_b32_e32 v147, 64, v147
	ds_read_b128 v[164:167], v147
	ds_read_b128 v[172:175], v147 offset:2048
	v_xor_b32_e32 v147, 64, v147
	s_add_u32 s34, s18, 0xfffc0080
	s_addc_u32 s35, s19, -1
	s_cmp_eq_u32 s64, 12
	s_cselect_b32 s35, s58, s35
	s_cselect_b32 s34, s59, s34
	s_cselect_b32 s37, s60, s63
	s_cselect_b32 s36, s61, s62
	v_mov_b32_e32 v138, v1
	ds_read_b128 v[176:179], v148
	ds_read_b128 v[184:187], v148 offset:2048
	ds_read_b128 v[200:203], v148 offset:4096
	ds_read_b128 v[208:211], v148 offset:6144
	v_xor_b32_e32 v148, 64, v148
	ds_read_b128 v[180:183], v148
	ds_read_b128 v[188:191], v148 offset:2048
	ds_read_b128 v[204:207], v148 offset:4096
	ds_read_b128 v[212:215], v148 offset:6144
	s_add_u32 s98, s62, 0x3f80
	s_addc_u32 s99, s63, 0
	s_add_i32 s100, s40, 0x1c000
	v_mov_b32_e32 v138, v140
	s_mov_b32 m0, s100
	s_nop 0
	global_load_lds_dwordx4 v138, s[98:99]
	v_mov_b32_e32 v138, v142
	s_add_i32 m0, s100, 0x2000
	s_nop 0
	global_load_lds_dwordx4 v138, s[98:99]
	v_mov_b32_e32 v138, v1
	s_add_i32 m0, s41, 0xc000
	s_nop 0
	global_load_lds_dwordx4 v138, s[18:19]
	v_mov_b32_e32 v138, v141
	s_add_i32 m0, s41, 0xe000
	s_nop 0
	global_load_lds_dwordx4 v138, s[18:19]
	s_waitcnt vmcnt(8)
	s_waitcnt lgkmcnt(0)
	s_barrier
	s_waitcnt lgkmcnt(0)
	v_mfma_scale_f32_16x16x128_f8f6f4 v[126:129], v[130:137], v[176:183], v[126:129], v149, v149 op_sel_hi:[0,0,0]
	v_mfma_scale_f32_16x16x128_f8f6f4 v[122:125], v[152:159], v[176:183], v[122:125], v149, v149 op_sel_hi:[0,0,0]
	v_mfma_scale_f32_16x16x128_f8f6f4 v[118:121], v[130:137], v[184:191], v[118:121], v149, v149 op_sel_hi:[0,0,0]
	v_mfma_scale_f32_16x16x128_f8f6f4 v[114:117], v[152:159], v[184:191], v[114:117], v149, v149 op_sel_hi:[0,0,0]
	v_mfma_scale_f32_16x16x128_f8f6f4 v[110:113], v[130:137], v[200:207], v[110:113], v149, v149 op_sel_hi:[0,0,0]
	v_mfma_scale_f32_16x16x128_f8f6f4 v[106:109], v[152:159], v[200:207], v[106:109], v149, v149 op_sel_hi:[0,0,0]
	v_mfma_scale_f32_16x16x128_f8f6f4 v[102:105], v[130:137], v[208:215], v[102:105], v149, v149 op_sel_hi:[0,0,0]
	v_mfma_scale_f32_16x16x128_f8f6f4 v[98:101], v[152:159], v[208:215], v[98:101], v149, v149 op_sel_hi:[0,0,0]
	v_mfma_scale_f32_16x16x128_f8f6f4 v[192:195], v[160:167], v[176:183], v[70:73], v149, v149 op_sel_hi:[0,0,0]
	v_mfma_scale_f32_16x16x128_f8f6f4 v[176:179], v[168:175], v[176:183], v[66:69], v149, v149 op_sel_hi:[0,0,0]
	v_mfma_scale_f32_16x16x128_f8f6f4 v[180:183], v[160:167], v[184:191], v[54:57], v149, v149 op_sel_hi:[0,0,0]
	v_mfma_scale_f32_16x16x128_f8f6f4 v[184:187], v[168:175], v[184:191], v[50:53], v149, v149 op_sel_hi:[0,0,0]
	v_mfma_scale_f32_16x16x128_f8f6f4 v[188:191], v[160:167], v[200:207], v[46:49], v149, v149 op_sel_hi:[0,0,0]
	v_mfma_scale_f32_16x16x128_f8f6f4 v[200:203], v[168:175], v[200:207], v[42:45], v149, v149 op_sel_hi:[0,0,0]
	v_mfma_scale_f32_16x16x128_f8f6f4 v[204:207], v[160:167], v[208:215], v[38:41], v149, v149 op_sel_hi:[0,0,0]
	v_mfma_scale_f32_16x16x128_f8f6f4 v[208:211], v[168:175], v[208:215], v[34:37], v149, v149 op_sel_hi:[0,0,0]
	s_barrier
	v_mov_b32_e32 v138, v140
	s_add_i32 s65, s50, s40
	s_nop 2
	ds_read_b128 v[38:41], v148 offset:16384
	ds_read_b128 v[46:49], v148 offset:18432
	ds_read_b128 v[54:57], v148 offset:20480
	ds_read_b128 v[70:73], v148 offset:22528
	v_xor_b32_e32 v148, 64, v148
	ds_read_b128 v[34:37], v148 offset:16384
	ds_read_b128 v[42:45], v148 offset:18432
	ds_read_b128 v[50:53], v148 offset:20480
	ds_read_b128 v[66:69], v148 offset:22528
	s_mov_b32 m0, s65
	s_nop 0
	global_load_lds_dwordx4 v138, s[36:37]
	v_mov_b32_e32 v138, v142
	s_add_i32 m0, s65, 0x2000
	s_nop 0
	global_load_lds_dwordx4 v138, s[36:37]
	v_mov_b32_e32 v138, v1
	s_mov_b32 m0, s41
	s_nop 0
	global_load_lds_dwordx4 v138, s[34:35]
	v_mov_b32_e32 v138, v141
	s_mov_b32 m0, s42
	s_nop 0
	global_load_lds_dwordx4 v138, s[34:35]
	s_waitcnt vmcnt(6)
	s_waitcnt lgkmcnt(0)
	s_barrier
	s_waitcnt lgkmcnt(0)
	v_mfma_scale_f32_16x16x128_f8f6f4 v[94:97], v[130:137], v[34:41], v[94:97], v149, v149 op_sel_hi:[0,0,0]
	v_mfma_scale_f32_16x16x128_f8f6f4 v[90:93], v[152:159], v[34:41], v[90:93], v149, v149 op_sel_hi:[0,0,0]
	v_mfma_scale_f32_16x16x128_f8f6f4 v[86:89], v[130:137], v[42:49], v[86:89], v149, v149 op_sel_hi:[0,0,0]
	v_mfma_scale_f32_16x16x128_f8f6f4 v[82:85], v[152:159], v[42:49], v[82:85], v149, v149 op_sel_hi:[0,0,0]
	v_mfma_scale_f32_16x16x128_f8f6f4 v[78:81], v[130:137], v[50:57], v[78:81], v149, v149 op_sel_hi:[0,0,0]
	v_mfma_scale_f32_16x16x128_f8f6f4 v[74:77], v[152:159], v[50:57], v[74:77], v149, v149 op_sel_hi:[0,0,0]
	v_mfma_scale_f32_16x16x128_f8f6f4 v[212:215], v[130:137], v[66:73], v[62:65], v149, v149 op_sel_hi:[0,0,0]
	v_mfma_scale_f32_16x16x128_f8f6f4 v[216:219], v[152:159], v[66:73], v[58:61], v149, v149 op_sel_hi:[0,0,0]
	v_mfma_scale_f32_16x16x128_f8f6f4 v[220:223], v[160:167], v[34:41], v[30:33], v149, v149 op_sel_hi:[0,0,0]
	v_mfma_scale_f32_16x16x128_f8f6f4 v[224:227], v[168:175], v[34:41], v[26:29], v149, v149 op_sel_hi:[0,0,0]
	v_mfma_scale_f32_16x16x128_f8f6f4 v[228:231], v[160:167], v[42:49], v[22:25], v149, v149 op_sel_hi:[0,0,0]
	v_mfma_scale_f32_16x16x128_f8f6f4 v[232:235], v[168:175], v[42:49], v[18:21], v149, v149 op_sel_hi:[0,0,0]
	v_mfma_scale_f32_16x16x128_f8f6f4 v[236:239], v[160:167], v[50:57], v[14:17], v149, v149 op_sel_hi:[0,0,0]
	v_mfma_scale_f32_16x16x128_f8f6f4 v[240:243], v[168:175], v[50:57], v[10:13], v149, v149 op_sel_hi:[0,0,0]
	v_mfma_scale_f32_16x16x128_f8f6f4 v[244:247], v[160:167], v[66:73], v[6:9], v149, v149 op_sel_hi:[0,0,0]
	v_mfma_scale_f32_16x16x128_f8f6f4 v[248:251], v[168:175], v[66:73], v[2:5], v149, v149 op_sel_hi:[0,0,0]
	s_barrier
; #define PG8_STAGE(bufoff, gbase, voff) do { _Pragma("unroll") for (int _i = 0; _i < 2; ++_i) { unsigned _vo = (voff)[_i]; asm volatile("" : "+v"(_vo)); \
;         __builtin_amdgcn_global_load_lds((const unsigned*)((const char*)(gbase) + _vo), (LAS unsigned*)(lds + (bufoff) + ldsw + _i * 8192), 16, 0, 0); } } while (0)
; #define PG8_STAGE_A(bufoff, gbase, h, go) do { if constexpr (Sched::GATHER) { PG8_STAGE(bufoff, gbase, go[h]); } else { PG8_STAGE(bufoff, (gbase) + (h) * hstep, voffA); } } while (0)
; #define PG8_LDA(dst, b, h) do { _Pragma("unroll") for (int m = 0; m < 4; ++m) _Pragma("unroll") for (int k = 0; k < 2; ++k) dst[m][k] = *(const LAS bf16x8*)(lds + PG8_SA(b, h) + aoff + m * 2048 + k * 1024); } while (0)
; #define PG8_LDB(dst, b, h) do { _Pragma("unroll") for (int n = 0; n < 2; ++n) _Pragma("unroll") for (int k = 0; k < 2; ++k) dst[n][k] = *(const LAS bf16x8*)(lds + PG8_SB(b, h) + boff + n * 2048 + k * 1024); } while (0)
; #define PG8_WAIT_V(n) asm volatile("s_waitcnt vmcnt(" #n ")" ::: "memory")
; #define PG8_WAIT_L(n) asm volatile("s_waitcnt lgkmcnt(" #n ")" ::: "memory")
; #define PG8_BAR __builtin_amdgcn_s_barrier()
; #define PG8_SCHED __builtin_amdgcn_sched_barrier(0)
;     ...
;             PG8_LDB(B0, 1, 0); PG8_LDB(B1, 1, 1); PG8_SCHED; PG8_LDA(At, 1, 0); PG8_STAGE_A(PG8_SA(0, 1), a2, 1, gc);
;             PG8_WAIT_V(8); PG8_WAIT_L(0); PG8_BAR; PG8_MMA(0, 0, At, B0); PG8_MMA(0, 1, At, B1); PG8_BAR; PG8_SCHED;
;             PG8_LDA(At, 1, 1); PG8_STAGE(PG8_SB(1, 0), b3, voffB); PG8_STAGE(PG8_SB(1, 1), b3 + hstep, voffB); PG8_STAGE_A(PG8_SA(1, 0), a3, 0, gc);
;             PG8_WAIT_V(8); PG8_WAIT_L(0); PG8_BAR; PG8_MMA(1, 0, At, B0); PG8_MMA(1, 1, At, B1); PG8_BAR; PG8_SCHED;
;         }
	s_add_i32 s65, 0, 0x18000
	s_add_i32 s68, 0, 0x1c000
	v_add_u32_e32 v14, s65, v145
	v_add_u32_e32 v18, s68, v145
	s_nop 0
	ds_read_b128 v[2:5], v14
	ds_read_b128 v[10:13], v14 offset:2048
	v_xor_b32_e32 v14, 64, v14
	ds_read_b128 v[6:9], v14
	ds_read_b128 v[14:17], v14 offset:2048
	ds_read_b128 v[130:133], v18
	ds_read_b128 v[152:155], v18 offset:2048
	v_xor_b32_e32 v18, 64, v18
	ds_read_b128 v[134:137], v18
	ds_read_b128 v[156:159], v18 offset:2048
	s_add_u32 s66, s34, 0x40000
	v_mov_b32_e32 v42, v1
	s_mov_b32 m0, s43
	ds_read_b128 v[18:21], v148 offset:32768
	ds_read_b128 v[26:29], v148 offset:34816
	ds_read_b128 v[34:37], v148 offset:36864
	ds_read_b128 v[58:61], v148 offset:38912
	v_xor_b32_e32 v148, 64, v148
	ds_read_b128 v[22:25], v148 offset:32768
	ds_read_b128 v[30:33], v148 offset:34816
	ds_read_b128 v[38:41], v148 offset:36864
	ds_read_b128 v[62:65], v148 offset:38912
	s_addc_u32 s67, s35, 0
	s_add_u32 s98, s36, 0x4000
	s_addc_u32 s99, s37, 0
	s_add_i32 s100, s51, s40
	v_mov_b32_e32 v42, v140
	s_mov_b32 m0, s100
	s_nop 0
	global_load_lds_dwordx4 v42, s[98:99]
	v_mov_b32_e32 v42, v142
	s_add_i32 m0, s100, 0x2000
	s_nop 0
	global_load_lds_dwordx4 v42, s[98:99]
	v_mov_b32_e32 v42, v1
	s_mov_b32 m0, s43
	s_nop 0
	global_load_lds_dwordx4 v42, s[66:67]
	v_mov_b32_e32 v42, v141
	s_mov_b32 m0, s44
	s_nop 0
	global_load_lds_dwordx4 v42, s[66:67]
	s_waitcnt vmcnt(8)
	s_waitcnt lgkmcnt(0)
	s_barrier
	s_waitcnt lgkmcnt(0)
	v_mfma_scale_f32_16x16x128_f8f6f4 v[126:129], v[2:9], v[18:25], v[126:129], v149, v149 op_sel_hi:[0,0,0]
	v_mfma_scale_f32_16x16x128_f8f6f4 v[122:125], v[10:17], v[18:25], v[122:125], v149, v149 op_sel_hi:[0,0,0]
	v_mfma_scale_f32_16x16x128_f8f6f4 v[118:121], v[2:9], v[26:33], v[118:121], v149, v149 op_sel_hi:[0,0,0]
	v_mfma_scale_f32_16x16x128_f8f6f4 v[114:117], v[10:17], v[26:33], v[114:117], v149, v149 op_sel_hi:[0,0,0]
	v_mfma_scale_f32_16x16x128_f8f6f4 v[110:113], v[2:9], v[34:41], v[110:113], v149, v149 op_sel_hi:[0,0,0]
	v_mfma_scale_f32_16x16x128_f8f6f4 v[106:109], v[10:17], v[34:41], v[106:109], v149, v149 op_sel_hi:[0,0,0]
	v_mfma_scale_f32_16x16x128_f8f6f4 v[102:105], v[2:9], v[58:65], v[102:105], v149, v149 op_sel_hi:[0,0,0]
	v_mfma_scale_f32_16x16x128_f8f6f4 v[98:101], v[10:17], v[58:65], v[98:101], v149, v149 op_sel_hi:[0,0,0]
	v_mfma_scale_f32_16x16x128_f8f6f4 v[70:73], v[130:137], v[18:25], v[192:195], v149, v149 op_sel_hi:[0,0,0]
	v_mfma_scale_f32_16x16x128_f8f6f4 v[66:69], v[152:159], v[18:25], v[176:179], v149, v149 op_sel_hi:[0,0,0]
	v_mfma_scale_f32_16x16x128_f8f6f4 v[54:57], v[130:137], v[26:33], v[180:183], v149, v149 op_sel_hi:[0,0,0]
	v_mfma_scale_f32_16x16x128_f8f6f4 v[50:53], v[152:159], v[26:33], v[184:187], v149, v149 op_sel_hi:[0,0,0]
	v_mfma_scale_f32_16x16x128_f8f6f4 v[46:49], v[130:137], v[34:41], v[188:191], v149, v149 op_sel_hi:[0,0,0]
	v_mfma_scale_f32_16x16x128_f8f6f4 v[42:45], v[152:159], v[34:41], v[200:203], v149, v149 op_sel_hi:[0,0,0]
	v_mfma_scale_f32_16x16x128_f8f6f4 v[38:41], v[130:137], v[58:65], v[204:207], v149, v149 op_sel_hi:[0,0,0]
	v_mfma_scale_f32_16x16x128_f8f6f4 v[34:37], v[152:159], v[58:65], v[208:211], v149, v149 op_sel_hi:[0,0,0]
	s_barrier
	v_mov_b32_e32 v138, v140
	ds_read_b128 v[22:25], v148 offset:49152
	ds_read_b128 v[164:167], v148 offset:51200
	ds_read_b128 v[172:175], v148 offset:53248
	ds_read_b128 v[180:183], v148 offset:55296
	v_xor_b32_e32 v148, 64, v148
	ds_read_b128 v[18:21], v148 offset:49152
	ds_read_b128 v[160:163], v148 offset:51200
	ds_read_b128 v[168:171], v148 offset:53248
	ds_read_b128 v[176:179], v148 offset:55296
	s_add_i32 s65, s65, s40
	v_lshl_add_u64 v[26:27], s[36:37], 0, v[138:139]
	v_lshl_add_u64 v[26:27], v[26:27], 0, s[6:7]
	s_mov_b32 m0, s65
	v_mov_b32_e32 v138, v142
	global_load_lds_dwordx4 v[26:27], off
	s_add_i32 m0, s65, 0x2000
	v_lshl_add_u64 v[26:27], s[36:37], 0, v[138:139]
	v_lshl_add_u64 v[26:27], v[26:27], 0, s[6:7]
	s_add_u32 s36, s36, 0x4080
	global_load_lds_dwordx4 v[26:27], off
	s_addc_u32 s37, s37, 0
	v_mov_b32_e32 v138, v1
	s_mov_b32 m0, s47
	v_lshl_add_u64 v[26:27], s[34:35], 0, v[138:139]
	v_lshl_add_u64 v[26:27], v[26:27], 0, s[6:7]
	v_mov_b32_e32 v138, v141
	global_load_lds_dwordx4 v[26:27], off
	s_mov_b32 m0, s48
	v_lshl_add_u64 v[26:27], s[34:35], 0, v[138:139]
	v_lshl_add_u64 v[26:27], v[26:27], 0, s[6:7]
	global_load_lds_dwordx4 v[26:27], off
	s_waitcnt vmcnt(6)
	s_waitcnt lgkmcnt(0)
	s_barrier
	s_waitcnt lgkmcnt(0)
	v_mfma_scale_f32_16x16x128_f8f6f4 v[94:97], v[2:9], v[18:25], v[94:97], v149, v149 op_sel_hi:[0,0,0]
	v_mfma_scale_f32_16x16x128_f8f6f4 v[90:93], v[10:17], v[18:25], v[90:93], v149, v149 op_sel_hi:[0,0,0]
	v_mfma_scale_f32_16x16x128_f8f6f4 v[86:89], v[2:9], v[160:167], v[86:89], v149, v149 op_sel_hi:[0,0,0]
	v_mfma_scale_f32_16x16x128_f8f6f4 v[82:85], v[10:17], v[160:167], v[82:85], v149, v149 op_sel_hi:[0,0,0]
	v_mfma_scale_f32_16x16x128_f8f6f4 v[78:81], v[2:9], v[168:175], v[78:81], v149, v149 op_sel_hi:[0,0,0]
	v_mfma_scale_f32_16x16x128_f8f6f4 v[74:77], v[10:17], v[168:175], v[74:77], v149, v149 op_sel_hi:[0,0,0]
	v_mfma_scale_f32_16x16x128_f8f6f4 v[62:65], v[2:9], v[176:183], v[212:215], v149, v149 op_sel_hi:[0,0,0]
	v_mfma_scale_f32_16x16x128_f8f6f4 v[58:61], v[10:17], v[176:183], v[216:219], v149, v149 op_sel_hi:[0,0,0]
	v_mfma_scale_f32_16x16x128_f8f6f4 v[30:33], v[130:137], v[18:25], v[220:223], v149, v149 op_sel_hi:[0,0,0]
	v_mfma_scale_f32_16x16x128_f8f6f4 v[26:29], v[152:159], v[18:25], v[224:227], v149, v149 op_sel_hi:[0,0,0]
	v_mfma_scale_f32_16x16x128_f8f6f4 v[22:25], v[130:137], v[160:167], v[228:231], v149, v149 op_sel_hi:[0,0,0]
	v_mfma_scale_f32_16x16x128_f8f6f4 v[18:21], v[152:159], v[160:167], v[232:235], v149, v149 op_sel_hi:[0,0,0]
	v_mfma_scale_f32_16x16x128_f8f6f4 v[14:17], v[130:137], v[168:175], v[236:239], v149, v149 op_sel_hi:[0,0,0]
	v_mfma_scale_f32_16x16x128_f8f6f4 v[10:13], v[152:159], v[168:175], v[240:243], v149, v149 op_sel_hi:[0,0,0]
	v_mfma_scale_f32_16x16x128_f8f6f4 v[6:9], v[130:137], v[176:183], v[244:247], v149, v149 op_sel_hi:[0,0,0]
	v_mfma_scale_f32_16x16x128_f8f6f4 v[2:5], v[152:159], v[176:183], v[248:251], v149, v149 op_sel_hi:[0,0,0]
	s_barrier
	s_add_i32 s64, s64, 2
	s_add_u32 s18, s18, 0x100
	s_addc_u32 s19, s19, 0
	s_add_u32 s62, s62, 0x100
	s_addc_u32 s63, s63, 0
	s_cmp_gt_u32 s64, 13
	s_cbranch_scc0 .LBB5_1678
	s_and_b64 vcc, exec, s[8:9]
	s_cbranch_vccz .LBB5_1681
	s_barrier
